# GEMM epilogues: lane-transposed (ds_bpermute) coalesced stores in INPROJ/OUT/gate; gate bias rows staged in LDS by LDS-DMA (no vmcnt(0) drains), gate sigmoid epilogue rewritten (folded constants, SDWA
# speedup vs baseline: 1.0457x; 1.0368x over previous
; __device__ __forceinline__ unsigned cvt_pk_bf16(float lo, float hi) { f32x2 v = {lo, hi}; bf16x2_t b = __builtin_convertvector(v, bf16x2_t); return __builtin_bit_cast(unsigned, b); }
; __device__ __forceinline__ float shx(float v, int mask, int lane) { return __builtin_bit_cast(float, __builtin_amdgcn_ds_bpermute((lane ^ mask) << 2, __builtin_bit_cast(int, v))); }
;     __device__ __forceinline__ void operator()(const f32x4 (&acc)[2][2][4][2], const g8::Unit& u, int wr, int wc, int fr, int fq) const {
;         const int row0 = u.pm * 256 + wr * 64 + fr;
;         {
;             const int col0 = u.pn * 256 + wc * 32 + 8 * fq;
;             float kq0 = 0.f, kq1 = 0.f;
; #pragma unroll
;             for (int ai = 0; ai < 2; ++ai)
; #pragma unroll
;                 for (int m = 0; m < 4; ++m) { const int row = row0 + ai * 128 + m * 16; bf16_t* rp = H + (size_t)row * HP + col0;
;                     float s0 = 0.f, s1 = 0.f;
; #pragma unroll
;                     for (int bj = 0; bj < 2; ++bj) { const f32x4 v0 = acc[ai][bj][m][0], v1 = acc[ai][bj][m][1];
;                         u32x4 w; w.x = cvt_pk_bf16(v0[0], v0[1]); w.y = cvt_pk_bf16(v0[2], v0[3]); w.z = cvt_pk_bf16(v1[0], v1[1]); w.w = cvt_pk_bf16(v1[2], v1[3]);
;                         *(u32x4*)(rp + bj * 128) = w;
;                         const float q = (v0[0] * v0[0] + v0[1] * v0[1]) + (v0[2] * v0[2] + v0[3] * v0[3]) + (v1[0] * v1[0] + v1[1] * v1[1]) + (v1[2] * v1[2] + v1[3] * v1[3]);
;                         if (bj == 0) s0 = q; else s1 = q; }
;                     if (u.pn == 8 || u.pn == 9) {
;                         const int ln = fq * 16 + fr;
;                         float t0 = s0, t1 = s1; t0 += shx(t0, 16, ln); t0 += shx(t0, 32, ln); t1 += shx(t1, 16, ln); t1 += shx(t1, 32, ln);
;                         kq0 = fmaxf(kq0, t0); kq1 = fmaxf(kq1, t1);
;                     }
;                     if (u.pn < 2) {
;                         float s = (u.pn == 0) ? (s0 + s1) : s0;
;                         { const int ln = fq * 16 + fr; s += shx(s, 16, ln); s += shx(s, 32, ln); }
;                         if (fq == 0) ssq[(size_t)row * 8 + u.pn * 4 + wc] = s;
;                     }
;                 }
.LBB0_370:
	s_mov_b32 s4, -1
	v_readlane_b32 s42, v253, 62
	v_mbcnt_lo_u32_b32 v1, s4, 0
	v_mbcnt_hi_u32_b32 v1, s4, v1
	s_lshl_b32 s4, s62, 8
	s_add_i32 s4, s4, s9
	v_and_or_b32 v144, v1, 15, s4
	v_lshrrev_b32_e32 v229, 2, v1
	v_and_b32_e32 v230, 3, v1
	v_and_b32_e32 v228, 60, v1
	v_or_b32_e32 v229, s4, v229
	v_lshl_or_b32 v228, v230, 6, v228
	s_lshl_b32 s4, s61, 8
	v_lshrrev_b32_e32 v145, 1, v1
	s_or_b32 s4, s4, s42
	v_and_b32_e32 v145, 56, v145
	v_add_u32_e32 v146, s4, v145
	v_lshl_add_u32 v230, v230, 3, s4
	v_mov_b32_e32 v231, 0
	v_mov_b64_e32 v[152:153], s[16:17]
	v_ashrrev_i32_e32 v147, 31, v146
	v_mad_i64_i32 v[152:153], s[42:43], v229, s33, v[152:153]
	v_lshl_add_u64 v[158:159], v[230:231], 1, v[152:153]
	v_cvt_pk_bf16_f32 v152, v128, v129
	v_mul_f32_e32 v129, v129, v129
	v_fmac_f32_e32 v129, v128, v128
	v_mul_f32_e32 v128, v131, v131
	v_cvt_pk_bf16_f32 v154, v124, v125
	v_fmac_f32_e32 v128, v130, v130
	v_mul_f32_e32 v125, v125, v125
	v_add_f32_e32 v128, v129, v128
	v_fmac_f32_e32 v125, v124, v124
	v_add_f32_e32 v124, v125, v128
	v_mul_f32_e32 v125, v127, v127
	v_cvt_pk_bf16_f32 v155, v126, v127
	v_fmac_f32_e32 v125, v126, v126
	v_cvt_pk_bf16_f32 v126, v120, v121
	v_mul_f32_e32 v121, v121, v121
	v_fmac_f32_e32 v121, v120, v120
	v_mul_f32_e32 v120, v123, v123
	v_cvt_pk_bf16_f32 v128, v116, v117
	v_fmac_f32_e32 v120, v122, v122
	v_mul_f32_e32 v117, v117, v117
	v_add_f32_e32 v120, v121, v120
	v_fmac_f32_e32 v117, v116, v116
	s_and_b32 s4, s61, -2
	v_add_f32_e32 v116, v117, v120
	v_mul_f32_e32 v117, v119, v119
	s_cmp_eq_u32 s4, 8
	v_lshlrev_b32_e32 v151, 2, v1
	v_fmac_f32_e32 v117, v118, v118
	s_cselect_b64 s[48:49], -1, 0
	s_cmp_lg_u32 s4, 8
	v_xor_b32_e32 v157, 64, v151
	v_xor_b32_e32 v156, 0x80, v151
	v_cvt_pk_bf16_f32 v153, v130, v131
	v_add_f32_e32 v124, v125, v124
	v_cvt_pk_bf16_f32 v127, v122, v123
	v_cvt_pk_bf16_f32 v129, v118, v119
	v_add_f32_e32 v116, v117, v116
	v_mov_b32_e32 v119, 0
	v_mov_b32_e32 v118, 0
	ds_bpermute_b32 v152, v228, v152
	ds_bpermute_b32 v153, v228, v153
	ds_bpermute_b32 v154, v228, v154
	ds_bpermute_b32 v155, v228, v155
	ds_bpermute_b32 v126, v228, v126
	ds_bpermute_b32 v127, v228, v127
	ds_bpermute_b32 v128, v228, v128
	ds_bpermute_b32 v129, v228, v129
	s_waitcnt lgkmcnt(0)
	global_store_dwordx4 v[158:159], v[152:155], off
	global_store_dwordx4 v[158:159], v[126:129], off offset:256
	s_cbranch_scc1 .LBB0_372
	ds_bpermute_b32 v117, v157, v124
	s_waitcnt lgkmcnt(0)
	v_add_f32_e32 v117, v124, v117
	ds_bpermute_b32 v118, v156, v117
	s_waitcnt lgkmcnt(0)
	v_add_f32_e32 v117, v117, v118
	ds_bpermute_b32 v118, v157, v116
	s_waitcnt lgkmcnt(0)
	v_add_f32_e32 v118, v116, v118
	ds_bpermute_b32 v119, v156, v118
	s_waitcnt lgkmcnt(0)
	v_add_f32_e32 v119, v118, v119
	v_max_f32_e32 v118, 0, v117
	v_max_f32_e32 v119, 0, v119

; __device__ __forceinline__ unsigned cvt_pk_bf16(float lo, float hi) { f32x2 v = {lo, hi}; bf16x2_t b = __builtin_convertvector(v, bf16x2_t); return __builtin_bit_cast(unsigned, b); }
; __device__ __forceinline__ float shx(float v, int mask, int lane) { return __builtin_bit_cast(float, __builtin_amdgcn_ds_bpermute((lane ^ mask) << 2, __builtin_bit_cast(int, v))); }
;     __device__ __forceinline__ void operator()(const f32x4 (&acc)[2][2][4][2], const g8::Unit& u, int wr, int wc, int fr, int fq) const {
;     ...
;                 for (int m = 0; m < 4; ++m) { const int row = row0 + ai * 128 + m * 16; bf16_t* rp = H + (size_t)row * HP + col0;
;                     float s0 = 0.f, s1 = 0.f;
; #pragma unroll
;                     for (int bj = 0; bj < 2; ++bj) { const f32x4 v0 = acc[ai][bj][m][0], v1 = acc[ai][bj][m][1];
;                         u32x4 w; w.x = cvt_pk_bf16(v0[0], v0[1]); w.y = cvt_pk_bf16(v0[2], v0[3]); w.z = cvt_pk_bf16(v1[0], v1[1]); w.w = cvt_pk_bf16(v1[2], v1[3]);
;                         *(u32x4*)(rp + bj * 128) = w;
;                         const float q = (v0[0] * v0[0] + v0[1] * v0[1]) + (v0[2] * v0[2] + v0[3] * v0[3]) + (v1[0] * v1[0] + v1[1] * v1[1]) + (v1[2] * v1[2] + v1[3] * v1[3]);
;                         if (bj == 0) s0 = q; else s1 = q; }
;                     if (u.pn == 8 || u.pn == 9) {
;                         const int ln = fq * 16 + fr;
;                         float t0 = s0, t1 = s1; t0 += shx(t0, 16, ln); t0 += shx(t0, 32, ln); t1 += shx(t1, 16, ln); t1 += shx(t1, 32, ln);
;                         kq0 = fmaxf(kq0, t0); kq1 = fmaxf(kq1, t1);
;                     }
;                     if (u.pn < 2) {
;                         float s = (u.pn == 0) ? (s0 + s1) : s0;
;                         { const int ln = fq * 16 + fr; s += shx(s, 16, ln); s += shx(s, 32, ln); }
;                         if (fq == 0) ssq[(size_t)row * 8 + u.pn * 4 + wc] = s;
;                     }
;                 }
.LBB0_376:
	v_or_b32_e32 v116, 16, v144
	v_mov_b64_e32 v[120:121], s[16:17]
	v_or_b32_e32 v232, 16, v229
	v_mad_i64_i32 v[120:121], s[46:47], v232, s33, v[120:121]
	v_lshl_add_u64 v[124:125], v[230:231], 1, v[120:121]
	v_cvt_pk_bf16_f32 v120, v112, v113
	v_mul_f32_e32 v113, v113, v113
	v_fmac_f32_e32 v113, v112, v112
	v_mul_f32_e32 v112, v115, v115
	v_cvt_pk_bf16_f32 v122, v108, v109
	v_fmac_f32_e32 v112, v114, v114
	v_mul_f32_e32 v109, v109, v109
	v_add_f32_e32 v112, v113, v112
	v_fmac_f32_e32 v109, v108, v108
	v_add_f32_e32 v108, v109, v112
	v_mul_f32_e32 v109, v111, v111
	v_cvt_pk_bf16_f32 v123, v110, v111
	v_fmac_f32_e32 v109, v110, v110
	v_cvt_pk_bf16_f32 v110, v104, v105
	v_mul_f32_e32 v105, v105, v105
	v_fmac_f32_e32 v105, v104, v104
	v_mul_f32_e32 v104, v107, v107
	v_cvt_pk_bf16_f32 v112, v100, v101
	v_fmac_f32_e32 v104, v106, v106
	v_mul_f32_e32 v101, v101, v101
	v_add_f32_e32 v104, v105, v104
	v_fmac_f32_e32 v101, v100, v100
	v_add_f32_e32 v100, v101, v104
	v_mul_f32_e32 v101, v103, v103
	v_cvt_pk_bf16_f32 v113, v102, v103
	v_fmac_f32_e32 v101, v102, v102
	v_cndmask_b32_e64 v102, 0, 1, s[48:49]
	v_cvt_pk_bf16_f32 v121, v114, v115
	v_add_f32_e32 v108, v109, v108
	v_cvt_pk_bf16_f32 v111, v106, v107
	v_cmp_ne_u32_e64 s[46:47], 1, v102
	s_andn2_b64 vcc, exec, s[48:49]
	v_add_f32_e32 v100, v101, v100
	ds_bpermute_b32 v120, v228, v120
	ds_bpermute_b32 v121, v228, v121
	ds_bpermute_b32 v122, v228, v122
	ds_bpermute_b32 v123, v228, v123
	ds_bpermute_b32 v110, v228, v110
	ds_bpermute_b32 v111, v228, v111
	ds_bpermute_b32 v112, v228, v112
	ds_bpermute_b32 v113, v228, v113
	s_waitcnt lgkmcnt(0)
	global_store_dwordx4 v[124:125], v[120:123], off
	global_store_dwordx4 v[124:125], v[110:113], off offset:256
	s_cbranch_vccnz .LBB0_378
	ds_bpermute_b32 v101, v157, v108
	s_waitcnt lgkmcnt(0)
	v_add_f32_e32 v101, v108, v101
	ds_bpermute_b32 v102, v156, v101
	s_waitcnt lgkmcnt(0)
	v_add_f32_e32 v101, v101, v102
	ds_bpermute_b32 v102, v157, v100
	s_waitcnt lgkmcnt(0)
	v_add_f32_e32 v102, v100, v102
	ds_bpermute_b32 v103, v156, v102
	s_waitcnt lgkmcnt(0)
	v_add_f32_e32 v102, v102, v103
	v_max_f32_e32 v103, v118, v118
	v_max_f32_e32 v118, v103, v101
	v_max_f32_e32 v101, v119, v119
	v_max_f32_e32 v119, v101, v102

; __device__ __forceinline__ unsigned cvt_pk_bf16(float lo, float hi) { f32x2 v = {lo, hi}; bf16x2_t b = __builtin_convertvector(v, bf16x2_t); return __builtin_bit_cast(unsigned, b); }
; __device__ __forceinline__ float shx(float v, int mask, int lane) { return __builtin_bit_cast(float, __builtin_amdgcn_ds_bpermute((lane ^ mask) << 2, __builtin_bit_cast(int, v))); }
;     __device__ __forceinline__ void operator()(const f32x4 (&acc)[2][2][4][2], const g8::Unit& u, int wr, int wc, int fr, int fq) const {
;     ...
;                 for (int m = 0; m < 4; ++m) { const int row = row0 + ai * 128 + m * 16; bf16_t* rp = H + (size_t)row * HP + col0;
;                     float s0 = 0.f, s1 = 0.f;
; #pragma unroll
;                     for (int bj = 0; bj < 2; ++bj) { const f32x4 v0 = acc[ai][bj][m][0], v1 = acc[ai][bj][m][1];
;                         u32x4 w; w.x = cvt_pk_bf16(v0[0], v0[1]); w.y = cvt_pk_bf16(v0[2], v0[3]); w.z = cvt_pk_bf16(v1[0], v1[1]); w.w = cvt_pk_bf16(v1[2], v1[3]);
;                         *(u32x4*)(rp + bj * 128) = w;
;                         const float q = (v0[0] * v0[0] + v0[1] * v0[1]) + (v0[2] * v0[2] + v0[3] * v0[3]) + (v1[0] * v1[0] + v1[1] * v1[1]) + (v1[2] * v1[2] + v1[3] * v1[3]);
;                         if (bj == 0) s0 = q; else s1 = q; }
;                     if (u.pn == 8 || u.pn == 9) {
;                         const int ln = fq * 16 + fr;
;                         float t0 = s0, t1 = s1; t0 += shx(t0, 16, ln); t0 += shx(t0, 32, ln); t1 += shx(t1, 16, ln); t1 += shx(t1, 32, ln);
;                         kq0 = fmaxf(kq0, t0); kq1 = fmaxf(kq1, t1);
;                     }
;                     if (u.pn < 2) {
;                         float s = (u.pn == 0) ? (s0 + s1) : s0;
;                         { const int ln = fq * 16 + fr; s += shx(s, 16, ln); s += shx(s, 32, ln); }
;                         if (fq == 0) ssq[(size_t)row * 8 + u.pn * 4 + wc] = s;
;                     }
;                 }
.LBB0_382:
	v_or_b32_e32 v100, 32, v144
	v_mov_b64_e32 v[102:103], s[16:17]
	v_or_b32_e32 v232, 32, v229
	v_mad_i64_i32 v[102:103], s[56:57], v232, s33, v[102:103]
	v_lshl_add_u64 v[106:107], v[230:231], 1, v[102:103]
	v_cvt_pk_bf16_f32 v102, v96, v97
	v_mul_f32_e32 v97, v97, v97
	v_fmac_f32_e32 v97, v96, v96
	v_mul_f32_e32 v96, v99, v99
	v_cvt_pk_bf16_f32 v104, v92, v93
	v_fmac_f32_e32 v96, v98, v98
	v_mul_f32_e32 v93, v93, v93
	v_add_f32_e32 v96, v97, v96
	v_fmac_f32_e32 v93, v92, v92
	v_add_f32_e32 v92, v93, v96
	v_mul_f32_e32 v93, v95, v95
	v_cvt_pk_bf16_f32 v105, v94, v95
	v_fmac_f32_e32 v93, v94, v94
	v_cvt_pk_bf16_f32 v94, v88, v89
	v_mul_f32_e32 v89, v89, v89
	v_fmac_f32_e32 v89, v88, v88
	v_mul_f32_e32 v88, v91, v91
	v_cvt_pk_bf16_f32 v96, v84, v85
	v_fmac_f32_e32 v88, v90, v90
	v_mul_f32_e32 v85, v85, v85
	v_add_f32_e32 v88, v89, v88
	v_fmac_f32_e32 v85, v84, v84
	v_add_f32_e32 v84, v85, v88
	v_mul_f32_e32 v85, v87, v87
	v_fmac_f32_e32 v85, v86, v86
	v_cvt_pk_bf16_f32 v103, v98, v99
	v_add_f32_e32 v92, v93, v92
	v_cvt_pk_bf16_f32 v95, v90, v91
	v_cvt_pk_bf16_f32 v97, v86, v87
	s_and_b64 vcc, exec, s[46:47]
	v_add_f32_e32 v84, v85, v84
	ds_bpermute_b32 v102, v228, v102
	ds_bpermute_b32 v103, v228, v103
	ds_bpermute_b32 v104, v228, v104
	ds_bpermute_b32 v105, v228, v105
	ds_bpermute_b32 v94, v228, v94
	ds_bpermute_b32 v95, v228, v95
	ds_bpermute_b32 v96, v228, v96
	ds_bpermute_b32 v97, v228, v97
	s_waitcnt lgkmcnt(0)
	global_store_dwordx4 v[106:107], v[102:105], off
	global_store_dwordx4 v[106:107], v[94:97], off offset:256
	s_cbranch_vccnz .LBB0_384
	ds_bpermute_b32 v85, v157, v92
	s_waitcnt lgkmcnt(0)
	v_add_f32_e32 v85, v92, v85
	ds_bpermute_b32 v86, v156, v85
	s_waitcnt lgkmcnt(0)
	v_add_f32_e32 v85, v85, v86
	ds_bpermute_b32 v86, v157, v84
	s_waitcnt lgkmcnt(0)
	v_add_f32_e32 v86, v84, v86
	ds_bpermute_b32 v87, v156, v86
	s_waitcnt lgkmcnt(0)
	v_add_f32_e32 v86, v86, v87
	v_max_f32_e32 v87, v118, v118
	v_max_f32_e32 v118, v87, v85
	v_max_f32_e32 v85, v119, v119
	v_max_f32_e32 v119, v85, v86

; __device__ __forceinline__ unsigned cvt_pk_bf16(float lo, float hi) { f32x2 v = {lo, hi}; bf16x2_t b = __builtin_convertvector(v, bf16x2_t); return __builtin_bit_cast(unsigned, b); }
; __device__ __forceinline__ float shx(float v, int mask, int lane) { return __builtin_bit_cast(float, __builtin_amdgcn_ds_bpermute((lane ^ mask) << 2, __builtin_bit_cast(int, v))); }
;     __device__ __forceinline__ void operator()(const f32x4 (&acc)[2][2][4][2], const g8::Unit& u, int wr, int wc, int fr, int fq) const {
;     ...
;                 for (int m = 0; m < 4; ++m) { const int row = row0 + ai * 128 + m * 16; bf16_t* rp = H + (size_t)row * HP + col0;
;                     float s0 = 0.f, s1 = 0.f;
; #pragma unroll
;                     for (int bj = 0; bj < 2; ++bj) { const f32x4 v0 = acc[ai][bj][m][0], v1 = acc[ai][bj][m][1];
;                         u32x4 w; w.x = cvt_pk_bf16(v0[0], v0[1]); w.y = cvt_pk_bf16(v0[2], v0[3]); w.z = cvt_pk_bf16(v1[0], v1[1]); w.w = cvt_pk_bf16(v1[2], v1[3]);
;                         *(u32x4*)(rp + bj * 128) = w;
;                         const float q = (v0[0] * v0[0] + v0[1] * v0[1]) + (v0[2] * v0[2] + v0[3] * v0[3]) + (v1[0] * v1[0] + v1[1] * v1[1]) + (v1[2] * v1[2] + v1[3] * v1[3]);
;                         if (bj == 0) s0 = q; else s1 = q; }
;                     if (u.pn == 8 || u.pn == 9) {
;                         const int ln = fq * 16 + fr;
;                         float t0 = s0, t1 = s1; t0 += shx(t0, 16, ln); t0 += shx(t0, 32, ln); t1 += shx(t1, 16, ln); t1 += shx(t1, 32, ln);
;                         kq0 = fmaxf(kq0, t0); kq1 = fmaxf(kq1, t1);
;                     }
;                     if (u.pn < 2) {
;                         float s = (u.pn == 0) ? (s0 + s1) : s0;
;                         { const int ln = fq * 16 + fr; s += shx(s, 16, ln); s += shx(s, 32, ln); }
;                         if (fq == 0) ssq[(size_t)row * 8 + u.pn * 4 + wc] = s;
;                     }
;                 }
.LBB0_388:
	v_or_b32_e32 v84, 48, v144
	v_mov_b64_e32 v[86:87], s[16:17]
	v_or_b32_e32 v232, 48, v229
	v_mad_i64_i32 v[86:87], s[56:57], v232, s33, v[86:87]
	v_lshl_add_u64 v[90:91], v[230:231], 1, v[86:87]
	v_cvt_pk_bf16_f32 v86, v80, v81
	v_mul_f32_e32 v81, v81, v81
	v_fmac_f32_e32 v81, v80, v80
	v_mul_f32_e32 v80, v83, v83
	v_cvt_pk_bf16_f32 v88, v76, v77
	v_fmac_f32_e32 v80, v82, v82
	v_mul_f32_e32 v77, v77, v77
	v_add_f32_e32 v80, v81, v80
	v_fmac_f32_e32 v77, v76, v76
	v_add_f32_e32 v76, v77, v80
	v_mul_f32_e32 v77, v79, v79
	v_cvt_pk_bf16_f32 v89, v78, v79
	v_fmac_f32_e32 v77, v78, v78
	v_cvt_pk_bf16_f32 v78, v72, v73
	v_mul_f32_e32 v73, v73, v73
	v_fmac_f32_e32 v73, v72, v72
	v_mul_f32_e32 v72, v75, v75
	v_cvt_pk_bf16_f32 v80, v68, v69
	v_fmac_f32_e32 v72, v74, v74
	v_mul_f32_e32 v69, v69, v69
	v_add_f32_e32 v72, v73, v72
	v_fmac_f32_e32 v69, v68, v68
	v_add_f32_e32 v68, v69, v72
	v_mul_f32_e32 v69, v71, v71
	v_fmac_f32_e32 v69, v70, v70
	v_cvt_pk_bf16_f32 v87, v82, v83
	v_add_f32_e32 v76, v77, v76
	v_cvt_pk_bf16_f32 v79, v74, v75
	v_cvt_pk_bf16_f32 v81, v70, v71
	s_and_b64 vcc, exec, s[46:47]
	v_add_f32_e32 v68, v69, v68
	ds_bpermute_b32 v86, v228, v86
	ds_bpermute_b32 v87, v228, v87
	ds_bpermute_b32 v88, v228, v88
	ds_bpermute_b32 v89, v228, v89
	ds_bpermute_b32 v78, v228, v78
	ds_bpermute_b32 v79, v228, v79
	ds_bpermute_b32 v80, v228, v80
	ds_bpermute_b32 v81, v228, v81
	s_waitcnt lgkmcnt(0)
	global_store_dwordx4 v[90:91], v[86:89], off
	global_store_dwordx4 v[90:91], v[78:81], off offset:256
	s_cbranch_vccnz .LBB0_390
	ds_bpermute_b32 v69, v157, v76
	s_waitcnt lgkmcnt(0)
	v_add_f32_e32 v69, v76, v69
	ds_bpermute_b32 v70, v156, v69
	s_waitcnt lgkmcnt(0)
	v_add_f32_e32 v69, v69, v70
	ds_bpermute_b32 v70, v157, v68
	s_waitcnt lgkmcnt(0)
	v_add_f32_e32 v70, v68, v70
	ds_bpermute_b32 v71, v156, v70
	s_waitcnt lgkmcnt(0)
	v_add_f32_e32 v70, v70, v71
	v_max_f32_e32 v71, v118, v118
	v_max_f32_e32 v118, v71, v69
	v_max_f32_e32 v69, v119, v119
	v_max_f32_e32 v119, v69, v70

; __device__ __forceinline__ unsigned cvt_pk_bf16(float lo, float hi) { f32x2 v = {lo, hi}; bf16x2_t b = __builtin_convertvector(v, bf16x2_t); return __builtin_bit_cast(unsigned, b); }
; __device__ __forceinline__ float shx(float v, int mask, int lane) { return __builtin_bit_cast(float, __builtin_amdgcn_ds_bpermute((lane ^ mask) << 2, __builtin_bit_cast(int, v))); }
;     __device__ __forceinline__ void operator()(const f32x4 (&acc)[2][2][4][2], const g8::Unit& u, int wr, int wc, int fr, int fq) const {
;     ...
;                 for (int m = 0; m < 4; ++m) { const int row = row0 + ai * 128 + m * 16; bf16_t* rp = H + (size_t)row * HP + col0;
;                     float s0 = 0.f, s1 = 0.f;
; #pragma unroll
;                     for (int bj = 0; bj < 2; ++bj) { const f32x4 v0 = acc[ai][bj][m][0], v1 = acc[ai][bj][m][1];
;                         u32x4 w; w.x = cvt_pk_bf16(v0[0], v0[1]); w.y = cvt_pk_bf16(v0[2], v0[3]); w.z = cvt_pk_bf16(v1[0], v1[1]); w.w = cvt_pk_bf16(v1[2], v1[3]);
;                         *(u32x4*)(rp + bj * 128) = w;
;                         const float q = (v0[0] * v0[0] + v0[1] * v0[1]) + (v0[2] * v0[2] + v0[3] * v0[3]) + (v1[0] * v1[0] + v1[1] * v1[1]) + (v1[2] * v1[2] + v1[3] * v1[3]);
;                         if (bj == 0) s0 = q; else s1 = q; }
;                     if (u.pn == 8 || u.pn == 9) {
;                         const int ln = fq * 16 + fr;
;                         float t0 = s0, t1 = s1; t0 += shx(t0, 16, ln); t0 += shx(t0, 32, ln); t1 += shx(t1, 16, ln); t1 += shx(t1, 32, ln);
;                         kq0 = fmaxf(kq0, t0); kq1 = fmaxf(kq1, t1);
;                     }
;                     if (u.pn < 2) {
;                         float s = (u.pn == 0) ? (s0 + s1) : s0;
;                         { const int ln = fq * 16 + fr; s += shx(s, 16, ln); s += shx(s, 32, ln); }
;                         if (fq == 0) ssq[(size_t)row * 8 + u.pn * 4 + wc] = s;
;                     }
;                 }
.LBB0_394:
	v_add_u32_e32 v68, 0x80, v144
	v_mov_b64_e32 v[70:71], s[16:17]
	v_add_u32_e32 v232, 0x80, v229
	v_mad_i64_i32 v[70:71], s[56:57], v232, s33, v[70:71]
	v_lshl_add_u64 v[74:75], v[230:231], 1, v[70:71]
	v_cvt_pk_bf16_f32 v70, v64, v65
	v_mul_f32_e32 v65, v65, v65
	v_fmac_f32_e32 v65, v64, v64
	v_mul_f32_e32 v64, v67, v67
	v_cvt_pk_bf16_f32 v72, v60, v61
	v_fmac_f32_e32 v64, v66, v66
	v_mul_f32_e32 v61, v61, v61
	v_add_f32_e32 v64, v65, v64
	v_fmac_f32_e32 v61, v60, v60
	v_add_f32_e32 v60, v61, v64
	v_mul_f32_e32 v61, v63, v63
	v_cvt_pk_bf16_f32 v73, v62, v63
	v_fmac_f32_e32 v61, v62, v62
	v_cvt_pk_bf16_f32 v62, v56, v57
	v_mul_f32_e32 v57, v57, v57
	v_fmac_f32_e32 v57, v56, v56
	v_mul_f32_e32 v56, v59, v59
	v_cvt_pk_bf16_f32 v64, v52, v53
	v_fmac_f32_e32 v56, v58, v58
	v_mul_f32_e32 v53, v53, v53
	v_add_f32_e32 v56, v57, v56
	v_fmac_f32_e32 v53, v52, v52
	v_add_f32_e32 v52, v53, v56
	v_mul_f32_e32 v53, v55, v55
	v_fmac_f32_e32 v53, v54, v54
	v_cvt_pk_bf16_f32 v71, v66, v67
	v_add_f32_e32 v60, v61, v60
	v_cvt_pk_bf16_f32 v63, v58, v59
	v_cvt_pk_bf16_f32 v65, v54, v55
	s_and_b64 vcc, exec, s[46:47]
	v_add_f32_e32 v52, v53, v52
	ds_bpermute_b32 v70, v228, v70
	ds_bpermute_b32 v71, v228, v71
	ds_bpermute_b32 v72, v228, v72
	ds_bpermute_b32 v73, v228, v73
	ds_bpermute_b32 v62, v228, v62
	ds_bpermute_b32 v63, v228, v63
	ds_bpermute_b32 v64, v228, v64
	ds_bpermute_b32 v65, v228, v65
	s_waitcnt lgkmcnt(0)
	global_store_dwordx4 v[74:75], v[70:73], off
	global_store_dwordx4 v[74:75], v[62:65], off offset:256
	s_cbranch_vccnz .LBB0_396
	ds_bpermute_b32 v53, v157, v60
	s_waitcnt lgkmcnt(0)
	v_add_f32_e32 v53, v60, v53
	ds_bpermute_b32 v54, v156, v53
	s_waitcnt lgkmcnt(0)
	v_add_f32_e32 v53, v53, v54
	ds_bpermute_b32 v54, v157, v52
	s_waitcnt lgkmcnt(0)
	v_add_f32_e32 v54, v52, v54
	ds_bpermute_b32 v55, v156, v54
	s_waitcnt lgkmcnt(0)
	v_add_f32_e32 v54, v54, v55
	v_max_f32_e32 v55, v118, v118
	v_max_f32_e32 v118, v55, v53
	v_max_f32_e32 v53, v119, v119
	v_max_f32_e32 v119, v53, v54

; __device__ __forceinline__ unsigned cvt_pk_bf16(float lo, float hi) { f32x2 v = {lo, hi}; bf16x2_t b = __builtin_convertvector(v, bf16x2_t); return __builtin_bit_cast(unsigned, b); }
; __device__ __forceinline__ float shx(float v, int mask, int lane) { return __builtin_bit_cast(float, __builtin_amdgcn_ds_bpermute((lane ^ mask) << 2, __builtin_bit_cast(int, v))); }
;     __device__ __forceinline__ void operator()(const f32x4 (&acc)[2][2][4][2], const g8::Unit& u, int wr, int wc, int fr, int fq) const {
;     ...
;                 for (int m = 0; m < 4; ++m) { const int row = row0 + ai * 128 + m * 16; bf16_t* rp = H + (size_t)row * HP + col0;
;                     float s0 = 0.f, s1 = 0.f;
; #pragma unroll
;                     for (int bj = 0; bj < 2; ++bj) { const f32x4 v0 = acc[ai][bj][m][0], v1 = acc[ai][bj][m][1];
;                         u32x4 w; w.x = cvt_pk_bf16(v0[0], v0[1]); w.y = cvt_pk_bf16(v0[2], v0[3]); w.z = cvt_pk_bf16(v1[0], v1[1]); w.w = cvt_pk_bf16(v1[2], v1[3]);
;                         *(u32x4*)(rp + bj * 128) = w;
;                         const float q = (v0[0] * v0[0] + v0[1] * v0[1]) + (v0[2] * v0[2] + v0[3] * v0[3]) + (v1[0] * v1[0] + v1[1] * v1[1]) + (v1[2] * v1[2] + v1[3] * v1[3]);
;                         if (bj == 0) s0 = q; else s1 = q; }
;                     if (u.pn == 8 || u.pn == 9) {
;                         const int ln = fq * 16 + fr;
;                         float t0 = s0, t1 = s1; t0 += shx(t0, 16, ln); t0 += shx(t0, 32, ln); t1 += shx(t1, 16, ln); t1 += shx(t1, 32, ln);
;                         kq0 = fmaxf(kq0, t0); kq1 = fmaxf(kq1, t1);
;                     }
;                     if (u.pn < 2) {
;                         float s = (u.pn == 0) ? (s0 + s1) : s0;
;                         { const int ln = fq * 16 + fr; s += shx(s, 16, ln); s += shx(s, 32, ln); }
;                         if (fq == 0) ssq[(size_t)row * 8 + u.pn * 4 + wc] = s;
;                     }
;                 }
.LBB0_400:
	v_add_u32_e32 v52, 0x90, v144
	v_mov_b64_e32 v[54:55], s[16:17]
	v_add_u32_e32 v232, 0x90, v229
	v_mad_i64_i32 v[54:55], s[56:57], v232, s33, v[54:55]
	v_lshl_add_u64 v[58:59], v[230:231], 1, v[54:55]
	v_cvt_pk_bf16_f32 v54, v48, v49
	v_mul_f32_e32 v49, v49, v49
	v_fmac_f32_e32 v49, v48, v48
	v_mul_f32_e32 v48, v51, v51
	v_cvt_pk_bf16_f32 v56, v44, v45
	v_fmac_f32_e32 v48, v50, v50
	v_mul_f32_e32 v45, v45, v45
	v_add_f32_e32 v48, v49, v48
	v_fmac_f32_e32 v45, v44, v44
	v_add_f32_e32 v44, v45, v48
	v_mul_f32_e32 v45, v47, v47
	v_cvt_pk_bf16_f32 v57, v46, v47
	v_fmac_f32_e32 v45, v46, v46
	v_cvt_pk_bf16_f32 v46, v40, v41
	v_mul_f32_e32 v41, v41, v41
	v_fmac_f32_e32 v41, v40, v40
	v_mul_f32_e32 v40, v43, v43
	v_cvt_pk_bf16_f32 v48, v36, v37
	v_fmac_f32_e32 v40, v42, v42
	v_mul_f32_e32 v37, v37, v37
	v_add_f32_e32 v40, v41, v40
	v_fmac_f32_e32 v37, v36, v36
	v_add_f32_e32 v36, v37, v40
	v_mul_f32_e32 v37, v39, v39
	v_fmac_f32_e32 v37, v38, v38
	v_cvt_pk_bf16_f32 v55, v50, v51
	v_add_f32_e32 v44, v45, v44
	v_cvt_pk_bf16_f32 v47, v42, v43
	v_cvt_pk_bf16_f32 v49, v38, v39
	s_and_b64 vcc, exec, s[46:47]
	v_add_f32_e32 v36, v37, v36
	ds_bpermute_b32 v54, v228, v54
	ds_bpermute_b32 v55, v228, v55
	ds_bpermute_b32 v56, v228, v56
	ds_bpermute_b32 v57, v228, v57
	ds_bpermute_b32 v46, v228, v46
	ds_bpermute_b32 v47, v228, v47
	ds_bpermute_b32 v48, v228, v48
	ds_bpermute_b32 v49, v228, v49
	s_waitcnt lgkmcnt(0)
	global_store_dwordx4 v[58:59], v[54:57], off
	global_store_dwordx4 v[58:59], v[46:49], off offset:256
	s_cbranch_vccnz .LBB0_402
	ds_bpermute_b32 v37, v157, v44
	s_waitcnt lgkmcnt(0)
	v_add_f32_e32 v37, v44, v37
	ds_bpermute_b32 v38, v156, v37
	s_waitcnt lgkmcnt(0)
	v_add_f32_e32 v37, v37, v38
	ds_bpermute_b32 v38, v157, v36
	s_waitcnt lgkmcnt(0)
	v_add_f32_e32 v38, v36, v38
	ds_bpermute_b32 v39, v156, v38
	s_waitcnt lgkmcnt(0)
	v_add_f32_e32 v38, v38, v39
	v_max_f32_e32 v39, v118, v118
	v_max_f32_e32 v118, v39, v37
	v_max_f32_e32 v37, v119, v119
	v_max_f32_e32 v119, v37, v38

; __device__ __forceinline__ unsigned cvt_pk_bf16(float lo, float hi) { f32x2 v = {lo, hi}; bf16x2_t b = __builtin_convertvector(v, bf16x2_t); return __builtin_bit_cast(unsigned, b); }
; __device__ __forceinline__ float shx(float v, int mask, int lane) { return __builtin_bit_cast(float, __builtin_amdgcn_ds_bpermute((lane ^ mask) << 2, __builtin_bit_cast(int, v))); }
;     __device__ __forceinline__ void operator()(const f32x4 (&acc)[2][2][4][2], const g8::Unit& u, int wr, int wc, int fr, int fq) const {
;     ...
;                 for (int m = 0; m < 4; ++m) { const int row = row0 + ai * 128 + m * 16; bf16_t* rp = H + (size_t)row * HP + col0;
;                     float s0 = 0.f, s1 = 0.f;
; #pragma unroll
;                     for (int bj = 0; bj < 2; ++bj) { const f32x4 v0 = acc[ai][bj][m][0], v1 = acc[ai][bj][m][1];
;                         u32x4 w; w.x = cvt_pk_bf16(v0[0], v0[1]); w.y = cvt_pk_bf16(v0[2], v0[3]); w.z = cvt_pk_bf16(v1[0], v1[1]); w.w = cvt_pk_bf16(v1[2], v1[3]);
;                         *(u32x4*)(rp + bj * 128) = w;
;                         const float q = (v0[0] * v0[0] + v0[1] * v0[1]) + (v0[2] * v0[2] + v0[3] * v0[3]) + (v1[0] * v1[0] + v1[1] * v1[1]) + (v1[2] * v1[2] + v1[3] * v1[3]);
;                         if (bj == 0) s0 = q; else s1 = q; }
;                     if (u.pn == 8 || u.pn == 9) {
;                         const int ln = fq * 16 + fr;
;                         float t0 = s0, t1 = s1; t0 += shx(t0, 16, ln); t0 += shx(t0, 32, ln); t1 += shx(t1, 16, ln); t1 += shx(t1, 32, ln);
;                         kq0 = fmaxf(kq0, t0); kq1 = fmaxf(kq1, t1);
;                     }
;                     if (u.pn < 2) {
;                         float s = (u.pn == 0) ? (s0 + s1) : s0;
;                         { const int ln = fq * 16 + fr; s += shx(s, 16, ln); s += shx(s, 32, ln); }
;                         if (fq == 0) ssq[(size_t)row * 8 + u.pn * 4 + wc] = s;
;                     }
;                 }
.LBB0_406:
	v_add_u32_e32 v36, 0xa0, v144
	v_mov_b64_e32 v[38:39], s[16:17]
	v_add_u32_e32 v232, 0xa0, v229
	v_mad_i64_i32 v[38:39], s[56:57], v232, s33, v[38:39]
	v_lshl_add_u64 v[42:43], v[230:231], 1, v[38:39]
	v_cvt_pk_bf16_f32 v38, v32, v33
	v_mul_f32_e32 v33, v33, v33
	v_fmac_f32_e32 v33, v32, v32
	v_mul_f32_e32 v32, v35, v35
	v_cvt_pk_bf16_f32 v40, v26, v27
	v_fmac_f32_e32 v32, v34, v34
	v_mul_f32_e32 v27, v27, v27
	v_add_f32_e32 v32, v33, v32
	v_fmac_f32_e32 v27, v26, v26
	v_add_f32_e32 v26, v27, v32
	v_cvt_pk_bf16_f32 v32, v22, v23
	v_mul_f32_e32 v23, v23, v23
	v_fmac_f32_e32 v23, v22, v22
	v_mul_f32_e32 v22, v25, v25
	v_cvt_pk_bf16_f32 v39, v34, v35
	v_cvt_pk_bf16_f32 v34, v18, v19
	v_fmac_f32_e32 v22, v24, v24
	v_mul_f32_e32 v19, v19, v19
	v_add_f32_e32 v22, v23, v22
	v_fmac_f32_e32 v19, v18, v18
	v_mul_f32_e32 v27, v29, v29
	v_add_f32_e32 v18, v19, v22
	v_mul_f32_e32 v19, v21, v21
	v_fmac_f32_e32 v27, v28, v28
	v_fmac_f32_e32 v19, v20, v20
	v_cvt_pk_bf16_f32 v41, v28, v29
	v_add_f32_e32 v26, v27, v26
	v_cvt_pk_bf16_f32 v33, v24, v25
	v_cvt_pk_bf16_f32 v35, v20, v21
	s_and_b64 vcc, exec, s[46:47]
	v_add_f32_e32 v18, v19, v18
	ds_bpermute_b32 v38, v228, v38
	ds_bpermute_b32 v39, v228, v39
	ds_bpermute_b32 v40, v228, v40
	ds_bpermute_b32 v41, v228, v41
	ds_bpermute_b32 v32, v228, v32
	ds_bpermute_b32 v33, v228, v33
	ds_bpermute_b32 v34, v228, v34
	ds_bpermute_b32 v35, v228, v35
	s_waitcnt lgkmcnt(0)
	global_store_dwordx4 v[42:43], v[38:41], off
	global_store_dwordx4 v[42:43], v[32:35], off offset:256
	s_cbranch_vccnz .LBB0_408
	ds_bpermute_b32 v19, v157, v26
	s_waitcnt lgkmcnt(0)
	v_add_f32_e32 v19, v26, v19
	ds_bpermute_b32 v20, v156, v19
	s_waitcnt lgkmcnt(0)
	v_add_f32_e32 v19, v19, v20
	ds_bpermute_b32 v20, v157, v18
	s_waitcnt lgkmcnt(0)
	v_add_f32_e32 v20, v18, v20
	ds_bpermute_b32 v21, v156, v20
	s_waitcnt lgkmcnt(0)
	v_add_f32_e32 v20, v20, v21
	v_max_f32_e32 v21, v118, v118
	v_max_f32_e32 v118, v21, v19
	v_max_f32_e32 v19, v119, v119
	v_max_f32_e32 v119, v19, v20

; __device__ __forceinline__ unsigned cvt_pk_bf16(float lo, float hi) { f32x2 v = {lo, hi}; bf16x2_t b = __builtin_convertvector(v, bf16x2_t); return __builtin_bit_cast(unsigned, b); }
;     __device__ __forceinline__ void operator()(const f32x4 (&acc)[2][2][4][2], const g8::Unit& u, int wr, int wc, int fr, int fq) const {
;     ...
;                 for (int m = 0; m < 4; ++m) { const int row = row0 + ai * 128 + m * 16; bf16_t* rp = H + (size_t)row * HP + col0;
;                     float s0 = 0.f, s1 = 0.f;
; #pragma unroll
;                     for (int bj = 0; bj < 2; ++bj) { const f32x4 v0 = acc[ai][bj][m][0], v1 = acc[ai][bj][m][1];
;                         u32x4 w; w.x = cvt_pk_bf16(v0[0], v0[1]); w.y = cvt_pk_bf16(v0[2], v0[3]); w.z = cvt_pk_bf16(v1[0], v1[1]); w.w = cvt_pk_bf16(v1[2], v1[3]);
;                         *(u32x4*)(rp + bj * 128) = w;
;                         const float q = (v0[0] * v0[0] + v0[1] * v0[1]) + (v0[2] * v0[2] + v0[3] * v0[3]) + (v1[0] * v1[0] + v1[1] * v1[1]) + (v1[2] * v1[2] + v1[3] * v1[3]);
;                         if (bj == 0) s0 = q; else s1 = q; }
;                     if (u.pn == 8 || u.pn == 9) {
;                         const int ln = fq * 16 + fr;
;                         float t0 = s0, t1 = s1; t0 += shx(t0, 16, ln); t0 += shx(t0, 32, ln); t1 += shx(t1, 16, ln); t1 += shx(t1, 32, ln);
;                         kq0 = fmaxf(kq0, t0); kq1 = fmaxf(kq1, t1);
;                     }
;                     if (u.pn < 2) {
;                         float s = (u.pn == 0) ? (s0 + s1) : s0;
;                         { const int ln = fq * 16 + fr; s += shx(s, 16, ln); s += shx(s, 32, ln); }
;                         if (fq == 0) ssq[(size_t)row * 8 + u.pn * 4 + wc] = s;
;                     }
;                 }
;             if (u.pn == 8 || u.pn == 9) {
;                 const int ln = fq * 16 + fr;
; #pragma unroll
;                 for (int o = 1; o < 16; o <<= 1) { kq0 = fmaxf(kq0, shx(kq0, o, ln)); kq1 = fmaxf(kq1, shx(kq1, o, ln)); }
;                 const int g0 = (u.pn == 8) ? -100 : 3 + wc, g1 = (u.pn == 8) ? wc - 1 : (wc == 0 ? 7 : -100);
;                 unsigned* km = kmax + (u.pm >> 5) * 8;
;                 if (ln == 0) { if (g0 >= 0) atomicMax(km + g0, __float_as_uint(kq0)); if (g1 >= 0) atomicMax(km + g1, __float_as_uint(kq1)); }
;             }
.LBB0_412:
	v_add_u32_e32 v18, 0xb0, v144
	v_mov_b64_e32 v[20:21], s[16:17]
	v_add_u32_e32 v232, 0xb0, v229
	v_mad_i64_i32 v[20:21], s[56:57], v232, s33, v[20:21]
	v_lshl_add_u64 v[24:25], v[230:231], 1, v[20:21]
	v_cvt_pk_bf16_f32 v20, v14, v15
	v_mul_f32_e32 v15, v15, v15
	v_fmac_f32_e32 v15, v14, v14
	v_mul_f32_e32 v14, v17, v17
	v_cvt_pk_bf16_f32 v22, v10, v11
	v_fmac_f32_e32 v14, v16, v16
	v_mul_f32_e32 v11, v11, v11
	v_add_f32_e32 v14, v15, v14
	v_fmac_f32_e32 v11, v10, v10
	v_add_f32_e32 v10, v11, v14
	v_mul_f32_e32 v11, v13, v13
	v_cvt_pk_bf16_f32 v23, v12, v13
	v_fmac_f32_e32 v11, v12, v12
	v_cvt_pk_bf16_f32 v12, v6, v7
	v_mul_f32_e32 v7, v7, v7
	v_fmac_f32_e32 v7, v6, v6
	v_mul_f32_e32 v6, v9, v9
	v_cvt_pk_bf16_f32 v14, v2, v3
	v_fmac_f32_e32 v6, v8, v8
	v_mul_f32_e32 v3, v3, v3
	v_add_f32_e32 v6, v7, v6
	v_fmac_f32_e32 v3, v2, v2
	v_add_f32_e32 v2, v3, v6
	v_mul_f32_e32 v3, v5, v5
	v_fmac_f32_e32 v3, v4, v4
	v_cvt_pk_bf16_f32 v21, v16, v17
	v_add_f32_e32 v10, v11, v10
	v_cvt_pk_bf16_f32 v13, v8, v9
	v_cvt_pk_bf16_f32 v15, v4, v5
	s_and_b64 vcc, exec, s[46:47]
	v_add_f32_e32 v2, v3, v2
	ds_bpermute_b32 v20, v228, v20
	ds_bpermute_b32 v21, v228, v21
	ds_bpermute_b32 v22, v228, v22
	ds_bpermute_b32 v23, v228, v23
	ds_bpermute_b32 v12, v228, v12
	ds_bpermute_b32 v13, v228, v13
	ds_bpermute_b32 v14, v228, v14
	ds_bpermute_b32 v15, v228, v15
	s_waitcnt lgkmcnt(0)
	global_store_dwordx4 v[24:25], v[20:23], off
	global_store_dwordx4 v[24:25], v[12:15], off offset:256
	s_cbranch_vccz .LBB0_416
	s_and_b64 vcc, exec, s[48:49]
	s_cbranch_vccz .LBB0_417

; __device__ __forceinline__ size_t ws_wg8(int l) { return (l & 1) ? WS_WS1 + 12 * MiB : WS_WG8; }
; #define LAS __attribute__((address_space(3)))
; #define G8_STAGE(bufoff, gbase, voff) do { _Pragma("unroll") for (int _i = 0; _i < 2; ++_i) \
;         __builtin_amdgcn_global_load_lds((const unsigned*)((const char*)(gbase) + (voff)[_i]), (LAS unsigned*)(lds + (bufoff) + ldsw + _i * 8192), 16, 0, 0); } while (0)
; #define G8_STAGE_A(bufoff, gbase, h_, nx_) do { if constexpr (Sched::GATHER) { unsigned vo_[2]; _Pragma("unroll") for (int q_ = 0; q_ < 2; ++q_) vo_[q_] = (nx_) ? gnxt[h_][q_] : goff[h_][q_]; G8_STAGE(bufoff, gbase, vo_); } \
;         else { G8_STAGE(bufoff, (gbase) + ((h_) ? hstepA : (size_t)0), voffA); } } while (0)
; #define G8_WAIT_V(n) asm volatile("s_waitcnt vmcnt(" #n ")" ::: "memory")
; template <int lda, int ldb, class Epi, class Sched>
; __device__ __forceinline__ void gemm_phase(LAS unsigned char* lds, int wid, int lane, const char* baseA, const char* baseB, const Sched& S, const Epi& E) {
;     ...
;     G8_STAGE(G8_SB(0, 0), cB, voffB); if constexpr (!Epi::HALFN) { G8_STAGE(G8_SB(0, 1), cB + hstepB, voffB); } G8_STAGE_A(G8_SA(0, 0), cA, 0, false); G8_STAGE_A(G8_SA(0, 1), cA, 1, false);
;     if (wr == 1) G8_BAR;
;     G8_WAIT_V(2); G8_BAR;
;     G8_STAGE(G8_SB(1, 0), cB + kstep, voffB); G8_STAGE_A(G8_SA(1, 0), cA + kstep, 0, false); if constexpr (!Epi::HALFN) { G8_STAGE(G8_SB(1, 1), cB + hstepB + kstep, voffB); }
;     if constexpr (Epi::HALFN) { G8_WAIT_V(4); } else { G8_WAIT_V(6); } G8_BAR;
; __device__ __forceinline__ void gate_batches(LAS unsigned char* lds, int wv, int l, int max_batches) {
;     const Frame F = make_frame(lds, wv); const KA a = kargs();
;     unsigned* qg = F.ctl + CW_CVQ + l * 16 + 8;
;     volatile LAS int* gslot = (volatile LAS int*)(lds + MISC_OFF + 512);
; #pragma unroll 1
;     for (int nb = 0; nb < max_batches; ++nb) {
;         int bt;
;         if (F.tid == 0) *gslot = (int)__hip_atomic_fetch_add(qg, 1u, __ATOMIC_RELAXED, __HIP_MEMORY_SCOPE_AGENT);
;         __syncthreads(); bt = *gslot; __syncthreads();
;         if (bt >= 512) break;
;         GateSched GS{bt * 2, 2};
;         EpiGate8 GE{(unsigned char*)(F.ws + WS_GT), a->in[14] + l * 4096};
;         g8::gemm_phase<512, 512>(F.lds, F.wave, F.lane, (const char*)(F.ws + WS_XB8), (const char*)(F.ws + ws_wg8(l)), GS, GE);
.LBB0_445:
	s_lshl_b32 s14, s72, 12
	s_ashr_i32 s15, s14, 31
	s_lshl_b64 s[14:15], s[14:15], 2
	s_waitcnt lgkmcnt(0)
	s_add_u32 s42, s10, s14
	s_addc_u32 s43, s11, s15
	v_mbcnt_lo_u32_b32 v149, -1, 0
	v_mbcnt_hi_u32_b32 v149, -1, v149
	s_lshl_b32 s14, s3, 8
	s_or_b32 s14, s14, s95
	v_and_b32_e32 v150, 31, v149
	v_lshrrev_b32_e32 v149, 5, v149
	v_lshl_or_b32 v149, v149, 7, v150
	v_add_lshl_u32 v154, v149, s14, 2
	v_mov_b32_e32 v155, 0
	s_lshr_b32 s14, s27, 1
	s_add_i32 s14, s14, 0x23000
	v_lshl_add_u64 v[154:155], s[42:43], 0, v[154:155]
	s_mov_b32 m0, s14
	s_nop 0
	global_load_lds_dword v[154:155], off
	v_add_co_u32_e32 v154, vcc, 0x400, v154
	s_add_i32 m0, s14, 0x100
	s_nop 0
	v_addc_co_u32_e32 v155, vcc, 0, v155, vcc
	global_load_lds_dword v[154:155], off
	v_mov_b32_e32 v161, v31
	s_add_u32 s10, s16, 0x16900000
	v_mov_b32_e32 v157, v31
	v_lshl_add_u64 v[8:9], s[44:45], 0, v[160:161]
	s_addc_u32 s11, s17, 0
	s_add_i32 s58, s27, 0x18000
	v_mov_b32_e32 v163, v31
	v_lshl_add_u64 v[10:11], s[44:45], 0, v[156:157]
	v_lshl_add_u64 v[8:9], v[8:9], 0, s[22:23]
	s_mov_b32 m0, s58
	s_add_i32 s59, s27, 0x1a000
	v_mov_b32_e32 v159, v31
	v_lshl_add_u64 v[12:13], s[46:47], 0, v[162:163]
	s_waitcnt vmcnt(4)
	s_barrier
	global_load_lds_dwordx4 v[8:9], off
	v_lshl_add_u64 v[8:9], v[10:11], 0, s[22:23]
	s_mov_b32 m0, s59
	s_add_i32 s60, s27, 0x8000
	s_add_i32 s61, s27, 0xa000
	v_lshl_add_u64 v[14:15], s[46:47], 0, v[158:159]
	global_load_lds_dwordx4 v[8:9], off
	v_lshl_add_u64 v[8:9], v[12:13], 0, s[22:23]
	s_mov_b32 m0, s60
	s_add_u32 s14, s44, 0x20080
	global_load_lds_dwordx4 v[8:9], off
	v_lshl_add_u64 v[8:9], v[14:15], 0, s[22:23]
	s_mov_b32 m0, s61
	s_addc_u32 s15, s45, 0
	s_add_i32 s62, s27, 0x1c000
	global_load_lds_dwordx4 v[8:9], off
	v_lshl_add_u64 v[8:9], s[14:15], 0, v[160:161]
	s_mov_b32 m0, s62
	s_add_i32 s63, s27, 0x1e000
	global_load_lds_dwordx4 v[8:9], off
	v_lshl_add_u64 v[8:9], s[14:15], 0, v[156:157]
	s_mov_b32 m0, s63
	v_and_b32_e32 v7, 15, v0
	global_load_lds_dwordx4 v[8:9], off
	v_or_b32_e32 v8, s9, v7
	v_lshlrev_b32_e32 v10, 6, v8
	v_and_b32_e32 v11, 48, v0
	s_movk_i32 s4, 0x3c0
	v_lshrrev_b32_e32 v9, 6, v0
	v_and_or_b32 v10, v10, s4, v11
	v_readlane_b32 s4, v254, 8
	v_lshlrev_b32_e32 v0, 2, v0
	v_lshlrev_b32_e32 v12, 10, v9
	v_lshl_or_b32 v7, v7, 6, v11
	v_add_lshl_u32 v9, v9, s4, 10
	v_and_b32_e32 v0, 32, v0
	v_bitop3_b32 v0, v7, v9, v0 bitop3:0xde
	v_or_b32_e32 v148, 0x10000, v0
	v_add_u32_e32 v151, 0x14000, v0
	v_or_b32_e32 v176, 0x18000, v0
	v_add_u32_e32 v177, 0x1c000, v0
	v_add_u32_e32 v178, 0x10400, v0
	v_add_u32_e32 v179, 0x10800, v0
	v_add_u32_e32 v180, 0x10c00, v0
	v_add_u32_e32 v181, 0x14400, v0
	v_add_u32_e32 v205, 0x14800, v0
	v_add_u32_e32 v206, 0x14c00, v0
	v_add_u32_e32 v207, 0x18400, v0
	v_add_u32_e32 v208, 0x18800, v0
	v_add_u32_e32 v209, 0x18c00, v0
	v_add_u32_e32 v210, 0x1c400, v0
	v_add_u32_e32 v211, 0x1c800, v0
	v_add_u32_e32 v212, 0x1cc00, v0
	v_lshlrev_b32_e32 v0, 13, v1
	v_and_b32_e32 v0, 0xffffc000, v0
	v_lshl_add_u32 v0, v2, 10, v0
	v_and_b32_e32 v1, 1, v1
	v_lshl_or_b32 v0, v1, 6, v0
	v_lshl_add_u32 v164, v3, 1, v0
	v_lshlrev_b32_e32 v0, 13, v4
	v_lshlrev_b32_e32 v8, 2, v8
	v_and_b32_e32 v0, 0xffffc000, v0
	v_and_b32_e32 v8, 32, v8
	s_waitcnt vmcnt(8)
	v_lshl_add_u32 v0, v5, 10, v0
	v_and_b32_e32 v1, 1, v4
	v_bitop3_b32 v7, v10, v12, v8 bitop3:0xde
	s_or_b32 s64, s3, 1
	v_lshl_or_b32 v0, v1, 6, v0
	v_readlane_b32 s4, v253, 61
	v_mov_b32_e32 v19, v18
	v_mov_b32_e32 v20, v18
	v_mov_b32_e32 v21, v18
	s_lshl_b32 s65, s64, 18
	v_mov_b32_e32 v165, v31
	v_lshl_add_u32 v166, v6, 1, v0
	v_mov_b32_e32 v167, v31
	s_mov_b64 s[14:15], -1
	v_add_u32_e32 v213, s4, v7
	s_mov_b32 s20, s50
	v_mov_b32_e32 v16, v18
	s_barrier
	s_branch .LBB0_448

;     static __device__ __forceinline__ unsigned q8(float z) { return (unsigned)(fast_sigmoid(z) * 255.f + 0.5f); }
;     __device__ __forceinline__ void operator()(const f32x4 (&acc)[2][2][4][2], const g8::Unit& u, int wr, int wc, int fr, int fq) const {
;         const int row0 = u.pm * 256 + wr * 64 + fr, col0 = u.pn * 256 + wc * 32 + 8 * fq;
; #pragma unroll
;         for (int bj = 0; bj < 2; ++bj) {
;             const f32x4 bv0 = *(const f32x4*)(bgate + col0 + bj * 128), bv1 = *(const f32x4*)(bgate + col0 + bj * 128 + 4);
; #pragma unroll
;             for (int ai = 0; ai < 2; ++ai)
; #pragma unroll
;                 for (int m = 0; m < 4; ++m) { const int row = row0 + ai * 128 + m * 16; unsigned char* rp = GT + (size_t)row * 4096 + col0 + bj * 128;
;                     const f32x4 v0 = acc[ai][bj][m][0] * 0.03125f + bv0, v1 = acc[ai][bj][m][1] * 0.03125f + bv1;
;                     u32x2 w; w.x = q8(v0[0]) | (q8(v0[1]) << 8) | (q8(v0[2]) << 16) | (q8(v0[3]) << 24); w.y = q8(v1[0]) | (q8(v1[1]) << 8) | (q8(v1[2]) << 16) | (q8(v1[3]) << 24);
;                     *(u32x2*)rp = w; } }
;     }
.LBB0_455:
	s_mov_b32 s4, -1
	s_and_b32 s44, s3, 1
	s_lshr_b32 s45, s27, 1
	s_lshl_b32 s44, s44, 8
	s_add_i32 s45, s45, 0x23000
	s_add_i32 s44, s44, s45
	s_lshl_b32 s3, s3, 8
	v_mbcnt_lo_u32_b32 v0, s4, 0
	v_mbcnt_hi_u32_b32 v0, s4, v0
	s_lshl_b32 s4, s20, 8
	s_add_i32 s4, s4, s9
	v_lshrrev_b32_e32 v168, 2, v0
	v_and_b32_e32 v170, 3, v0
	v_and_b32_e32 v17, 60, v0
	v_or_b32_e32 v168, s4, v168
	v_lshrrev_b32_e32 v0, 1, v0
	s_or_b32 s3, s3, s95
	v_lshl_or_b32 v17, v170, 6, v17
	v_and_b32_e32 v0, 56, v0
	v_lshl_add_u32 v170, v170, 3, s3
	v_lshl_add_u32 v12, v0, 2, s44
	ds_read_b128 v[4:7], v12
	ds_read_b128 v[0:3], v12 offset:16
	ds_read_b128 v[214:217], v12 offset:128
	ds_read_b128 v[218:221], v12 offset:144
	v_ashrrev_i32_e32 v171, 31, v170
	v_ashrrev_i32_e32 v169, 31, v168
	v_lshlrev_b64 v[8:9], 12, v[168:169]
	s_mov_b64 s[44:45], 0x10000
	s_mov_b64 vcc, 0x80000
	v_lshl_add_u64 v[8:9], s[10:11], 0, v[8:9]
	s_mov_b32 s20, 0xbd38aa3b
	s_mov_b32 s21, 0x3b808081
	v_lshl_add_u64 v[8:9], v[8:9], 0, v[170:171]
	v_lshl_add_u64 v[10:11], v[8:9], 0, s[44:45]
	v_lshl_add_u64 v[222:223], v[8:9], 0, vcc
	v_lshl_add_u64 v[14:15], v[10:11], 0, s[44:45]
	v_lshl_add_u64 v[224:225], v[222:223], 0, s[44:45]
	v_lshl_add_u64 v[168:169], v[14:15], 0, s[44:45]
	v_lshl_add_u64 v[226:227], v[224:225], 0, s[44:45]
	v_lshl_add_u64 v[228:229], v[226:227], 0, s[44:45]
	s_waitcnt lgkmcnt(0)
	v_mul_f32_e32 v0, 0xbfb8aa3b, v0
	v_mul_f32_e32 v1, 0xbfb8aa3b, v1
	v_mul_f32_e32 v2, 0xbfb8aa3b, v2
	v_mul_f32_e32 v3, 0xbfb8aa3b, v3
	v_mul_f32_e32 v4, 0xbfb8aa3b, v4
	v_mul_f32_e32 v5, 0xbfb8aa3b, v5
	v_mul_f32_e32 v6, 0xbfb8aa3b, v6
	v_mul_f32_e32 v7, 0xbfb8aa3b, v7
	v_mul_f32_e32 v214, 0xbfb8aa3b, v214
	v_mul_f32_e32 v215, 0xbfb8aa3b, v215
	v_mul_f32_e32 v216, 0xbfb8aa3b, v216
	v_mul_f32_e32 v217, 0xbfb8aa3b, v217
	v_mul_f32_e32 v218, 0xbfb8aa3b, v218
	v_mul_f32_e32 v219, 0xbfb8aa3b, v219
	v_mul_f32_e32 v220, 0xbfb8aa3b, v220
	v_mul_f32_e32 v221, 0xbfb8aa3b, v221
	v_pk_fma_f32 v[144:145], v[144:145], s[20:21], v[4:5] op_sel_hi:[1,0,1]
	v_pk_fma_f32 v[146:147], v[146:147], s[20:21], v[6:7] op_sel_hi:[1,0,1]
	v_pk_fma_f32 v[140:141], v[140:141], s[20:21], v[0:1] op_sel_hi:[1,0,1]
	v_pk_fma_f32 v[142:143], v[142:143], s[20:21], v[2:3] op_sel_hi:[1,0,1]
	v_pk_fma_f32 v[136:137], v[136:137], s[20:21], v[4:5] op_sel_hi:[1,0,1]
	v_pk_fma_f32 v[138:139], v[138:139], s[20:21], v[6:7] op_sel_hi:[1,0,1]
	v_pk_fma_f32 v[132:133], v[132:133], s[20:21], v[0:1] op_sel_hi:[1,0,1]
	v_pk_fma_f32 v[134:135], v[134:135], s[20:21], v[2:3] op_sel_hi:[1,0,1]
	v_exp_f32_e32 v144, v144
	v_exp_f32_e32 v145, v145
	v_exp_f32_e32 v146, v146
	v_exp_f32_e32 v147, v147
	v_exp_f32_e32 v140, v140
	v_exp_f32_e32 v141, v141
	v_exp_f32_e32 v142, v142
	v_exp_f32_e32 v143, v143
	v_exp_f32_e32 v136, v136
	v_exp_f32_e32 v137, v137
	v_exp_f32_e32 v138, v138
	v_exp_f32_e32 v139, v139
	v_exp_f32_e32 v132, v132
	v_exp_f32_e32 v133, v133
	v_exp_f32_e32 v134, v134
	v_exp_f32_e32 v135, v135
	v_fma_f32 v144, v144, s21, s21
	v_fma_f32 v145, v145, s21, s21
	v_fma_f32 v146, v146, s21, s21
	v_fma_f32 v147, v147, s21, s21
	v_fma_f32 v140, v140, s21, s21
	v_fma_f32 v141, v141, s21, s21
	v_fma_f32 v142, v142, s21, s21
	v_fma_f32 v143, v143, s21, s21
	v_fma_f32 v136, v136, s21, s21
	v_fma_f32 v137, v137, s21, s21
	v_fma_f32 v138, v138, s21, s21
	v_fma_f32 v139, v139, s21, s21
	v_fma_f32 v132, v132, s21, s21
	v_fma_f32 v133, v133, s21, s21
	v_fma_f32 v134, v134, s21, s21
	v_fma_f32 v135, v135, s21, s21
	v_rcp_f32_e32 v144, v144
	v_rcp_f32_e32 v145, v145
	v_rcp_f32_e32 v146, v146
	v_rcp_f32_e32 v147, v147
	v_rcp_f32_e32 v140, v140
	v_rcp_f32_e32 v141, v141
	v_rcp_f32_e32 v142, v142
	v_rcp_f32_e32 v143, v143
	v_rcp_f32_e32 v136, v136
	v_rcp_f32_e32 v137, v137
	v_rcp_f32_e32 v138, v138
	v_rcp_f32_e32 v139, v139
	v_rcp_f32_e32 v132, v132
	v_rcp_f32_e32 v133, v133
	v_rcp_f32_e32 v134, v134
	v_rcp_f32_e32 v135, v135
	v_cvt_rpi_i32_f32_e32 v144, v144
	v_cvt_rpi_i32_f32_e32 v136, v136
	v_cvt_rpi_i32_f32_sdwa v144, v145 dst_sel:BYTE_1 dst_unused:UNUSED_PRESERVE src0_sel:DWORD
	v_cvt_rpi_i32_f32_sdwa v136, v137 dst_sel:BYTE_1 dst_unused:UNUSED_PRESERVE src0_sel:DWORD
	v_cvt_rpi_i32_f32_e32 v145, v140
	v_cvt_rpi_i32_f32_e32 v137, v132
	v_cvt_rpi_i32_f32_sdwa v144, v146 dst_sel:BYTE_2 dst_unused:UNUSED_PRESERVE src0_sel:DWORD
	v_cvt_rpi_i32_f32_sdwa v136, v138 dst_sel:BYTE_2 dst_unused:UNUSED_PRESERVE src0_sel:DWORD
	v_cvt_rpi_i32_f32_sdwa v145, v141 dst_sel:BYTE_1 dst_unused:UNUSED_PRESERVE src0_sel:DWORD
	v_cvt_rpi_i32_f32_sdwa v137, v133 dst_sel:BYTE_1 dst_unused:UNUSED_PRESERVE src0_sel:DWORD
	v_cvt_rpi_i32_f32_sdwa v144, v147 dst_sel:BYTE_3 dst_unused:UNUSED_PRESERVE src0_sel:DWORD
	v_cvt_rpi_i32_f32_sdwa v136, v139 dst_sel:BYTE_3 dst_unused:UNUSED_PRESERVE src0_sel:DWORD
	v_cvt_rpi_i32_f32_sdwa v145, v142 dst_sel:BYTE_2 dst_unused:UNUSED_PRESERVE src0_sel:DWORD
	v_cvt_rpi_i32_f32_sdwa v137, v134 dst_sel:BYTE_2 dst_unused:UNUSED_PRESERVE src0_sel:DWORD
	v_cvt_rpi_i32_f32_sdwa v145, v143 dst_sel:BYTE_3 dst_unused:UNUSED_PRESERVE src0_sel:DWORD
	v_cvt_rpi_i32_f32_sdwa v137, v135 dst_sel:BYTE_3 dst_unused:UNUSED_PRESERVE src0_sel:DWORD
	ds_bpermute_b32 v144, v17, v144
	ds_bpermute_b32 v145, v17, v145
	ds_bpermute_b32 v136, v17, v136
	ds_bpermute_b32 v137, v17, v137
	v_pk_fma_f32 v[128:129], v[128:129], s[20:21], v[4:5] op_sel_hi:[1,0,1]
	v_pk_fma_f32 v[130:131], v[130:131], s[20:21], v[6:7] op_sel_hi:[1,0,1]
	v_pk_fma_f32 v[124:125], v[124:125], s[20:21], v[0:1] op_sel_hi:[1,0,1]
	v_pk_fma_f32 v[126:127], v[126:127], s[20:21], v[2:3] op_sel_hi:[1,0,1]
	v_pk_fma_f32 v[120:121], v[120:121], s[20:21], v[4:5] op_sel_hi:[1,0,1]
;     static __device__ __forceinline__ unsigned q8(float z) { return (unsigned)(fast_sigmoid(z) * 255.f + 0.5f); }
;     __device__ __forceinline__ void operator()(const f32x4 (&acc)[2][2][4][2], const g8::Unit& u, int wr, int wc, int fr, int fq) const {
;         const int row0 = u.pm * 256 + wr * 64 + fr, col0 = u.pn * 256 + wc * 32 + 8 * fq;
; #pragma unroll
;         for (int bj = 0; bj < 2; ++bj) {
;             const f32x4 bv0 = *(const f32x4*)(bgate + col0 + bj * 128), bv1 = *(const f32x4*)(bgate + col0 + bj * 128 + 4);
; #pragma unroll
;             for (int ai = 0; ai < 2; ++ai)
; #pragma unroll
;                 for (int m = 0; m < 4; ++m) { const int row = row0 + ai * 128 + m * 16; unsigned char* rp = GT + (size_t)row * 4096 + col0 + bj * 128;
;                     const f32x4 v0 = acc[ai][bj][m][0] * 0.03125f + bv0, v1 = acc[ai][bj][m][1] * 0.03125f + bv1;
;                     u32x2 w; w.x = q8(v0[0]) | (q8(v0[1]) << 8) | (q8(v0[2]) << 16) | (q8(v0[3]) << 24); w.y = q8(v1[0]) | (q8(v1[1]) << 8) | (q8(v1[2]) << 16) | (q8(v1[3]) << 24);
;                     *(u32x2*)rp = w; } }
;     }
	v_pk_fma_f32 v[122:123], v[122:123], s[20:21], v[6:7] op_sel_hi:[1,0,1]
	v_pk_fma_f32 v[116:117], v[116:117], s[20:21], v[0:1] op_sel_hi:[1,0,1]
	v_pk_fma_f32 v[118:119], v[118:119], s[20:21], v[2:3] op_sel_hi:[1,0,1]
	v_exp_f32_e32 v128, v128
	v_exp_f32_e32 v129, v129
	v_exp_f32_e32 v130, v130
	v_exp_f32_e32 v131, v131
	v_exp_f32_e32 v124, v124
	v_exp_f32_e32 v125, v125
	v_exp_f32_e32 v126, v126
	v_exp_f32_e32 v127, v127
	v_exp_f32_e32 v120, v120
	v_exp_f32_e32 v121, v121
	v_exp_f32_e32 v122, v122
	v_exp_f32_e32 v123, v123
	v_exp_f32_e32 v116, v116
	v_exp_f32_e32 v117, v117
	v_exp_f32_e32 v118, v118
	v_exp_f32_e32 v119, v119
	v_fma_f32 v128, v128, s21, s21
	v_fma_f32 v129, v129, s21, s21
	v_fma_f32 v130, v130, s21, s21
	v_fma_f32 v131, v131, s21, s21
	v_fma_f32 v124, v124, s21, s21
	v_fma_f32 v125, v125, s21, s21
	v_fma_f32 v126, v126, s21, s21
	v_fma_f32 v127, v127, s21, s21
	v_fma_f32 v120, v120, s21, s21
	v_fma_f32 v121, v121, s21, s21
	v_fma_f32 v122, v122, s21, s21
	v_fma_f32 v123, v123, s21, s21
	v_fma_f32 v116, v116, s21, s21
	v_fma_f32 v117, v117, s21, s21
	v_fma_f32 v118, v118, s21, s21
	v_fma_f32 v119, v119, s21, s21
	v_rcp_f32_e32 v128, v128
	v_rcp_f32_e32 v129, v129
	v_rcp_f32_e32 v130, v130
	v_rcp_f32_e32 v131, v131
	v_rcp_f32_e32 v124, v124
	v_rcp_f32_e32 v125, v125
	v_rcp_f32_e32 v126, v126
	v_rcp_f32_e32 v127, v127
	v_rcp_f32_e32 v120, v120
	v_rcp_f32_e32 v121, v121
	v_rcp_f32_e32 v122, v122
	v_rcp_f32_e32 v123, v123
	v_rcp_f32_e32 v116, v116
	v_rcp_f32_e32 v117, v117
	v_rcp_f32_e32 v118, v118
	v_rcp_f32_e32 v119, v119
	v_cvt_rpi_i32_f32_e32 v128, v128
	v_cvt_rpi_i32_f32_e32 v120, v120
	v_cvt_rpi_i32_f32_sdwa v128, v129 dst_sel:BYTE_1 dst_unused:UNUSED_PRESERVE src0_sel:DWORD
	v_cvt_rpi_i32_f32_sdwa v120, v121 dst_sel:BYTE_1 dst_unused:UNUSED_PRESERVE src0_sel:DWORD
	v_cvt_rpi_i32_f32_e32 v129, v124
	v_cvt_rpi_i32_f32_e32 v121, v116
	v_cvt_rpi_i32_f32_sdwa v128, v130 dst_sel:BYTE_2 dst_unused:UNUSED_PRESERVE src0_sel:DWORD
	v_cvt_rpi_i32_f32_sdwa v120, v122 dst_sel:BYTE_2 dst_unused:UNUSED_PRESERVE src0_sel:DWORD
	v_cvt_rpi_i32_f32_sdwa v129, v125 dst_sel:BYTE_1 dst_unused:UNUSED_PRESERVE src0_sel:DWORD
	v_cvt_rpi_i32_f32_sdwa v121, v117 dst_sel:BYTE_1 dst_unused:UNUSED_PRESERVE src0_sel:DWORD
	v_cvt_rpi_i32_f32_sdwa v128, v131 dst_sel:BYTE_3 dst_unused:UNUSED_PRESERVE src0_sel:DWORD
	v_cvt_rpi_i32_f32_sdwa v120, v123 dst_sel:BYTE_3 dst_unused:UNUSED_PRESERVE src0_sel:DWORD
	v_cvt_rpi_i32_f32_sdwa v129, v126 dst_sel:BYTE_2 dst_unused:UNUSED_PRESERVE src0_sel:DWORD
	v_cvt_rpi_i32_f32_sdwa v121, v118 dst_sel:BYTE_2 dst_unused:UNUSED_PRESERVE src0_sel:DWORD
	v_cvt_rpi_i32_f32_sdwa v129, v127 dst_sel:BYTE_3 dst_unused:UNUSED_PRESERVE src0_sel:DWORD
	v_cvt_rpi_i32_f32_sdwa v121, v119 dst_sel:BYTE_3 dst_unused:UNUSED_PRESERVE src0_sel:DWORD
	ds_bpermute_b32 v128, v17, v128
	ds_bpermute_b32 v129, v17, v129
	ds_bpermute_b32 v120, v17, v120
	ds_bpermute_b32 v121, v17, v121
	s_waitcnt lgkmcnt(4)
	global_store_dwordx2 v[8:9], v[144:145], off
	global_store_dwordx2 v[10:11], v[136:137], off
	v_pk_fma_f32 v[112:113], v[112:113], s[20:21], v[4:5] op_sel_hi:[1,0,1]
	v_pk_fma_f32 v[114:115], v[114:115], s[20:21], v[6:7] op_sel_hi:[1,0,1]
	v_pk_fma_f32 v[108:109], v[108:109], s[20:21], v[0:1] op_sel_hi:[1,0,1]
	v_pk_fma_f32 v[110:111], v[110:111], s[20:21], v[2:3] op_sel_hi:[1,0,1]
	v_pk_fma_f32 v[104:105], v[104:105], s[20:21], v[4:5] op_sel_hi:[1,0,1]
	v_pk_fma_f32 v[106:107], v[106:107], s[20:21], v[6:7] op_sel_hi:[1,0,1]
	v_pk_fma_f32 v[100:101], v[100:101], s[20:21], v[0:1] op_sel_hi:[1,0,1]
	v_pk_fma_f32 v[102:103], v[102:103], s[20:21], v[2:3] op_sel_hi:[1,0,1]
	v_exp_f32_e32 v112, v112
	v_exp_f32_e32 v113, v113
	v_exp_f32_e32 v114, v114
	v_exp_f32_e32 v115, v115
	v_exp_f32_e32 v108, v108
	v_exp_f32_e32 v109, v109
	v_exp_f32_e32 v110, v110
	v_exp_f32_e32 v111, v111
	v_exp_f32_e32 v104, v104
	v_exp_f32_e32 v105, v105
	v_exp_f32_e32 v106, v106
	v_exp_f32_e32 v107, v107
	v_exp_f32_e32 v100, v100
	v_exp_f32_e32 v101, v101
	v_exp_f32_e32 v102, v102
	v_exp_f32_e32 v103, v103
	v_fma_f32 v112, v112, s21, s21
	v_fma_f32 v113, v113, s21, s21
	v_fma_f32 v114, v114, s21, s21
	v_fma_f32 v115, v115, s21, s21
	v_fma_f32 v108, v108, s21, s21
	v_fma_f32 v109, v109, s21, s21
	v_fma_f32 v110, v110, s21, s21
	v_fma_f32 v111, v111, s21, s21
	v_fma_f32 v104, v104, s21, s21
	v_fma_f32 v105, v105, s21, s21
	v_fma_f32 v106, v106, s21, s21
	v_fma_f32 v107, v107, s21, s21
	v_fma_f32 v100, v100, s21, s21
	v_fma_f32 v101, v101, s21, s21
	v_fma_f32 v102, v102, s21, s21
	v_fma_f32 v103, v103, s21, s21
	v_rcp_f32_e32 v112, v112
	v_rcp_f32_e32 v113, v113
	v_rcp_f32_e32 v114, v114
	v_rcp_f32_e32 v115, v115
	v_rcp_f32_e32 v108, v108
	v_rcp_f32_e32 v109, v109
	v_rcp_f32_e32 v110, v110
	v_rcp_f32_e32 v111, v111
	v_rcp_f32_e32 v104, v104
	v_rcp_f32_e32 v105, v105
	v_rcp_f32_e32 v106, v106
	v_rcp_f32_e32 v107, v107
	v_rcp_f32_e32 v100, v100
	v_rcp_f32_e32 v101, v101
	v_rcp_f32_e32 v102, v102
	v_rcp_f32_e32 v103, v103
	v_cvt_rpi_i32_f32_e32 v112, v112
	v_cvt_rpi_i32_f32_e32 v104, v104
	v_cvt_rpi_i32_f32_sdwa v112, v113 dst_sel:BYTE_1 dst_unused:UNUSED_PRESERVE src0_sel:DWORD
	v_cvt_rpi_i32_f32_sdwa v104, v105 dst_sel:BYTE_1 dst_unused:UNUSED_PRESERVE src0_sel:DWORD
	v_cvt_rpi_i32_f32_e32 v113, v108
	v_cvt_rpi_i32_f32_e32 v105, v100
	v_cvt_rpi_i32_f32_sdwa v112, v114 dst_sel:BYTE_2 dst_unused:UNUSED_PRESERVE src0_sel:DWORD
	v_cvt_rpi_i32_f32_sdwa v104, v106 dst_sel:BYTE_2 dst_unused:UNUSED_PRESERVE src0_sel:DWORD
	v_cvt_rpi_i32_f32_sdwa v113, v109 dst_sel:BYTE_1 dst_unused:UNUSED_PRESERVE src0_sel:DWORD
	v_cvt_rpi_i32_f32_sdwa v105, v101 dst_sel:BYTE_1 dst_unused:UNUSED_PRESERVE src0_sel:DWORD
	v_cvt_rpi_i32_f32_sdwa v112, v115 dst_sel:BYTE_3 dst_unused:UNUSED_PRESERVE src0_sel:DWORD
	v_cvt_rpi_i32_f32_sdwa v104, v107 dst_sel:BYTE_3 dst_unused:UNUSED_PRESERVE src0_sel:DWORD
	v_cvt_rpi_i32_f32_sdwa v113, v110 dst_sel:BYTE_2 dst_unused:UNUSED_PRESERVE src0_sel:DWORD
	v_cvt_rpi_i32_f32_sdwa v105, v102 dst_sel:BYTE_2 dst_unused:UNUSED_PRESERVE src0_sel:DWORD
	v_cvt_rpi_i32_f32_sdwa v113, v111 dst_sel:BYTE_3 dst_unused:UNUSED_PRESERVE src0_sel:DWORD
	v_cvt_rpi_i32_f32_sdwa v105, v103 dst_sel:BYTE_3 dst_unused:UNUSED_PRESERVE src0_sel:DWORD
	ds_bpermute_b32 v112, v17, v112
	ds_bpermute_b32 v113, v17, v113
	ds_bpermute_b32 v104, v17, v104
	ds_bpermute_b32 v105, v17, v105
	s_waitcnt lgkmcnt(4)
;     static __device__ __forceinline__ unsigned q8(float z) { return (unsigned)(fast_sigmoid(z) * 255.f + 0.5f); }
;     __device__ __forceinline__ void operator()(const f32x4 (&acc)[2][2][4][2], const g8::Unit& u, int wr, int wc, int fr, int fq) const {
;         const int row0 = u.pm * 256 + wr * 64 + fr, col0 = u.pn * 256 + wc * 32 + 8 * fq;
; #pragma unroll
;         for (int bj = 0; bj < 2; ++bj) {
;             const f32x4 bv0 = *(const f32x4*)(bgate + col0 + bj * 128), bv1 = *(const f32x4*)(bgate + col0 + bj * 128 + 4);
; #pragma unroll
;             for (int ai = 0; ai < 2; ++ai)
; #pragma unroll
;                 for (int m = 0; m < 4; ++m) { const int row = row0 + ai * 128 + m * 16; unsigned char* rp = GT + (size_t)row * 4096 + col0 + bj * 128;
;                     const f32x4 v0 = acc[ai][bj][m][0] * 0.03125f + bv0, v1 = acc[ai][bj][m][1] * 0.03125f + bv1;
;                     u32x2 w; w.x = q8(v0[0]) | (q8(v0[1]) << 8) | (q8(v0[2]) << 16) | (q8(v0[3]) << 24); w.y = q8(v1[0]) | (q8(v1[1]) << 8) | (q8(v1[2]) << 16) | (q8(v1[3]) << 24);
;                     *(u32x2*)rp = w; } }
;     }
	global_store_dwordx2 v[14:15], v[128:129], off
	global_store_dwordx2 v[168:169], v[120:121], off
	v_pk_fma_f32 v[96:97], v[96:97], s[20:21], v[4:5] op_sel_hi:[1,0,1]
	v_pk_fma_f32 v[98:99], v[98:99], s[20:21], v[6:7] op_sel_hi:[1,0,1]
	v_pk_fma_f32 v[92:93], v[92:93], s[20:21], v[0:1] op_sel_hi:[1,0,1]
	v_pk_fma_f32 v[94:95], v[94:95], s[20:21], v[2:3] op_sel_hi:[1,0,1]
	v_pk_fma_f32 v[88:89], v[88:89], s[20:21], v[4:5] op_sel_hi:[1,0,1]
	v_pk_fma_f32 v[90:91], v[90:91], s[20:21], v[6:7] op_sel_hi:[1,0,1]
	v_pk_fma_f32 v[84:85], v[84:85], s[20:21], v[0:1] op_sel_hi:[1,0,1]
	v_pk_fma_f32 v[86:87], v[86:87], s[20:21], v[2:3] op_sel_hi:[1,0,1]
	v_exp_f32_e32 v96, v96
	v_exp_f32_e32 v97, v97
	v_exp_f32_e32 v98, v98
	v_exp_f32_e32 v99, v99
	v_exp_f32_e32 v92, v92
	v_exp_f32_e32 v93, v93
	v_exp_f32_e32 v94, v94
	v_exp_f32_e32 v95, v95
	v_exp_f32_e32 v88, v88
	v_exp_f32_e32 v89, v89
	v_exp_f32_e32 v90, v90
	v_exp_f32_e32 v91, v91
	v_exp_f32_e32 v84, v84
	v_exp_f32_e32 v85, v85
	v_exp_f32_e32 v86, v86
	v_exp_f32_e32 v87, v87
	v_fma_f32 v96, v96, s21, s21
	v_fma_f32 v97, v97, s21, s21
	v_fma_f32 v98, v98, s21, s21
	v_fma_f32 v99, v99, s21, s21
	v_fma_f32 v92, v92, s21, s21
	v_fma_f32 v93, v93, s21, s21
	v_fma_f32 v94, v94, s21, s21
	v_fma_f32 v95, v95, s21, s21
	v_fma_f32 v88, v88, s21, s21
	v_fma_f32 v89, v89, s21, s21
	v_fma_f32 v90, v90, s21, s21
	v_fma_f32 v91, v91, s21, s21
	v_fma_f32 v84, v84, s21, s21
	v_fma_f32 v85, v85, s21, s21
	v_fma_f32 v86, v86, s21, s21
	v_fma_f32 v87, v87, s21, s21
	v_rcp_f32_e32 v96, v96
	v_rcp_f32_e32 v97, v97
	v_rcp_f32_e32 v98, v98
	v_rcp_f32_e32 v99, v99
	v_rcp_f32_e32 v92, v92
	v_rcp_f32_e32 v93, v93
	v_rcp_f32_e32 v94, v94
	v_rcp_f32_e32 v95, v95
	v_rcp_f32_e32 v88, v88
	v_rcp_f32_e32 v89, v89
	v_rcp_f32_e32 v90, v90
	v_rcp_f32_e32 v91, v91
	v_rcp_f32_e32 v84, v84
	v_rcp_f32_e32 v85, v85
	v_rcp_f32_e32 v86, v86
	v_rcp_f32_e32 v87, v87
	v_cvt_rpi_i32_f32_e32 v96, v96
	v_cvt_rpi_i32_f32_e32 v88, v88
	v_cvt_rpi_i32_f32_sdwa v96, v97 dst_sel:BYTE_1 dst_unused:UNUSED_PRESERVE src0_sel:DWORD
	v_cvt_rpi_i32_f32_sdwa v88, v89 dst_sel:BYTE_1 dst_unused:UNUSED_PRESERVE src0_sel:DWORD
	v_cvt_rpi_i32_f32_e32 v97, v92
	v_cvt_rpi_i32_f32_e32 v89, v84
	v_cvt_rpi_i32_f32_sdwa v96, v98 dst_sel:BYTE_2 dst_unused:UNUSED_PRESERVE src0_sel:DWORD
	v_cvt_rpi_i32_f32_sdwa v88, v90 dst_sel:BYTE_2 dst_unused:UNUSED_PRESERVE src0_sel:DWORD
	v_cvt_rpi_i32_f32_sdwa v97, v93 dst_sel:BYTE_1 dst_unused:UNUSED_PRESERVE src0_sel:DWORD
	v_cvt_rpi_i32_f32_sdwa v89, v85 dst_sel:BYTE_1 dst_unused:UNUSED_PRESERVE src0_sel:DWORD
	v_cvt_rpi_i32_f32_sdwa v96, v99 dst_sel:BYTE_3 dst_unused:UNUSED_PRESERVE src0_sel:DWORD
	v_cvt_rpi_i32_f32_sdwa v88, v91 dst_sel:BYTE_3 dst_unused:UNUSED_PRESERVE src0_sel:DWORD
	v_cvt_rpi_i32_f32_sdwa v97, v94 dst_sel:BYTE_2 dst_unused:UNUSED_PRESERVE src0_sel:DWORD
	v_cvt_rpi_i32_f32_sdwa v89, v86 dst_sel:BYTE_2 dst_unused:UNUSED_PRESERVE src0_sel:DWORD
	v_cvt_rpi_i32_f32_sdwa v97, v95 dst_sel:BYTE_3 dst_unused:UNUSED_PRESERVE src0_sel:DWORD
	v_cvt_rpi_i32_f32_sdwa v89, v87 dst_sel:BYTE_3 dst_unused:UNUSED_PRESERVE src0_sel:DWORD
	ds_bpermute_b32 v96, v17, v96
	ds_bpermute_b32 v97, v17, v97
	ds_bpermute_b32 v88, v17, v88
	ds_bpermute_b32 v89, v17, v89
	s_waitcnt lgkmcnt(4)
	global_store_dwordx2 v[222:223], v[112:113], off
	global_store_dwordx2 v[224:225], v[104:105], off
	v_pk_fma_f32 v[80:81], v[80:81], s[20:21], v[214:215] op_sel_hi:[1,0,1]
	v_pk_fma_f32 v[82:83], v[82:83], s[20:21], v[216:217] op_sel_hi:[1,0,1]
	v_pk_fma_f32 v[76:77], v[76:77], s[20:21], v[218:219] op_sel_hi:[1,0,1]
	v_pk_fma_f32 v[78:79], v[78:79], s[20:21], v[220:221] op_sel_hi:[1,0,1]
	v_pk_fma_f32 v[72:73], v[72:73], s[20:21], v[214:215] op_sel_hi:[1,0,1]
	v_pk_fma_f32 v[74:75], v[74:75], s[20:21], v[216:217] op_sel_hi:[1,0,1]
	v_pk_fma_f32 v[68:69], v[68:69], s[20:21], v[218:219] op_sel_hi:[1,0,1]
	v_pk_fma_f32 v[70:71], v[70:71], s[20:21], v[220:221] op_sel_hi:[1,0,1]
	v_exp_f32_e32 v80, v80
	v_exp_f32_e32 v81, v81
	v_exp_f32_e32 v82, v82
	v_exp_f32_e32 v83, v83
	v_exp_f32_e32 v76, v76
	v_exp_f32_e32 v77, v77
	v_exp_f32_e32 v78, v78
	v_exp_f32_e32 v79, v79
	v_exp_f32_e32 v72, v72
	v_exp_f32_e32 v73, v73
	v_exp_f32_e32 v74, v74
	v_exp_f32_e32 v75, v75
	v_exp_f32_e32 v68, v68
	v_exp_f32_e32 v69, v69
	v_exp_f32_e32 v70, v70
	v_exp_f32_e32 v71, v71
	v_fma_f32 v80, v80, s21, s21
	v_fma_f32 v81, v81, s21, s21
	v_fma_f32 v82, v82, s21, s21
	v_fma_f32 v83, v83, s21, s21
	v_fma_f32 v76, v76, s21, s21
	v_fma_f32 v77, v77, s21, s21
	v_fma_f32 v78, v78, s21, s21
	v_fma_f32 v79, v79, s21, s21
	v_fma_f32 v72, v72, s21, s21
	v_fma_f32 v73, v73, s21, s21
	v_fma_f32 v74, v74, s21, s21
	v_fma_f32 v75, v75, s21, s21
	v_fma_f32 v68, v68, s21, s21
	v_fma_f32 v69, v69, s21, s21
	v_fma_f32 v70, v70, s21, s21
	v_fma_f32 v71, v71, s21, s21
	v_rcp_f32_e32 v80, v80
	v_rcp_f32_e32 v81, v81
	v_rcp_f32_e32 v82, v82
	v_rcp_f32_e32 v83, v83
	v_rcp_f32_e32 v76, v76
	v_rcp_f32_e32 v77, v77
	v_rcp_f32_e32 v78, v78
	v_rcp_f32_e32 v79, v79
	v_rcp_f32_e32 v72, v72
	v_rcp_f32_e32 v73, v73
	v_rcp_f32_e32 v74, v74
	v_rcp_f32_e32 v75, v75
	v_rcp_f32_e32 v68, v68
	v_rcp_f32_e32 v69, v69
	v_rcp_f32_e32 v70, v70
	v_rcp_f32_e32 v71, v71
	v_cvt_rpi_i32_f32_e32 v80, v80
	v_cvt_rpi_i32_f32_e32 v72, v72
	v_cvt_rpi_i32_f32_sdwa v80, v81 dst_sel:BYTE_1 dst_unused:UNUSED_PRESERVE src0_sel:DWORD
	v_cvt_rpi_i32_f32_sdwa v72, v73 dst_sel:BYTE_1 dst_unused:UNUSED_PRESERVE src0_sel:DWORD
	v_cvt_rpi_i32_f32_e32 v81, v76
	v_cvt_rpi_i32_f32_e32 v73, v68
	v_cvt_rpi_i32_f32_sdwa v80, v82 dst_sel:BYTE_2 dst_unused:UNUSED_PRESERVE src0_sel:DWORD
	v_cvt_rpi_i32_f32_sdwa v72, v74 dst_sel:BYTE_2 dst_unused:UNUSED_PRESERVE src0_sel:DWORD
	v_cvt_rpi_i32_f32_sdwa v81, v77 dst_sel:BYTE_1 dst_unused:UNUSED_PRESERVE src0_sel:DWORD
	v_cvt_rpi_i32_f32_sdwa v73, v69 dst_sel:BYTE_1 dst_unused:UNUSED_PRESERVE src0_sel:DWORD
	v_cvt_rpi_i32_f32_sdwa v80, v83 dst_sel:BYTE_3 dst_unused:UNUSED_PRESERVE src0_sel:DWORD
	v_cvt_rpi_i32_f32_sdwa v72, v75 dst_sel:BYTE_3 dst_unused:UNUSED_PRESERVE src0_sel:DWORD
	v_cvt_rpi_i32_f32_sdwa v81, v78 dst_sel:BYTE_2 dst_unused:UNUSED_PRESERVE src0_sel:DWORD
	v_cvt_rpi_i32_f32_sdwa v73, v70 dst_sel:BYTE_2 dst_unused:UNUSED_PRESERVE src0_sel:DWORD
	v_cvt_rpi_i32_f32_sdwa v81, v79 dst_sel:BYTE_3 dst_unused:UNUSED_PRESERVE src0_sel:DWORD
	v_cvt_rpi_i32_f32_sdwa v73, v71 dst_sel:BYTE_3 dst_unused:UNUSED_PRESERVE src0_sel:DWORD
	ds_bpermute_b32 v80, v17, v80
	ds_bpermute_b32 v81, v17, v81
	ds_bpermute_b32 v72, v17, v72
	ds_bpermute_b32 v73, v17, v73
	s_waitcnt lgkmcnt(4)
;     static __device__ __forceinline__ unsigned q8(float z) { return (unsigned)(fast_sigmoid(z) * 255.f + 0.5f); }
;     __device__ __forceinline__ void operator()(const f32x4 (&acc)[2][2][4][2], const g8::Unit& u, int wr, int wc, int fr, int fq) const {
;         const int row0 = u.pm * 256 + wr * 64 + fr, col0 = u.pn * 256 + wc * 32 + 8 * fq;
; #pragma unroll
;         for (int bj = 0; bj < 2; ++bj) {
;             const f32x4 bv0 = *(const f32x4*)(bgate + col0 + bj * 128), bv1 = *(const f32x4*)(bgate + col0 + bj * 128 + 4);
; #pragma unroll
;             for (int ai = 0; ai < 2; ++ai)
; #pragma unroll
;                 for (int m = 0; m < 4; ++m) { const int row = row0 + ai * 128 + m * 16; unsigned char* rp = GT + (size_t)row * 4096 + col0 + bj * 128;
;                     const f32x4 v0 = acc[ai][bj][m][0] * 0.03125f + bv0, v1 = acc[ai][bj][m][1] * 0.03125f + bv1;
;                     u32x2 w; w.x = q8(v0[0]) | (q8(v0[1]) << 8) | (q8(v0[2]) << 16) | (q8(v0[3]) << 24); w.y = q8(v1[0]) | (q8(v1[1]) << 8) | (q8(v1[2]) << 16) | (q8(v1[3]) << 24);
;                     *(u32x2*)rp = w; } }
;     }
	global_store_dwordx2 v[226:227], v[96:97], off
	global_store_dwordx2 v[228:229], v[88:89], off
	v_pk_fma_f32 v[64:65], v[64:65], s[20:21], v[214:215] op_sel_hi:[1,0,1]
	v_pk_fma_f32 v[66:67], v[66:67], s[20:21], v[216:217] op_sel_hi:[1,0,1]
	v_pk_fma_f32 v[60:61], v[60:61], s[20:21], v[218:219] op_sel_hi:[1,0,1]
	v_pk_fma_f32 v[62:63], v[62:63], s[20:21], v[220:221] op_sel_hi:[1,0,1]
	v_pk_fma_f32 v[56:57], v[56:57], s[20:21], v[214:215] op_sel_hi:[1,0,1]
	v_pk_fma_f32 v[58:59], v[58:59], s[20:21], v[216:217] op_sel_hi:[1,0,1]
	v_pk_fma_f32 v[52:53], v[52:53], s[20:21], v[218:219] op_sel_hi:[1,0,1]
	v_pk_fma_f32 v[54:55], v[54:55], s[20:21], v[220:221] op_sel_hi:[1,0,1]
	v_exp_f32_e32 v64, v64
	v_exp_f32_e32 v65, v65
	v_exp_f32_e32 v66, v66
	v_exp_f32_e32 v67, v67
	v_exp_f32_e32 v60, v60
	v_exp_f32_e32 v61, v61
	v_exp_f32_e32 v62, v62
	v_exp_f32_e32 v63, v63
	v_exp_f32_e32 v56, v56
	v_exp_f32_e32 v57, v57
	v_exp_f32_e32 v58, v58
	v_exp_f32_e32 v59, v59
	v_exp_f32_e32 v52, v52
	v_exp_f32_e32 v53, v53
	v_exp_f32_e32 v54, v54
	v_exp_f32_e32 v55, v55
	v_fma_f32 v64, v64, s21, s21
	v_fma_f32 v65, v65, s21, s21
	v_fma_f32 v66, v66, s21, s21
	v_fma_f32 v67, v67, s21, s21
	v_fma_f32 v60, v60, s21, s21
	v_fma_f32 v61, v61, s21, s21
	v_fma_f32 v62, v62, s21, s21
	v_fma_f32 v63, v63, s21, s21
	v_fma_f32 v56, v56, s21, s21
	v_fma_f32 v57, v57, s21, s21
	v_fma_f32 v58, v58, s21, s21
	v_fma_f32 v59, v59, s21, s21
	v_fma_f32 v52, v52, s21, s21
	v_fma_f32 v53, v53, s21, s21
	v_fma_f32 v54, v54, s21, s21
	v_fma_f32 v55, v55, s21, s21
	v_rcp_f32_e32 v64, v64
	v_rcp_f32_e32 v65, v65
	v_rcp_f32_e32 v66, v66
	v_rcp_f32_e32 v67, v67
	v_rcp_f32_e32 v60, v60
	v_rcp_f32_e32 v61, v61
	v_rcp_f32_e32 v62, v62
	v_rcp_f32_e32 v63, v63
	v_rcp_f32_e32 v56, v56
	v_rcp_f32_e32 v57, v57
	v_rcp_f32_e32 v58, v58
	v_rcp_f32_e32 v59, v59
	v_rcp_f32_e32 v52, v52
	v_rcp_f32_e32 v53, v53
	v_rcp_f32_e32 v54, v54
	v_rcp_f32_e32 v55, v55
	v_cvt_rpi_i32_f32_e32 v64, v64
	v_cvt_rpi_i32_f32_e32 v56, v56
	v_cvt_rpi_i32_f32_sdwa v64, v65 dst_sel:BYTE_1 dst_unused:UNUSED_PRESERVE src0_sel:DWORD
	v_cvt_rpi_i32_f32_sdwa v56, v57 dst_sel:BYTE_1 dst_unused:UNUSED_PRESERVE src0_sel:DWORD
	v_cvt_rpi_i32_f32_e32 v65, v60
	v_cvt_rpi_i32_f32_e32 v57, v52
	v_cvt_rpi_i32_f32_sdwa v64, v66 dst_sel:BYTE_2 dst_unused:UNUSED_PRESERVE src0_sel:DWORD
	v_cvt_rpi_i32_f32_sdwa v56, v58 dst_sel:BYTE_2 dst_unused:UNUSED_PRESERVE src0_sel:DWORD
	v_cvt_rpi_i32_f32_sdwa v65, v61 dst_sel:BYTE_1 dst_unused:UNUSED_PRESERVE src0_sel:DWORD
	v_cvt_rpi_i32_f32_sdwa v57, v53 dst_sel:BYTE_1 dst_unused:UNUSED_PRESERVE src0_sel:DWORD
	v_cvt_rpi_i32_f32_sdwa v64, v67 dst_sel:BYTE_3 dst_unused:UNUSED_PRESERVE src0_sel:DWORD
	v_cvt_rpi_i32_f32_sdwa v56, v59 dst_sel:BYTE_3 dst_unused:UNUSED_PRESERVE src0_sel:DWORD
	v_cvt_rpi_i32_f32_sdwa v65, v62 dst_sel:BYTE_2 dst_unused:UNUSED_PRESERVE src0_sel:DWORD
	v_cvt_rpi_i32_f32_sdwa v57, v54 dst_sel:BYTE_2 dst_unused:UNUSED_PRESERVE src0_sel:DWORD
	v_cvt_rpi_i32_f32_sdwa v65, v63 dst_sel:BYTE_3 dst_unused:UNUSED_PRESERVE src0_sel:DWORD
	v_cvt_rpi_i32_f32_sdwa v57, v55 dst_sel:BYTE_3 dst_unused:UNUSED_PRESERVE src0_sel:DWORD
	ds_bpermute_b32 v64, v17, v64
	ds_bpermute_b32 v65, v17, v65
	ds_bpermute_b32 v56, v17, v56
	ds_bpermute_b32 v57, v17, v57
	s_waitcnt lgkmcnt(4)
	global_store_dwordx2 v[8:9], v[80:81], off offset:128
	global_store_dwordx2 v[10:11], v[72:73], off offset:128
	v_pk_fma_f32 v[48:49], v[48:49], s[20:21], v[214:215] op_sel_hi:[1,0,1]
	v_pk_fma_f32 v[50:51], v[50:51], s[20:21], v[216:217] op_sel_hi:[1,0,1]
	v_pk_fma_f32 v[44:45], v[44:45], s[20:21], v[218:219] op_sel_hi:[1,0,1]
	v_pk_fma_f32 v[46:47], v[46:47], s[20:21], v[220:221] op_sel_hi:[1,0,1]
	v_pk_fma_f32 v[40:41], v[40:41], s[20:21], v[214:215] op_sel_hi:[1,0,1]
	v_pk_fma_f32 v[42:43], v[42:43], s[20:21], v[216:217] op_sel_hi:[1,0,1]
	v_pk_fma_f32 v[36:37], v[36:37], s[20:21], v[218:219] op_sel_hi:[1,0,1]
	v_pk_fma_f32 v[38:39], v[38:39], s[20:21], v[220:221] op_sel_hi:[1,0,1]
	v_exp_f32_e32 v48, v48
	v_exp_f32_e32 v49, v49
	v_exp_f32_e32 v50, v50
	v_exp_f32_e32 v51, v51
	v_exp_f32_e32 v44, v44
	v_exp_f32_e32 v45, v45
	v_exp_f32_e32 v46, v46
	v_exp_f32_e32 v47, v47
	v_exp_f32_e32 v40, v40
	v_exp_f32_e32 v41, v41
	v_exp_f32_e32 v42, v42
	v_exp_f32_e32 v43, v43
	v_exp_f32_e32 v36, v36
	v_exp_f32_e32 v37, v37
	v_exp_f32_e32 v38, v38
	v_exp_f32_e32 v39, v39
	v_fma_f32 v48, v48, s21, s21
	v_fma_f32 v49, v49, s21, s21
	v_fma_f32 v50, v50, s21, s21
	v_fma_f32 v51, v51, s21, s21
	v_fma_f32 v44, v44, s21, s21
	v_fma_f32 v45, v45, s21, s21
	v_fma_f32 v46, v46, s21, s21
	v_fma_f32 v47, v47, s21, s21
	v_fma_f32 v40, v40, s21, s21
	v_fma_f32 v41, v41, s21, s21
	v_fma_f32 v42, v42, s21, s21
	v_fma_f32 v43, v43, s21, s21
	v_fma_f32 v36, v36, s21, s21
	v_fma_f32 v37, v37, s21, s21
	v_fma_f32 v38, v38, s21, s21
	v_fma_f32 v39, v39, s21, s21
	v_rcp_f32_e32 v48, v48
	v_rcp_f32_e32 v49, v49
	v_rcp_f32_e32 v50, v50
	v_rcp_f32_e32 v51, v51
	v_rcp_f32_e32 v44, v44
	v_rcp_f32_e32 v45, v45
	v_rcp_f32_e32 v46, v46
	v_rcp_f32_e32 v47, v47
	v_rcp_f32_e32 v40, v40
	v_rcp_f32_e32 v41, v41
	v_rcp_f32_e32 v42, v42
	v_rcp_f32_e32 v43, v43
	v_rcp_f32_e32 v36, v36
	v_rcp_f32_e32 v37, v37
	v_rcp_f32_e32 v38, v38
	v_rcp_f32_e32 v39, v39
	v_cvt_rpi_i32_f32_e32 v48, v48
	v_cvt_rpi_i32_f32_e32 v40, v40
	v_cvt_rpi_i32_f32_sdwa v48, v49 dst_sel:BYTE_1 dst_unused:UNUSED_PRESERVE src0_sel:DWORD
	v_cvt_rpi_i32_f32_sdwa v40, v41 dst_sel:BYTE_1 dst_unused:UNUSED_PRESERVE src0_sel:DWORD
	v_cvt_rpi_i32_f32_e32 v49, v44
	v_cvt_rpi_i32_f32_e32 v41, v36
	v_cvt_rpi_i32_f32_sdwa v48, v50 dst_sel:BYTE_2 dst_unused:UNUSED_PRESERVE src0_sel:DWORD
	v_cvt_rpi_i32_f32_sdwa v40, v42 dst_sel:BYTE_2 dst_unused:UNUSED_PRESERVE src0_sel:DWORD
	v_cvt_rpi_i32_f32_sdwa v49, v45 dst_sel:BYTE_1 dst_unused:UNUSED_PRESERVE src0_sel:DWORD
	v_cvt_rpi_i32_f32_sdwa v41, v37 dst_sel:BYTE_1 dst_unused:UNUSED_PRESERVE src0_sel:DWORD
	v_cvt_rpi_i32_f32_sdwa v48, v51 dst_sel:BYTE_3 dst_unused:UNUSED_PRESERVE src0_sel:DWORD
	v_cvt_rpi_i32_f32_sdwa v40, v43 dst_sel:BYTE_3 dst_unused:UNUSED_PRESERVE src0_sel:DWORD
	v_cvt_rpi_i32_f32_sdwa v49, v46 dst_sel:BYTE_2 dst_unused:UNUSED_PRESERVE src0_sel:DWORD
	v_cvt_rpi_i32_f32_sdwa v41, v38 dst_sel:BYTE_2 dst_unused:UNUSED_PRESERVE src0_sel:DWORD
	v_cvt_rpi_i32_f32_sdwa v49, v47 dst_sel:BYTE_3 dst_unused:UNUSED_PRESERVE src0_sel:DWORD
	v_cvt_rpi_i32_f32_sdwa v41, v39 dst_sel:BYTE_3 dst_unused:UNUSED_PRESERVE src0_sel:DWORD
	ds_bpermute_b32 v48, v17, v48
	ds_bpermute_b32 v49, v17, v49
	ds_bpermute_b32 v40, v17, v40
	ds_bpermute_b32 v41, v17, v41
	s_waitcnt lgkmcnt(4)
;     static __device__ __forceinline__ unsigned q8(float z) { return (unsigned)(fast_sigmoid(z) * 255.f + 0.5f); }
;     __device__ __forceinline__ void operator()(const f32x4 (&acc)[2][2][4][2], const g8::Unit& u, int wr, int wc, int fr, int fq) const {
;         const int row0 = u.pm * 256 + wr * 64 + fr, col0 = u.pn * 256 + wc * 32 + 8 * fq;
; #pragma unroll
;         for (int bj = 0; bj < 2; ++bj) {
;             const f32x4 bv0 = *(const f32x4*)(bgate + col0 + bj * 128), bv1 = *(const f32x4*)(bgate + col0 + bj * 128 + 4);
; #pragma unroll
;             for (int ai = 0; ai < 2; ++ai)
; #pragma unroll
;                 for (int m = 0; m < 4; ++m) { const int row = row0 + ai * 128 + m * 16; unsigned char* rp = GT + (size_t)row * 4096 + col0 + bj * 128;
;                     const f32x4 v0 = acc[ai][bj][m][0] * 0.03125f + bv0, v1 = acc[ai][bj][m][1] * 0.03125f + bv1;
;                     u32x2 w; w.x = q8(v0[0]) | (q8(v0[1]) << 8) | (q8(v0[2]) << 16) | (q8(v0[3]) << 24); w.y = q8(v1[0]) | (q8(v1[1]) << 8) | (q8(v1[2]) << 16) | (q8(v1[3]) << 24);
;                     *(u32x2*)rp = w; } }
;     }
	global_store_dwordx2 v[14:15], v[64:65], off offset:128
	global_store_dwordx2 v[168:169], v[56:57], off offset:128
	v_pk_fma_f32 v[32:33], v[32:33], s[20:21], v[214:215] op_sel_hi:[1,0,1]
	v_pk_fma_f32 v[34:35], v[34:35], s[20:21], v[216:217] op_sel_hi:[1,0,1]
	v_pk_fma_f32 v[26:27], v[26:27], s[20:21], v[218:219] op_sel_hi:[1,0,1]
	v_pk_fma_f32 v[28:29], v[28:29], s[20:21], v[220:221] op_sel_hi:[1,0,1]
	v_pk_fma_f32 v[22:23], v[22:23], s[20:21], v[214:215] op_sel_hi:[1,0,1]
	v_pk_fma_f32 v[24:25], v[24:25], s[20:21], v[216:217] op_sel_hi:[1,0,1]
	v_pk_fma_f32 v[18:19], v[18:19], s[20:21], v[218:219] op_sel_hi:[1,0,1]
	v_pk_fma_f32 v[20:21], v[20:21], s[20:21], v[220:221] op_sel_hi:[1,0,1]
	v_exp_f32_e32 v32, v32
	v_exp_f32_e32 v33, v33
	v_exp_f32_e32 v34, v34
	v_exp_f32_e32 v35, v35
	v_exp_f32_e32 v26, v26
	v_exp_f32_e32 v27, v27
	v_exp_f32_e32 v28, v28
	v_exp_f32_e32 v29, v29
	v_exp_f32_e32 v22, v22
	v_exp_f32_e32 v23, v23
	v_exp_f32_e32 v24, v24
	v_exp_f32_e32 v25, v25
	v_exp_f32_e32 v18, v18
	v_exp_f32_e32 v19, v19
	v_exp_f32_e32 v20, v20
	v_exp_f32_e32 v21, v21
	v_fma_f32 v32, v32, s21, s21
	v_fma_f32 v33, v33, s21, s21
	v_fma_f32 v34, v34, s21, s21
	v_fma_f32 v35, v35, s21, s21
	v_fma_f32 v26, v26, s21, s21
	v_fma_f32 v27, v27, s21, s21
	v_fma_f32 v28, v28, s21, s21
	v_fma_f32 v29, v29, s21, s21
	v_fma_f32 v22, v22, s21, s21
	v_fma_f32 v23, v23, s21, s21
	v_fma_f32 v24, v24, s21, s21
	v_fma_f32 v25, v25, s21, s21
	v_fma_f32 v18, v18, s21, s21
	v_fma_f32 v19, v19, s21, s21
	v_fma_f32 v20, v20, s21, s21
	v_fma_f32 v21, v21, s21, s21
	v_rcp_f32_e32 v32, v32
	v_rcp_f32_e32 v33, v33
	v_rcp_f32_e32 v34, v34
	v_rcp_f32_e32 v35, v35
	v_rcp_f32_e32 v26, v26
	v_rcp_f32_e32 v27, v27
	v_rcp_f32_e32 v28, v28
	v_rcp_f32_e32 v29, v29
	v_rcp_f32_e32 v22, v22
	v_rcp_f32_e32 v23, v23
	v_rcp_f32_e32 v24, v24
	v_rcp_f32_e32 v25, v25
	v_rcp_f32_e32 v18, v18
	v_rcp_f32_e32 v19, v19
	v_rcp_f32_e32 v20, v20
	v_rcp_f32_e32 v21, v21
	v_cvt_rpi_i32_f32_e32 v32, v32
	v_cvt_rpi_i32_f32_e32 v22, v22
	v_cvt_rpi_i32_f32_sdwa v32, v33 dst_sel:BYTE_1 dst_unused:UNUSED_PRESERVE src0_sel:DWORD
	v_cvt_rpi_i32_f32_sdwa v22, v23 dst_sel:BYTE_1 dst_unused:UNUSED_PRESERVE src0_sel:DWORD
	v_cvt_rpi_i32_f32_e32 v33, v26
	v_cvt_rpi_i32_f32_e32 v23, v18
	v_cvt_rpi_i32_f32_sdwa v32, v34 dst_sel:BYTE_2 dst_unused:UNUSED_PRESERVE src0_sel:DWORD
	v_cvt_rpi_i32_f32_sdwa v22, v24 dst_sel:BYTE_2 dst_unused:UNUSED_PRESERVE src0_sel:DWORD
	v_cvt_rpi_i32_f32_sdwa v33, v27 dst_sel:BYTE_1 dst_unused:UNUSED_PRESERVE src0_sel:DWORD
	v_cvt_rpi_i32_f32_sdwa v23, v19 dst_sel:BYTE_1 dst_unused:UNUSED_PRESERVE src0_sel:DWORD
	v_cvt_rpi_i32_f32_sdwa v32, v35 dst_sel:BYTE_3 dst_unused:UNUSED_PRESERVE src0_sel:DWORD
	v_cvt_rpi_i32_f32_sdwa v22, v25 dst_sel:BYTE_3 dst_unused:UNUSED_PRESERVE src0_sel:DWORD
	v_cvt_rpi_i32_f32_sdwa v33, v28 dst_sel:BYTE_2 dst_unused:UNUSED_PRESERVE src0_sel:DWORD
	v_cvt_rpi_i32_f32_sdwa v23, v20 dst_sel:BYTE_2 dst_unused:UNUSED_PRESERVE src0_sel:DWORD
	v_cvt_rpi_i32_f32_sdwa v33, v29 dst_sel:BYTE_3 dst_unused:UNUSED_PRESERVE src0_sel:DWORD
	v_cvt_rpi_i32_f32_sdwa v23, v21 dst_sel:BYTE_3 dst_unused:UNUSED_PRESERVE src0_sel:DWORD
	ds_bpermute_b32 v32, v17, v32
	ds_bpermute_b32 v33, v17, v33
	ds_bpermute_b32 v22, v17, v22
	ds_bpermute_b32 v23, v17, v23
	s_waitcnt lgkmcnt(4)
	global_store_dwordx2 v[222:223], v[48:49], off offset:128
	global_store_dwordx2 v[224:225], v[40:41], off offset:128
	s_waitcnt lgkmcnt(0)
	global_store_dwordx2 v[226:227], v[32:33], off offset:128
	global_store_dwordx2 v[228:229], v[22:23], off offset:128
	s_mov_b64 s[44:45], -1
	s_andn2_b64 vcc, exec, s[14:15]
	s_cbranch_vccnz .LBB0_447
	s_and_b64 vcc, exec, s[38:39]
	s_cbranch_vccnz .LBB0_446
	s_barrier
	s_branch .LBB0_446

; #define G8_STAGE(bufoff, gbase, voff) do { _Pragma("unroll") for (int _i = 0; _i < 2; ++_i) \
;         __builtin_amdgcn_global_load_lds((const unsigned*)((const char*)(gbase) + (voff)[_i]), (LAS unsigned*)(lds + (bufoff) + ldsw + _i * 8192), 16, 0, 0); } while (0)
; #define G8_STAGE_A(bufoff, gbase, h_, nx_) do { if constexpr (Sched::GATHER) { unsigned vo_[2]; _Pragma("unroll") for (int q_ = 0; q_ < 2; ++q_) vo_[q_] = (nx_) ? gnxt[h_][q_] : goff[h_][q_]; G8_STAGE(bufoff, gbase, vo_); } \
;         else { G8_STAGE(bufoff, (gbase) + ((h_) ? hstepA : (size_t)0), voffA); } } while (0)
; #define G8_WAIT_V(n) asm volatile("s_waitcnt vmcnt(" #n ")" ::: "memory")
; #define G8_BAR __builtin_amdgcn_s_barrier()
; template <int lda, int ldb, class Epi, class Sched>
; __device__ __forceinline__ void gemm_phase(LAS unsigned char* lds, int wid, int lane, const char* baseA, const char* baseB, const Sched& S, const Epi& E) {
;     ...
;     G8_STAGE(G8_SB(0, 0), cB, voffB); if constexpr (!Epi::HALFN) { G8_STAGE(G8_SB(0, 1), cB + hstepB, voffB); } G8_STAGE_A(G8_SA(0, 0), cA, 0, false); G8_STAGE_A(G8_SA(0, 1), cA, 1, false);
;     if (wr == 1) G8_BAR;
;     G8_WAIT_V(2); G8_BAR;
;     G8_STAGE(G8_SB(1, 0), cB + kstep, voffB); G8_STAGE_A(G8_SA(1, 0), cA + kstep, 0, false); if constexpr (!Epi::HALFN) { G8_STAGE(G8_SB(1, 1), cB + hstepB + kstep, voffB); }
;     if constexpr (Epi::HALFN) { G8_WAIT_V(4); } else { G8_WAIT_V(6); } G8_BAR;
.LBB0_1078:
	s_waitcnt lgkmcnt(0)
	s_add_u32 s14, s14, s48
	s_addc_u32 s15, s15, s49
	v_mbcnt_lo_u32_b32 v149, -1, 0
	v_mbcnt_hi_u32_b32 v149, -1, v149
	s_lshl_b32 s16, s3, 8
	s_or_b32 s16, s16, s95
	v_and_b32_e32 v150, 31, v149
	v_lshrrev_b32_e32 v149, 5, v149
	v_lshl_or_b32 v149, v149, 7, v150
	v_add_lshl_u32 v154, v149, s16, 2
	v_mov_b32_e32 v155, 0
	s_lshr_b32 s16, s27, 1
	s_add_i32 s16, s16, 0x23000
	v_lshl_add_u64 v[154:155], s[14:15], 0, v[154:155]
	s_mov_b32 m0, s16
	s_nop 0
	global_load_lds_dword v[154:155], off
	v_add_co_u32_e32 v154, vcc, 0x400, v154
	s_add_i32 m0, s16, 0x100
	s_nop 0
	v_addc_co_u32_e32 v155, vcc, 0, v155, vcc
	global_load_lds_dword v[154:155], off
	s_add_i32 s67, s27, 0x18000
	v_lshl_add_u64 v[0:1], v[0:1], 0, s[22:23]
	s_mov_b32 m0, s67
	s_add_i32 s68, s27, 0x1a000
	s_waitcnt vmcnt(4)
	s_barrier
	global_load_lds_dwordx4 v[0:1], off
	v_lshl_add_u64 v[0:1], v[2:3], 0, s[22:23]
	s_mov_b32 m0, s68
	s_add_i32 s69, s27, 0x8000
	s_add_i32 s70, s27, 0xa000
	global_load_lds_dwordx4 v[0:1], off
	v_lshl_add_u64 v[0:1], v[6:7], 0, s[22:23]
	s_mov_b32 m0, s69
	s_add_u32 s16, s52, 0x20080
	global_load_lds_dwordx4 v[0:1], off
	v_lshl_add_u64 v[0:1], v[4:5], 0, s[22:23]
	s_mov_b32 m0, s70
	s_addc_u32 s17, s53, 0
	s_add_i32 s71, s27, 0x1c000
	global_load_lds_dwordx4 v[0:1], off
	v_lshl_add_u64 v[0:1], s[16:17], 0, v[160:161]
	s_mov_b32 m0, s71
	s_add_i32 s72, s27, 0x1e000
	global_load_lds_dwordx4 v[0:1], off
	v_lshl_add_u64 v[0:1], s[16:17], 0, v[156:157]
	s_mov_b32 m0, s72
	s_or_b32 s73, s3, 1
	global_load_lds_dwordx4 v[0:1], off
	s_waitcnt vmcnt(8)
	v_mov_b32_e32 v19, v18
	v_mov_b32_e32 v20, v18
	v_mov_b32_e32 v21, v18
	s_lshl_b32 s74, s73, 18
	s_mov_b64 s[16:17], -1
	s_mov_b32 s20, s59
	v_mov_b32_e32 v16, v18
	s_barrier
	s_branch .LBB0_1081

; #define G8_XLDA(b, h) do { if constexpr (Epi::FP8) { G8_LD8(A8, G8_SA(b, h) + aoff, 4); } else { G8_LDA(At, b, h); } } while (0)
; template <int lda, int ldb, class Epi, class Sched>
; __device__ __forceinline__ void gemm_phase(LAS unsigned char* lds, int wid, int lane, const char* baseA, const char* baseB, const Sched& S, const Epi& E) {
;     ...
;         const bool has_next = S.next(ui + 1, nxt);
;         const char* nA = Sched::GATHER ? baseA : (has_next ? baseA + nxt.ao : cA); const char* nB = has_next ? baseB + nxt.bo : cB;
;         if constexpr (Sched::GATHER) { if (has_next) { G8_GOFF(gnxt, nxt); } else { _Pragma("unroll") for (int h_ = 0; h_ < 2; ++h_) _Pragma("unroll") for (int i_ = 0; i_ < 2; ++i_) gnxt[h_][i_] = goff[h_][i_]; } }
;         int nt = cur.nt; asm volatile("" : "+s"(nt));
; #pragma unroll 1
;         for (int t = 0; t < nt; t += 2) {
;             const bool last = (t == nt - 2);
;             const char* a1 = cA + (size_t)(t + 1) * kstep;
;             const char* a2 = last ? nA : cA + (size_t)(t + 2) * kstep; const char* b2 = last ? nB : cB + (size_t)(t + 2) * kstep;
;             const char* a3 = a2 + kstep; const char* b3 = b2 + kstep;
;     ...
;             G8_XLDB0(0, 0); if constexpr (!Epi::HALFN) { G8_XLDB1(0, 1); } G8_SCHED; G8_XLDA(0, 0); G8_STAGE_A(G8_SA(1, 1), a1, 1, false);
;             G8_WAIT_VK; G8_WAIT_L(0); G8_BAR; G8_MM0(0, 0); if constexpr (!Epi::HALFN) { G8_MM1(0, 1); } G8_BAR; G8_SCHED;
;             G8_XLDA(0, 1); G8_STAGE(G8_SB(0, 0), b2, voffB); if constexpr (!Epi::HALFN) { G8_STAGE(G8_SB(0, 1), b2 + hstepB, voffB); } G8_STAGE_A(G8_SA(0, 0), a2, 0, last);
;             G8_WAIT_VK; G8_WAIT_L(0); G8_BAR; G8_MM0(1, 0); if constexpr (!Epi::HALFN) { G8_MM1(1, 1); } G8_BAR; G8_SCHED;
;             G8_XLDB0(1, 0); if constexpr (!Epi::HALFN) { G8_XLDB1(1, 1); } G8_SCHED; G8_XLDA(1, 0); G8_STAGE_A(G8_SA(0, 1), a2, 1, last);
;             G8_WAIT_VK; G8_WAIT_L(0); G8_BAR; G8_MM0(0, 0); if constexpr (!Epi::HALFN) { G8_MM1(0, 1); } G8_BAR; G8_SCHED;
;             G8_XLDA(1, 1); G8_STAGE(G8_SB(1, 0), b3, voffB); if constexpr (!Epi::HALFN) { G8_STAGE(G8_SB(1, 1), b3 + hstepB, voffB); } G8_STAGE_A(G8_SA(1, 0), a3, 0, last);
;             G8_WAIT_VK; G8_WAIT_L(0); G8_BAR; G8_MM0(1, 0); if constexpr (!Epi::HALFN) { G8_MM1(1, 1); } G8_BAR; G8_SCHED;
;         }
;         if (wr == 0) G8_BAR;
;         { const int ln_ = lane_id();
.LBB0_1083:
	s_add_u32 s34, s2, s34
	s_addc_u32 s35, s13, s35
	s_add_u32 s50, s31, s77
	s_addc_u32 s51, s58, 0
	s_mov_b32 s4, 8
	s_cmp_lt_i32 s4, 1
	s_cbranch_scc1 .LBB0_1091
	s_and_b64 s[28:29], exec, s[16:17]
	s_cselect_b32 s21, s35, s55
	s_cselect_b32 s28, s34, s54
	s_cselect_b32 s29, s51, s53
	s_cselect_b32 s79, s50, s52
	s_add_i32 s80, s4, -2
	s_add_u32 s81, s52, 0x100
	s_addc_u32 s82, s53, 0
	s_add_u32 s52, s54, 0x20080
	v_mov_b64_e32 v[24:25], v[20:21]
	v_mov_b64_e32 v[28:29], v[20:21]
	v_mov_b64_e32 v[34:35], v[20:21]
	v_mov_b64_e32 v[38:39], v[20:21]
	v_mov_b64_e32 v[42:43], v[20:21]
	v_mov_b64_e32 v[46:47], v[20:21]
	v_mov_b64_e32 v[50:51], v[20:21]
	v_mov_b64_e32 v[86:87], v[20:21]
	v_mov_b64_e32 v[90:91], v[20:21]
	v_mov_b64_e32 v[94:95], v[20:21]
	v_mov_b64_e32 v[98:99], v[20:21]
	v_mov_b64_e32 v[102:103], v[20:21]
	v_mov_b64_e32 v[106:107], v[20:21]
	v_mov_b64_e32 v[110:111], v[20:21]
	v_mov_b64_e32 v[114:115], v[20:21]
	v_mov_b64_e32 v[54:55], v[20:21]
	v_mov_b64_e32 v[58:59], v[20:21]
	v_mov_b64_e32 v[62:63], v[20:21]
	v_mov_b64_e32 v[66:67], v[20:21]
	v_mov_b64_e32 v[70:71], v[20:21]
	v_mov_b64_e32 v[74:75], v[20:21]
	v_mov_b64_e32 v[78:79], v[20:21]
	v_mov_b64_e32 v[82:83], v[20:21]
	v_mov_b64_e32 v[118:119], v[20:21]
	v_mov_b64_e32 v[122:123], v[20:21]
	v_mov_b64_e32 v[126:127], v[20:21]
	v_mov_b64_e32 v[130:131], v[20:21]
	v_mov_b64_e32 v[134:135], v[20:21]
	v_mov_b64_e32 v[138:139], v[20:21]
	v_mov_b64_e32 v[142:143], v[20:21]
	v_mov_b64_e32 v[146:147], v[20:21]
	s_addc_u32 s53, s55, 0
	s_mov_b32 s54, 0
	v_mov_b64_e32 v[22:23], v[18:19]
	v_mov_b64_e32 v[26:27], v[18:19]
	v_mov_b64_e32 v[32:33], v[18:19]
	v_mov_b64_e32 v[36:37], v[18:19]
	v_mov_b64_e32 v[40:41], v[18:19]
	v_mov_b64_e32 v[44:45], v[18:19]
	v_mov_b64_e32 v[48:49], v[18:19]
	v_mov_b64_e32 v[84:85], v[18:19]
	v_mov_b64_e32 v[88:89], v[18:19]
	v_mov_b64_e32 v[92:93], v[18:19]
	v_mov_b64_e32 v[96:97], v[18:19]
	v_mov_b64_e32 v[100:101], v[18:19]
	v_mov_b64_e32 v[104:105], v[18:19]
	v_mov_b64_e32 v[108:109], v[18:19]
	v_mov_b64_e32 v[112:113], v[18:19]
	v_mov_b64_e32 v[52:53], v[18:19]
	v_mov_b64_e32 v[56:57], v[18:19]
	v_mov_b64_e32 v[60:61], v[18:19]
	v_mov_b64_e32 v[64:65], v[18:19]
	v_mov_b64_e32 v[68:69], v[18:19]
	v_mov_b64_e32 v[72:73], v[18:19]
	v_mov_b64_e32 v[76:77], v[18:19]
	v_mov_b64_e32 v[80:81], v[18:19]
	v_mov_b64_e32 v[116:117], v[18:19]
	v_mov_b64_e32 v[120:121], v[18:19]
	v_mov_b64_e32 v[124:125], v[18:19]
	v_mov_b64_e32 v[128:129], v[18:19]
	v_mov_b64_e32 v[132:133], v[18:19]
	v_mov_b64_e32 v[136:137], v[18:19]
	v_mov_b64_e32 v[140:141], v[18:19]
	v_mov_b64_e32 v[144:145], v[18:19]

;     static __device__ __forceinline__ unsigned q8(float z) { return (unsigned)(fast_sigmoid(z) * 255.f + 0.5f); }
;     __device__ __forceinline__ void operator()(const f32x4 (&acc)[2][2][4][2], const g8::Unit& u, int wr, int wc, int fr, int fq) const {
;         const int row0 = u.pm * 256 + wr * 64 + fr, col0 = u.pn * 256 + wc * 32 + 8 * fq;
; #pragma unroll
;         for (int bj = 0; bj < 2; ++bj) {
;             const f32x4 bv0 = *(const f32x4*)(bgate + col0 + bj * 128), bv1 = *(const f32x4*)(bgate + col0 + bj * 128 + 4);
; #pragma unroll
;             for (int ai = 0; ai < 2; ++ai)
; #pragma unroll
;                 for (int m = 0; m < 4; ++m) { const int row = row0 + ai * 128 + m * 16; unsigned char* rp = GT + (size_t)row * 4096 + col0 + bj * 128;
;                     const f32x4 v0 = acc[ai][bj][m][0] * 0.03125f + bv0, v1 = acc[ai][bj][m][1] * 0.03125f + bv1;
;                     u32x2 w; w.x = q8(v0[0]) | (q8(v0[1]) << 8) | (q8(v0[2]) << 16) | (q8(v0[3]) << 24); w.y = q8(v1[0]) | (q8(v1[1]) << 8) | (q8(v1[2]) << 16) | (q8(v1[3]) << 24);
;                     *(u32x2*)rp = w; } }
;     }
.LBB0_1088:
	s_mov_b32 s4, -1
	s_and_b32 s52, s3, 1
	s_lshr_b32 s53, s27, 1
	s_lshl_b32 s52, s52, 8
	s_add_i32 s53, s53, 0x23000
	s_add_i32 s52, s52, s53
	s_lshl_b32 s3, s3, 8
	v_mbcnt_lo_u32_b32 v0, s4, 0
	v_mbcnt_hi_u32_b32 v0, s4, v0
	s_lshl_b32 s4, s20, 8
	s_add_i32 s4, s4, s9
	v_lshrrev_b32_e32 v168, 2, v0
	v_and_b32_e32 v170, 3, v0
	v_and_b32_e32 v17, 60, v0
	v_or_b32_e32 v168, s4, v168
	v_lshrrev_b32_e32 v0, 1, v0
	s_or_b32 s3, s3, s95
	v_lshl_or_b32 v17, v170, 6, v17
	v_and_b32_e32 v0, 56, v0
	v_lshl_add_u32 v170, v170, 3, s3
	v_lshl_add_u32 v12, v0, 2, s52
	ds_read_b128 v[4:7], v12
	ds_read_b128 v[0:3], v12 offset:16
	ds_read_b128 v[184:187], v12 offset:128
	ds_read_b128 v[188:191], v12 offset:144
	v_ashrrev_i32_e32 v171, 31, v170
	v_ashrrev_i32_e32 v169, 31, v168
	v_lshlrev_b64 v[8:9], 12, v[168:169]
	s_mov_b64 s[52:53], 0x10000
	s_mov_b64 vcc, 0x80000
	v_lshl_add_u64 v[8:9], s[46:47], 0, v[8:9]
	s_mov_b32 s20, 0xbd38aa3b
	s_mov_b32 s21, 0x3b808081
	v_lshl_add_u64 v[8:9], v[8:9], 0, v[170:171]
	v_lshl_add_u64 v[10:11], v[8:9], 0, s[52:53]
	v_lshl_add_u64 v[192:193], v[8:9], 0, vcc
	v_lshl_add_u64 v[14:15], v[10:11], 0, s[52:53]
	v_lshl_add_u64 v[194:195], v[192:193], 0, s[52:53]
	v_lshl_add_u64 v[168:169], v[14:15], 0, s[52:53]
	v_lshl_add_u64 v[196:197], v[194:195], 0, s[52:53]
	v_lshl_add_u64 v[198:199], v[196:197], 0, s[52:53]
	s_waitcnt lgkmcnt(0)
	v_mul_f32_e32 v0, 0xbfb8aa3b, v0
	v_mul_f32_e32 v1, 0xbfb8aa3b, v1
	v_mul_f32_e32 v2, 0xbfb8aa3b, v2
	v_mul_f32_e32 v3, 0xbfb8aa3b, v3
	v_mul_f32_e32 v4, 0xbfb8aa3b, v4
	v_mul_f32_e32 v5, 0xbfb8aa3b, v5
	v_mul_f32_e32 v6, 0xbfb8aa3b, v6
	v_mul_f32_e32 v7, 0xbfb8aa3b, v7
	v_mul_f32_e32 v184, 0xbfb8aa3b, v184
	v_mul_f32_e32 v185, 0xbfb8aa3b, v185
	v_mul_f32_e32 v186, 0xbfb8aa3b, v186
	v_mul_f32_e32 v187, 0xbfb8aa3b, v187
	v_mul_f32_e32 v188, 0xbfb8aa3b, v188
	v_mul_f32_e32 v189, 0xbfb8aa3b, v189
	v_mul_f32_e32 v190, 0xbfb8aa3b, v190
	v_mul_f32_e32 v191, 0xbfb8aa3b, v191
	v_pk_fma_f32 v[144:145], v[144:145], s[20:21], v[4:5] op_sel_hi:[1,0,1]
	v_pk_fma_f32 v[146:147], v[146:147], s[20:21], v[6:7] op_sel_hi:[1,0,1]
	v_pk_fma_f32 v[140:141], v[140:141], s[20:21], v[0:1] op_sel_hi:[1,0,1]
	v_pk_fma_f32 v[142:143], v[142:143], s[20:21], v[2:3] op_sel_hi:[1,0,1]
	v_pk_fma_f32 v[136:137], v[136:137], s[20:21], v[4:5] op_sel_hi:[1,0,1]
	v_pk_fma_f32 v[138:139], v[138:139], s[20:21], v[6:7] op_sel_hi:[1,0,1]
	v_pk_fma_f32 v[132:133], v[132:133], s[20:21], v[0:1] op_sel_hi:[1,0,1]
	v_pk_fma_f32 v[134:135], v[134:135], s[20:21], v[2:3] op_sel_hi:[1,0,1]
	v_exp_f32_e32 v144, v144
	v_exp_f32_e32 v145, v145
	v_exp_f32_e32 v146, v146
	v_exp_f32_e32 v147, v147
	v_exp_f32_e32 v140, v140
	v_exp_f32_e32 v141, v141
	v_exp_f32_e32 v142, v142
	v_exp_f32_e32 v143, v143
	v_exp_f32_e32 v136, v136
	v_exp_f32_e32 v137, v137
	v_exp_f32_e32 v138, v138
	v_exp_f32_e32 v139, v139
	v_exp_f32_e32 v132, v132
	v_exp_f32_e32 v133, v133
	v_exp_f32_e32 v134, v134
	v_exp_f32_e32 v135, v135
	v_fma_f32 v144, v144, s21, s21
	v_fma_f32 v145, v145, s21, s21
	v_fma_f32 v146, v146, s21, s21
	v_fma_f32 v147, v147, s21, s21
	v_fma_f32 v140, v140, s21, s21
	v_fma_f32 v141, v141, s21, s21
	v_fma_f32 v142, v142, s21, s21
	v_fma_f32 v143, v143, s21, s21
	v_fma_f32 v136, v136, s21, s21
	v_fma_f32 v137, v137, s21, s21
	v_fma_f32 v138, v138, s21, s21
	v_fma_f32 v139, v139, s21, s21
	v_fma_f32 v132, v132, s21, s21
	v_fma_f32 v133, v133, s21, s21
	v_fma_f32 v134, v134, s21, s21
	v_fma_f32 v135, v135, s21, s21
	v_rcp_f32_e32 v144, v144
	v_rcp_f32_e32 v145, v145
	v_rcp_f32_e32 v146, v146
	v_rcp_f32_e32 v147, v147
	v_rcp_f32_e32 v140, v140
	v_rcp_f32_e32 v141, v141
	v_rcp_f32_e32 v142, v142
	v_rcp_f32_e32 v143, v143
	v_rcp_f32_e32 v136, v136
	v_rcp_f32_e32 v137, v137
	v_rcp_f32_e32 v138, v138
	v_rcp_f32_e32 v139, v139
	v_rcp_f32_e32 v132, v132
	v_rcp_f32_e32 v133, v133
	v_rcp_f32_e32 v134, v134
	v_rcp_f32_e32 v135, v135
	v_cvt_rpi_i32_f32_e32 v144, v144
	v_cvt_rpi_i32_f32_e32 v136, v136
	v_cvt_rpi_i32_f32_sdwa v144, v145 dst_sel:BYTE_1 dst_unused:UNUSED_PRESERVE src0_sel:DWORD
	v_cvt_rpi_i32_f32_sdwa v136, v137 dst_sel:BYTE_1 dst_unused:UNUSED_PRESERVE src0_sel:DWORD
	v_cvt_rpi_i32_f32_e32 v145, v140
	v_cvt_rpi_i32_f32_e32 v137, v132
	v_cvt_rpi_i32_f32_sdwa v144, v146 dst_sel:BYTE_2 dst_unused:UNUSED_PRESERVE src0_sel:DWORD
	v_cvt_rpi_i32_f32_sdwa v136, v138 dst_sel:BYTE_2 dst_unused:UNUSED_PRESERVE src0_sel:DWORD
	v_cvt_rpi_i32_f32_sdwa v145, v141 dst_sel:BYTE_1 dst_unused:UNUSED_PRESERVE src0_sel:DWORD
	v_cvt_rpi_i32_f32_sdwa v137, v133 dst_sel:BYTE_1 dst_unused:UNUSED_PRESERVE src0_sel:DWORD
	v_cvt_rpi_i32_f32_sdwa v144, v147 dst_sel:BYTE_3 dst_unused:UNUSED_PRESERVE src0_sel:DWORD
	v_cvt_rpi_i32_f32_sdwa v136, v139 dst_sel:BYTE_3 dst_unused:UNUSED_PRESERVE src0_sel:DWORD
	v_cvt_rpi_i32_f32_sdwa v145, v142 dst_sel:BYTE_2 dst_unused:UNUSED_PRESERVE src0_sel:DWORD
	v_cvt_rpi_i32_f32_sdwa v137, v134 dst_sel:BYTE_2 dst_unused:UNUSED_PRESERVE src0_sel:DWORD
	v_cvt_rpi_i32_f32_sdwa v145, v143 dst_sel:BYTE_3 dst_unused:UNUSED_PRESERVE src0_sel:DWORD
	v_cvt_rpi_i32_f32_sdwa v137, v135 dst_sel:BYTE_3 dst_unused:UNUSED_PRESERVE src0_sel:DWORD
	ds_bpermute_b32 v144, v17, v144
	ds_bpermute_b32 v145, v17, v145
	ds_bpermute_b32 v136, v17, v136
	ds_bpermute_b32 v137, v17, v137
	v_pk_fma_f32 v[128:129], v[128:129], s[20:21], v[4:5] op_sel_hi:[1,0,1]
	v_pk_fma_f32 v[130:131], v[130:131], s[20:21], v[6:7] op_sel_hi:[1,0,1]
	v_pk_fma_f32 v[124:125], v[124:125], s[20:21], v[0:1] op_sel_hi:[1,0,1]
	v_pk_fma_f32 v[126:127], v[126:127], s[20:21], v[2:3] op_sel_hi:[1,0,1]
	v_pk_fma_f32 v[120:121], v[120:121], s[20:21], v[4:5] op_sel_hi:[1,0,1]
;     static __device__ __forceinline__ unsigned q8(float z) { return (unsigned)(fast_sigmoid(z) * 255.f + 0.5f); }
;     __device__ __forceinline__ void operator()(const f32x4 (&acc)[2][2][4][2], const g8::Unit& u, int wr, int wc, int fr, int fq) const {
;         const int row0 = u.pm * 256 + wr * 64 + fr, col0 = u.pn * 256 + wc * 32 + 8 * fq;
; #pragma unroll
;         for (int bj = 0; bj < 2; ++bj) {
;             const f32x4 bv0 = *(const f32x4*)(bgate + col0 + bj * 128), bv1 = *(const f32x4*)(bgate + col0 + bj * 128 + 4);
; #pragma unroll
;             for (int ai = 0; ai < 2; ++ai)
; #pragma unroll
;                 for (int m = 0; m < 4; ++m) { const int row = row0 + ai * 128 + m * 16; unsigned char* rp = GT + (size_t)row * 4096 + col0 + bj * 128;
;                     const f32x4 v0 = acc[ai][bj][m][0] * 0.03125f + bv0, v1 = acc[ai][bj][m][1] * 0.03125f + bv1;
;                     u32x2 w; w.x = q8(v0[0]) | (q8(v0[1]) << 8) | (q8(v0[2]) << 16) | (q8(v0[3]) << 24); w.y = q8(v1[0]) | (q8(v1[1]) << 8) | (q8(v1[2]) << 16) | (q8(v1[3]) << 24);
;                     *(u32x2*)rp = w; } }
;     }
	v_pk_fma_f32 v[122:123], v[122:123], s[20:21], v[6:7] op_sel_hi:[1,0,1]
	v_pk_fma_f32 v[116:117], v[116:117], s[20:21], v[0:1] op_sel_hi:[1,0,1]
	v_pk_fma_f32 v[118:119], v[118:119], s[20:21], v[2:3] op_sel_hi:[1,0,1]
	v_exp_f32_e32 v128, v128
	v_exp_f32_e32 v129, v129
	v_exp_f32_e32 v130, v130
	v_exp_f32_e32 v131, v131
	v_exp_f32_e32 v124, v124
	v_exp_f32_e32 v125, v125
	v_exp_f32_e32 v126, v126
	v_exp_f32_e32 v127, v127
	v_exp_f32_e32 v120, v120
	v_exp_f32_e32 v121, v121
	v_exp_f32_e32 v122, v122
	v_exp_f32_e32 v123, v123
	v_exp_f32_e32 v116, v116
	v_exp_f32_e32 v117, v117
	v_exp_f32_e32 v118, v118
	v_exp_f32_e32 v119, v119
	v_fma_f32 v128, v128, s21, s21
	v_fma_f32 v129, v129, s21, s21
	v_fma_f32 v130, v130, s21, s21
	v_fma_f32 v131, v131, s21, s21
	v_fma_f32 v124, v124, s21, s21
	v_fma_f32 v125, v125, s21, s21
	v_fma_f32 v126, v126, s21, s21
	v_fma_f32 v127, v127, s21, s21
	v_fma_f32 v120, v120, s21, s21
	v_fma_f32 v121, v121, s21, s21
	v_fma_f32 v122, v122, s21, s21
	v_fma_f32 v123, v123, s21, s21
	v_fma_f32 v116, v116, s21, s21
	v_fma_f32 v117, v117, s21, s21
	v_fma_f32 v118, v118, s21, s21
	v_fma_f32 v119, v119, s21, s21
	v_rcp_f32_e32 v128, v128
	v_rcp_f32_e32 v129, v129
	v_rcp_f32_e32 v130, v130
	v_rcp_f32_e32 v131, v131
	v_rcp_f32_e32 v124, v124
	v_rcp_f32_e32 v125, v125
	v_rcp_f32_e32 v126, v126
	v_rcp_f32_e32 v127, v127
	v_rcp_f32_e32 v120, v120
	v_rcp_f32_e32 v121, v121
	v_rcp_f32_e32 v122, v122
	v_rcp_f32_e32 v123, v123
	v_rcp_f32_e32 v116, v116
	v_rcp_f32_e32 v117, v117
	v_rcp_f32_e32 v118, v118
	v_rcp_f32_e32 v119, v119
	v_cvt_rpi_i32_f32_e32 v128, v128
	v_cvt_rpi_i32_f32_e32 v120, v120
	v_cvt_rpi_i32_f32_sdwa v128, v129 dst_sel:BYTE_1 dst_unused:UNUSED_PRESERVE src0_sel:DWORD
	v_cvt_rpi_i32_f32_sdwa v120, v121 dst_sel:BYTE_1 dst_unused:UNUSED_PRESERVE src0_sel:DWORD
	v_cvt_rpi_i32_f32_e32 v129, v124
	v_cvt_rpi_i32_f32_e32 v121, v116
	v_cvt_rpi_i32_f32_sdwa v128, v130 dst_sel:BYTE_2 dst_unused:UNUSED_PRESERVE src0_sel:DWORD
	v_cvt_rpi_i32_f32_sdwa v120, v122 dst_sel:BYTE_2 dst_unused:UNUSED_PRESERVE src0_sel:DWORD
	v_cvt_rpi_i32_f32_sdwa v129, v125 dst_sel:BYTE_1 dst_unused:UNUSED_PRESERVE src0_sel:DWORD
	v_cvt_rpi_i32_f32_sdwa v121, v117 dst_sel:BYTE_1 dst_unused:UNUSED_PRESERVE src0_sel:DWORD
	v_cvt_rpi_i32_f32_sdwa v128, v131 dst_sel:BYTE_3 dst_unused:UNUSED_PRESERVE src0_sel:DWORD
	v_cvt_rpi_i32_f32_sdwa v120, v123 dst_sel:BYTE_3 dst_unused:UNUSED_PRESERVE src0_sel:DWORD
	v_cvt_rpi_i32_f32_sdwa v129, v126 dst_sel:BYTE_2 dst_unused:UNUSED_PRESERVE src0_sel:DWORD
	v_cvt_rpi_i32_f32_sdwa v121, v118 dst_sel:BYTE_2 dst_unused:UNUSED_PRESERVE src0_sel:DWORD
	v_cvt_rpi_i32_f32_sdwa v129, v127 dst_sel:BYTE_3 dst_unused:UNUSED_PRESERVE src0_sel:DWORD
	v_cvt_rpi_i32_f32_sdwa v121, v119 dst_sel:BYTE_3 dst_unused:UNUSED_PRESERVE src0_sel:DWORD
	ds_bpermute_b32 v128, v17, v128
	ds_bpermute_b32 v129, v17, v129
	ds_bpermute_b32 v120, v17, v120
	ds_bpermute_b32 v121, v17, v121
	s_waitcnt lgkmcnt(4)
	global_store_dwordx2 v[8:9], v[144:145], off
	global_store_dwordx2 v[10:11], v[136:137], off
	v_pk_fma_f32 v[112:113], v[112:113], s[20:21], v[4:5] op_sel_hi:[1,0,1]
	v_pk_fma_f32 v[114:115], v[114:115], s[20:21], v[6:7] op_sel_hi:[1,0,1]
	v_pk_fma_f32 v[108:109], v[108:109], s[20:21], v[0:1] op_sel_hi:[1,0,1]
	v_pk_fma_f32 v[110:111], v[110:111], s[20:21], v[2:3] op_sel_hi:[1,0,1]
	v_pk_fma_f32 v[104:105], v[104:105], s[20:21], v[4:5] op_sel_hi:[1,0,1]
	v_pk_fma_f32 v[106:107], v[106:107], s[20:21], v[6:7] op_sel_hi:[1,0,1]
	v_pk_fma_f32 v[100:101], v[100:101], s[20:21], v[0:1] op_sel_hi:[1,0,1]
	v_pk_fma_f32 v[102:103], v[102:103], s[20:21], v[2:3] op_sel_hi:[1,0,1]
	v_exp_f32_e32 v112, v112
	v_exp_f32_e32 v113, v113
	v_exp_f32_e32 v114, v114
	v_exp_f32_e32 v115, v115
	v_exp_f32_e32 v108, v108
	v_exp_f32_e32 v109, v109
	v_exp_f32_e32 v110, v110
	v_exp_f32_e32 v111, v111
	v_exp_f32_e32 v104, v104
	v_exp_f32_e32 v105, v105
	v_exp_f32_e32 v106, v106
	v_exp_f32_e32 v107, v107
	v_exp_f32_e32 v100, v100
	v_exp_f32_e32 v101, v101
	v_exp_f32_e32 v102, v102
	v_exp_f32_e32 v103, v103
	v_fma_f32 v112, v112, s21, s21
	v_fma_f32 v113, v113, s21, s21
	v_fma_f32 v114, v114, s21, s21
	v_fma_f32 v115, v115, s21, s21
	v_fma_f32 v108, v108, s21, s21
	v_fma_f32 v109, v109, s21, s21
	v_fma_f32 v110, v110, s21, s21
	v_fma_f32 v111, v111, s21, s21
	v_fma_f32 v104, v104, s21, s21
	v_fma_f32 v105, v105, s21, s21
	v_fma_f32 v106, v106, s21, s21
	v_fma_f32 v107, v107, s21, s21
	v_fma_f32 v100, v100, s21, s21
	v_fma_f32 v101, v101, s21, s21
	v_fma_f32 v102, v102, s21, s21
	v_fma_f32 v103, v103, s21, s21
	v_rcp_f32_e32 v112, v112
	v_rcp_f32_e32 v113, v113
	v_rcp_f32_e32 v114, v114
	v_rcp_f32_e32 v115, v115
	v_rcp_f32_e32 v108, v108
	v_rcp_f32_e32 v109, v109
	v_rcp_f32_e32 v110, v110
	v_rcp_f32_e32 v111, v111
	v_rcp_f32_e32 v104, v104
	v_rcp_f32_e32 v105, v105
	v_rcp_f32_e32 v106, v106
	v_rcp_f32_e32 v107, v107
	v_rcp_f32_e32 v100, v100
	v_rcp_f32_e32 v101, v101
	v_rcp_f32_e32 v102, v102
	v_rcp_f32_e32 v103, v103
	v_cvt_rpi_i32_f32_e32 v112, v112
	v_cvt_rpi_i32_f32_e32 v104, v104
	v_cvt_rpi_i32_f32_sdwa v112, v113 dst_sel:BYTE_1 dst_unused:UNUSED_PRESERVE src0_sel:DWORD
	v_cvt_rpi_i32_f32_sdwa v104, v105 dst_sel:BYTE_1 dst_unused:UNUSED_PRESERVE src0_sel:DWORD
	v_cvt_rpi_i32_f32_e32 v113, v108
	v_cvt_rpi_i32_f32_e32 v105, v100
	v_cvt_rpi_i32_f32_sdwa v112, v114 dst_sel:BYTE_2 dst_unused:UNUSED_PRESERVE src0_sel:DWORD
	v_cvt_rpi_i32_f32_sdwa v104, v106 dst_sel:BYTE_2 dst_unused:UNUSED_PRESERVE src0_sel:DWORD
	v_cvt_rpi_i32_f32_sdwa v113, v109 dst_sel:BYTE_1 dst_unused:UNUSED_PRESERVE src0_sel:DWORD
	v_cvt_rpi_i32_f32_sdwa v105, v101 dst_sel:BYTE_1 dst_unused:UNUSED_PRESERVE src0_sel:DWORD
	v_cvt_rpi_i32_f32_sdwa v112, v115 dst_sel:BYTE_3 dst_unused:UNUSED_PRESERVE src0_sel:DWORD
	v_cvt_rpi_i32_f32_sdwa v104, v107 dst_sel:BYTE_3 dst_unused:UNUSED_PRESERVE src0_sel:DWORD
	v_cvt_rpi_i32_f32_sdwa v113, v110 dst_sel:BYTE_2 dst_unused:UNUSED_PRESERVE src0_sel:DWORD
	v_cvt_rpi_i32_f32_sdwa v105, v102 dst_sel:BYTE_2 dst_unused:UNUSED_PRESERVE src0_sel:DWORD
	v_cvt_rpi_i32_f32_sdwa v113, v111 dst_sel:BYTE_3 dst_unused:UNUSED_PRESERVE src0_sel:DWORD
	v_cvt_rpi_i32_f32_sdwa v105, v103 dst_sel:BYTE_3 dst_unused:UNUSED_PRESERVE src0_sel:DWORD
	ds_bpermute_b32 v112, v17, v112
	ds_bpermute_b32 v113, v17, v113
	ds_bpermute_b32 v104, v17, v104
	ds_bpermute_b32 v105, v17, v105
	s_waitcnt lgkmcnt(4)
;     static __device__ __forceinline__ unsigned q8(float z) { return (unsigned)(fast_sigmoid(z) * 255.f + 0.5f); }
;     __device__ __forceinline__ void operator()(const f32x4 (&acc)[2][2][4][2], const g8::Unit& u, int wr, int wc, int fr, int fq) const {
;         const int row0 = u.pm * 256 + wr * 64 + fr, col0 = u.pn * 256 + wc * 32 + 8 * fq;
; #pragma unroll
;         for (int bj = 0; bj < 2; ++bj) {
;             const f32x4 bv0 = *(const f32x4*)(bgate + col0 + bj * 128), bv1 = *(const f32x4*)(bgate + col0 + bj * 128 + 4);
; #pragma unroll
;             for (int ai = 0; ai < 2; ++ai)
; #pragma unroll
;                 for (int m = 0; m < 4; ++m) { const int row = row0 + ai * 128 + m * 16; unsigned char* rp = GT + (size_t)row * 4096 + col0 + bj * 128;
;                     const f32x4 v0 = acc[ai][bj][m][0] * 0.03125f + bv0, v1 = acc[ai][bj][m][1] * 0.03125f + bv1;
;                     u32x2 w; w.x = q8(v0[0]) | (q8(v0[1]) << 8) | (q8(v0[2]) << 16) | (q8(v0[3]) << 24); w.y = q8(v1[0]) | (q8(v1[1]) << 8) | (q8(v1[2]) << 16) | (q8(v1[3]) << 24);
;                     *(u32x2*)rp = w; } }
;     }
	global_store_dwordx2 v[14:15], v[128:129], off
	global_store_dwordx2 v[168:169], v[120:121], off
	v_pk_fma_f32 v[96:97], v[96:97], s[20:21], v[4:5] op_sel_hi:[1,0,1]
	v_pk_fma_f32 v[98:99], v[98:99], s[20:21], v[6:7] op_sel_hi:[1,0,1]
	v_pk_fma_f32 v[92:93], v[92:93], s[20:21], v[0:1] op_sel_hi:[1,0,1]
	v_pk_fma_f32 v[94:95], v[94:95], s[20:21], v[2:3] op_sel_hi:[1,0,1]
	v_pk_fma_f32 v[88:89], v[88:89], s[20:21], v[4:5] op_sel_hi:[1,0,1]
	v_pk_fma_f32 v[90:91], v[90:91], s[20:21], v[6:7] op_sel_hi:[1,0,1]
	v_pk_fma_f32 v[84:85], v[84:85], s[20:21], v[0:1] op_sel_hi:[1,0,1]
	v_pk_fma_f32 v[86:87], v[86:87], s[20:21], v[2:3] op_sel_hi:[1,0,1]
	v_exp_f32_e32 v96, v96
	v_exp_f32_e32 v97, v97
	v_exp_f32_e32 v98, v98
	v_exp_f32_e32 v99, v99
	v_exp_f32_e32 v92, v92
	v_exp_f32_e32 v93, v93
	v_exp_f32_e32 v94, v94
	v_exp_f32_e32 v95, v95
	v_exp_f32_e32 v88, v88
	v_exp_f32_e32 v89, v89
	v_exp_f32_e32 v90, v90
	v_exp_f32_e32 v91, v91
	v_exp_f32_e32 v84, v84
	v_exp_f32_e32 v85, v85
	v_exp_f32_e32 v86, v86
	v_exp_f32_e32 v87, v87
	v_fma_f32 v96, v96, s21, s21
	v_fma_f32 v97, v97, s21, s21
	v_fma_f32 v98, v98, s21, s21
	v_fma_f32 v99, v99, s21, s21
	v_fma_f32 v92, v92, s21, s21
	v_fma_f32 v93, v93, s21, s21
	v_fma_f32 v94, v94, s21, s21
	v_fma_f32 v95, v95, s21, s21
	v_fma_f32 v88, v88, s21, s21
	v_fma_f32 v89, v89, s21, s21
	v_fma_f32 v90, v90, s21, s21
	v_fma_f32 v91, v91, s21, s21
	v_fma_f32 v84, v84, s21, s21
	v_fma_f32 v85, v85, s21, s21
	v_fma_f32 v86, v86, s21, s21
	v_fma_f32 v87, v87, s21, s21
	v_rcp_f32_e32 v96, v96
	v_rcp_f32_e32 v97, v97
	v_rcp_f32_e32 v98, v98
	v_rcp_f32_e32 v99, v99
	v_rcp_f32_e32 v92, v92
	v_rcp_f32_e32 v93, v93
	v_rcp_f32_e32 v94, v94
	v_rcp_f32_e32 v95, v95
	v_rcp_f32_e32 v88, v88
	v_rcp_f32_e32 v89, v89
	v_rcp_f32_e32 v90, v90
	v_rcp_f32_e32 v91, v91
	v_rcp_f32_e32 v84, v84
	v_rcp_f32_e32 v85, v85
	v_rcp_f32_e32 v86, v86
	v_rcp_f32_e32 v87, v87
	v_cvt_rpi_i32_f32_e32 v96, v96
	v_cvt_rpi_i32_f32_e32 v88, v88
	v_cvt_rpi_i32_f32_sdwa v96, v97 dst_sel:BYTE_1 dst_unused:UNUSED_PRESERVE src0_sel:DWORD
	v_cvt_rpi_i32_f32_sdwa v88, v89 dst_sel:BYTE_1 dst_unused:UNUSED_PRESERVE src0_sel:DWORD
	v_cvt_rpi_i32_f32_e32 v97, v92
	v_cvt_rpi_i32_f32_e32 v89, v84
	v_cvt_rpi_i32_f32_sdwa v96, v98 dst_sel:BYTE_2 dst_unused:UNUSED_PRESERVE src0_sel:DWORD
	v_cvt_rpi_i32_f32_sdwa v88, v90 dst_sel:BYTE_2 dst_unused:UNUSED_PRESERVE src0_sel:DWORD
	v_cvt_rpi_i32_f32_sdwa v97, v93 dst_sel:BYTE_1 dst_unused:UNUSED_PRESERVE src0_sel:DWORD
	v_cvt_rpi_i32_f32_sdwa v89, v85 dst_sel:BYTE_1 dst_unused:UNUSED_PRESERVE src0_sel:DWORD
	v_cvt_rpi_i32_f32_sdwa v96, v99 dst_sel:BYTE_3 dst_unused:UNUSED_PRESERVE src0_sel:DWORD
	v_cvt_rpi_i32_f32_sdwa v88, v91 dst_sel:BYTE_3 dst_unused:UNUSED_PRESERVE src0_sel:DWORD
	v_cvt_rpi_i32_f32_sdwa v97, v94 dst_sel:BYTE_2 dst_unused:UNUSED_PRESERVE src0_sel:DWORD
	v_cvt_rpi_i32_f32_sdwa v89, v86 dst_sel:BYTE_2 dst_unused:UNUSED_PRESERVE src0_sel:DWORD
	v_cvt_rpi_i32_f32_sdwa v97, v95 dst_sel:BYTE_3 dst_unused:UNUSED_PRESERVE src0_sel:DWORD
	v_cvt_rpi_i32_f32_sdwa v89, v87 dst_sel:BYTE_3 dst_unused:UNUSED_PRESERVE src0_sel:DWORD
	ds_bpermute_b32 v96, v17, v96
	ds_bpermute_b32 v97, v17, v97
	ds_bpermute_b32 v88, v17, v88
	ds_bpermute_b32 v89, v17, v89
	s_waitcnt lgkmcnt(4)
	global_store_dwordx2 v[192:193], v[112:113], off
	global_store_dwordx2 v[194:195], v[104:105], off
	v_pk_fma_f32 v[80:81], v[80:81], s[20:21], v[184:185] op_sel_hi:[1,0,1]
	v_pk_fma_f32 v[82:83], v[82:83], s[20:21], v[186:187] op_sel_hi:[1,0,1]
	v_pk_fma_f32 v[76:77], v[76:77], s[20:21], v[188:189] op_sel_hi:[1,0,1]
	v_pk_fma_f32 v[78:79], v[78:79], s[20:21], v[190:191] op_sel_hi:[1,0,1]
	v_pk_fma_f32 v[72:73], v[72:73], s[20:21], v[184:185] op_sel_hi:[1,0,1]
	v_pk_fma_f32 v[74:75], v[74:75], s[20:21], v[186:187] op_sel_hi:[1,0,1]
	v_pk_fma_f32 v[68:69], v[68:69], s[20:21], v[188:189] op_sel_hi:[1,0,1]
	v_pk_fma_f32 v[70:71], v[70:71], s[20:21], v[190:191] op_sel_hi:[1,0,1]
	v_exp_f32_e32 v80, v80
	v_exp_f32_e32 v81, v81
	v_exp_f32_e32 v82, v82
	v_exp_f32_e32 v83, v83
	v_exp_f32_e32 v76, v76
	v_exp_f32_e32 v77, v77
	v_exp_f32_e32 v78, v78
	v_exp_f32_e32 v79, v79
	v_exp_f32_e32 v72, v72
	v_exp_f32_e32 v73, v73
	v_exp_f32_e32 v74, v74
	v_exp_f32_e32 v75, v75
	v_exp_f32_e32 v68, v68
	v_exp_f32_e32 v69, v69
	v_exp_f32_e32 v70, v70
	v_exp_f32_e32 v71, v71
	v_fma_f32 v80, v80, s21, s21
	v_fma_f32 v81, v81, s21, s21
	v_fma_f32 v82, v82, s21, s21
	v_fma_f32 v83, v83, s21, s21
	v_fma_f32 v76, v76, s21, s21
	v_fma_f32 v77, v77, s21, s21
	v_fma_f32 v78, v78, s21, s21
	v_fma_f32 v79, v79, s21, s21
	v_fma_f32 v72, v72, s21, s21
	v_fma_f32 v73, v73, s21, s21
	v_fma_f32 v74, v74, s21, s21
	v_fma_f32 v75, v75, s21, s21
	v_fma_f32 v68, v68, s21, s21
	v_fma_f32 v69, v69, s21, s21
	v_fma_f32 v70, v70, s21, s21
	v_fma_f32 v71, v71, s21, s21
	v_rcp_f32_e32 v80, v80
	v_rcp_f32_e32 v81, v81
	v_rcp_f32_e32 v82, v82
	v_rcp_f32_e32 v83, v83
	v_rcp_f32_e32 v76, v76
	v_rcp_f32_e32 v77, v77
	v_rcp_f32_e32 v78, v78
	v_rcp_f32_e32 v79, v79
	v_rcp_f32_e32 v72, v72
	v_rcp_f32_e32 v73, v73
	v_rcp_f32_e32 v74, v74
	v_rcp_f32_e32 v75, v75
	v_rcp_f32_e32 v68, v68
	v_rcp_f32_e32 v69, v69
	v_rcp_f32_e32 v70, v70
	v_rcp_f32_e32 v71, v71
	v_cvt_rpi_i32_f32_e32 v80, v80
	v_cvt_rpi_i32_f32_e32 v72, v72
	v_cvt_rpi_i32_f32_sdwa v80, v81 dst_sel:BYTE_1 dst_unused:UNUSED_PRESERVE src0_sel:DWORD
	v_cvt_rpi_i32_f32_sdwa v72, v73 dst_sel:BYTE_1 dst_unused:UNUSED_PRESERVE src0_sel:DWORD
	v_cvt_rpi_i32_f32_e32 v81, v76
	v_cvt_rpi_i32_f32_e32 v73, v68
	v_cvt_rpi_i32_f32_sdwa v80, v82 dst_sel:BYTE_2 dst_unused:UNUSED_PRESERVE src0_sel:DWORD
	v_cvt_rpi_i32_f32_sdwa v72, v74 dst_sel:BYTE_2 dst_unused:UNUSED_PRESERVE src0_sel:DWORD
	v_cvt_rpi_i32_f32_sdwa v81, v77 dst_sel:BYTE_1 dst_unused:UNUSED_PRESERVE src0_sel:DWORD
	v_cvt_rpi_i32_f32_sdwa v73, v69 dst_sel:BYTE_1 dst_unused:UNUSED_PRESERVE src0_sel:DWORD
	v_cvt_rpi_i32_f32_sdwa v80, v83 dst_sel:BYTE_3 dst_unused:UNUSED_PRESERVE src0_sel:DWORD
	v_cvt_rpi_i32_f32_sdwa v72, v75 dst_sel:BYTE_3 dst_unused:UNUSED_PRESERVE src0_sel:DWORD
	v_cvt_rpi_i32_f32_sdwa v81, v78 dst_sel:BYTE_2 dst_unused:UNUSED_PRESERVE src0_sel:DWORD
	v_cvt_rpi_i32_f32_sdwa v73, v70 dst_sel:BYTE_2 dst_unused:UNUSED_PRESERVE src0_sel:DWORD
	v_cvt_rpi_i32_f32_sdwa v81, v79 dst_sel:BYTE_3 dst_unused:UNUSED_PRESERVE src0_sel:DWORD
	v_cvt_rpi_i32_f32_sdwa v73, v71 dst_sel:BYTE_3 dst_unused:UNUSED_PRESERVE src0_sel:DWORD
	ds_bpermute_b32 v80, v17, v80
	ds_bpermute_b32 v81, v17, v81
	ds_bpermute_b32 v72, v17, v72
	ds_bpermute_b32 v73, v17, v73
	s_waitcnt lgkmcnt(4)
;     static __device__ __forceinline__ unsigned q8(float z) { return (unsigned)(fast_sigmoid(z) * 255.f + 0.5f); }
;     __device__ __forceinline__ void operator()(const f32x4 (&acc)[2][2][4][2], const g8::Unit& u, int wr, int wc, int fr, int fq) const {
;         const int row0 = u.pm * 256 + wr * 64 + fr, col0 = u.pn * 256 + wc * 32 + 8 * fq;
; #pragma unroll
;         for (int bj = 0; bj < 2; ++bj) {
;             const f32x4 bv0 = *(const f32x4*)(bgate + col0 + bj * 128), bv1 = *(const f32x4*)(bgate + col0 + bj * 128 + 4);
; #pragma unroll
;             for (int ai = 0; ai < 2; ++ai)
; #pragma unroll
;                 for (int m = 0; m < 4; ++m) { const int row = row0 + ai * 128 + m * 16; unsigned char* rp = GT + (size_t)row * 4096 + col0 + bj * 128;
;                     const f32x4 v0 = acc[ai][bj][m][0] * 0.03125f + bv0, v1 = acc[ai][bj][m][1] * 0.03125f + bv1;
;                     u32x2 w; w.x = q8(v0[0]) | (q8(v0[1]) << 8) | (q8(v0[2]) << 16) | (q8(v0[3]) << 24); w.y = q8(v1[0]) | (q8(v1[1]) << 8) | (q8(v1[2]) << 16) | (q8(v1[3]) << 24);
;                     *(u32x2*)rp = w; } }
;     }
	global_store_dwordx2 v[196:197], v[96:97], off
	global_store_dwordx2 v[198:199], v[88:89], off
	v_pk_fma_f32 v[64:65], v[64:65], s[20:21], v[184:185] op_sel_hi:[1,0,1]
	v_pk_fma_f32 v[66:67], v[66:67], s[20:21], v[186:187] op_sel_hi:[1,0,1]
	v_pk_fma_f32 v[60:61], v[60:61], s[20:21], v[188:189] op_sel_hi:[1,0,1]
	v_pk_fma_f32 v[62:63], v[62:63], s[20:21], v[190:191] op_sel_hi:[1,0,1]
	v_pk_fma_f32 v[56:57], v[56:57], s[20:21], v[184:185] op_sel_hi:[1,0,1]
	v_pk_fma_f32 v[58:59], v[58:59], s[20:21], v[186:187] op_sel_hi:[1,0,1]
	v_pk_fma_f32 v[52:53], v[52:53], s[20:21], v[188:189] op_sel_hi:[1,0,1]
	v_pk_fma_f32 v[54:55], v[54:55], s[20:21], v[190:191] op_sel_hi:[1,0,1]
	v_exp_f32_e32 v64, v64
	v_exp_f32_e32 v65, v65
	v_exp_f32_e32 v66, v66
	v_exp_f32_e32 v67, v67
	v_exp_f32_e32 v60, v60
	v_exp_f32_e32 v61, v61
	v_exp_f32_e32 v62, v62
	v_exp_f32_e32 v63, v63
	v_exp_f32_e32 v56, v56
	v_exp_f32_e32 v57, v57
	v_exp_f32_e32 v58, v58
	v_exp_f32_e32 v59, v59
	v_exp_f32_e32 v52, v52
	v_exp_f32_e32 v53, v53
	v_exp_f32_e32 v54, v54
	v_exp_f32_e32 v55, v55
	v_fma_f32 v64, v64, s21, s21
	v_fma_f32 v65, v65, s21, s21
	v_fma_f32 v66, v66, s21, s21
	v_fma_f32 v67, v67, s21, s21
	v_fma_f32 v60, v60, s21, s21
	v_fma_f32 v61, v61, s21, s21
	v_fma_f32 v62, v62, s21, s21
	v_fma_f32 v63, v63, s21, s21
	v_fma_f32 v56, v56, s21, s21
	v_fma_f32 v57, v57, s21, s21
	v_fma_f32 v58, v58, s21, s21
	v_fma_f32 v59, v59, s21, s21
	v_fma_f32 v52, v52, s21, s21
	v_fma_f32 v53, v53, s21, s21
	v_fma_f32 v54, v54, s21, s21
	v_fma_f32 v55, v55, s21, s21
	v_rcp_f32_e32 v64, v64
	v_rcp_f32_e32 v65, v65
	v_rcp_f32_e32 v66, v66
	v_rcp_f32_e32 v67, v67
	v_rcp_f32_e32 v60, v60
	v_rcp_f32_e32 v61, v61
	v_rcp_f32_e32 v62, v62
	v_rcp_f32_e32 v63, v63
	v_rcp_f32_e32 v56, v56
	v_rcp_f32_e32 v57, v57
	v_rcp_f32_e32 v58, v58
	v_rcp_f32_e32 v59, v59
	v_rcp_f32_e32 v52, v52
	v_rcp_f32_e32 v53, v53
	v_rcp_f32_e32 v54, v54
	v_rcp_f32_e32 v55, v55
	v_cvt_rpi_i32_f32_e32 v64, v64
	v_cvt_rpi_i32_f32_e32 v56, v56
	v_cvt_rpi_i32_f32_sdwa v64, v65 dst_sel:BYTE_1 dst_unused:UNUSED_PRESERVE src0_sel:DWORD
	v_cvt_rpi_i32_f32_sdwa v56, v57 dst_sel:BYTE_1 dst_unused:UNUSED_PRESERVE src0_sel:DWORD
	v_cvt_rpi_i32_f32_e32 v65, v60
	v_cvt_rpi_i32_f32_e32 v57, v52
	v_cvt_rpi_i32_f32_sdwa v64, v66 dst_sel:BYTE_2 dst_unused:UNUSED_PRESERVE src0_sel:DWORD
	v_cvt_rpi_i32_f32_sdwa v56, v58 dst_sel:BYTE_2 dst_unused:UNUSED_PRESERVE src0_sel:DWORD
	v_cvt_rpi_i32_f32_sdwa v65, v61 dst_sel:BYTE_1 dst_unused:UNUSED_PRESERVE src0_sel:DWORD
	v_cvt_rpi_i32_f32_sdwa v57, v53 dst_sel:BYTE_1 dst_unused:UNUSED_PRESERVE src0_sel:DWORD
	v_cvt_rpi_i32_f32_sdwa v64, v67 dst_sel:BYTE_3 dst_unused:UNUSED_PRESERVE src0_sel:DWORD
	v_cvt_rpi_i32_f32_sdwa v56, v59 dst_sel:BYTE_3 dst_unused:UNUSED_PRESERVE src0_sel:DWORD
	v_cvt_rpi_i32_f32_sdwa v65, v62 dst_sel:BYTE_2 dst_unused:UNUSED_PRESERVE src0_sel:DWORD
	v_cvt_rpi_i32_f32_sdwa v57, v54 dst_sel:BYTE_2 dst_unused:UNUSED_PRESERVE src0_sel:DWORD
	v_cvt_rpi_i32_f32_sdwa v65, v63 dst_sel:BYTE_3 dst_unused:UNUSED_PRESERVE src0_sel:DWORD
	v_cvt_rpi_i32_f32_sdwa v57, v55 dst_sel:BYTE_3 dst_unused:UNUSED_PRESERVE src0_sel:DWORD
	ds_bpermute_b32 v64, v17, v64
	ds_bpermute_b32 v65, v17, v65
	ds_bpermute_b32 v56, v17, v56
	ds_bpermute_b32 v57, v17, v57
	s_waitcnt lgkmcnt(4)
	global_store_dwordx2 v[8:9], v[80:81], off offset:128
	global_store_dwordx2 v[10:11], v[72:73], off offset:128
	v_pk_fma_f32 v[48:49], v[48:49], s[20:21], v[184:185] op_sel_hi:[1,0,1]
	v_pk_fma_f32 v[50:51], v[50:51], s[20:21], v[186:187] op_sel_hi:[1,0,1]
	v_pk_fma_f32 v[44:45], v[44:45], s[20:21], v[188:189] op_sel_hi:[1,0,1]
	v_pk_fma_f32 v[46:47], v[46:47], s[20:21], v[190:191] op_sel_hi:[1,0,1]
	v_pk_fma_f32 v[40:41], v[40:41], s[20:21], v[184:185] op_sel_hi:[1,0,1]
	v_pk_fma_f32 v[42:43], v[42:43], s[20:21], v[186:187] op_sel_hi:[1,0,1]
	v_pk_fma_f32 v[36:37], v[36:37], s[20:21], v[188:189] op_sel_hi:[1,0,1]
	v_pk_fma_f32 v[38:39], v[38:39], s[20:21], v[190:191] op_sel_hi:[1,0,1]
	v_exp_f32_e32 v48, v48
	v_exp_f32_e32 v49, v49
	v_exp_f32_e32 v50, v50
	v_exp_f32_e32 v51, v51
	v_exp_f32_e32 v44, v44
	v_exp_f32_e32 v45, v45
	v_exp_f32_e32 v46, v46
	v_exp_f32_e32 v47, v47
	v_exp_f32_e32 v40, v40
	v_exp_f32_e32 v41, v41
	v_exp_f32_e32 v42, v42
	v_exp_f32_e32 v43, v43
	v_exp_f32_e32 v36, v36
	v_exp_f32_e32 v37, v37
	v_exp_f32_e32 v38, v38
	v_exp_f32_e32 v39, v39
	v_fma_f32 v48, v48, s21, s21
	v_fma_f32 v49, v49, s21, s21
	v_fma_f32 v50, v50, s21, s21
	v_fma_f32 v51, v51, s21, s21
	v_fma_f32 v44, v44, s21, s21
	v_fma_f32 v45, v45, s21, s21
	v_fma_f32 v46, v46, s21, s21
	v_fma_f32 v47, v47, s21, s21
	v_fma_f32 v40, v40, s21, s21
	v_fma_f32 v41, v41, s21, s21
	v_fma_f32 v42, v42, s21, s21
	v_fma_f32 v43, v43, s21, s21
	v_fma_f32 v36, v36, s21, s21
	v_fma_f32 v37, v37, s21, s21
	v_fma_f32 v38, v38, s21, s21
	v_fma_f32 v39, v39, s21, s21
	v_rcp_f32_e32 v48, v48
	v_rcp_f32_e32 v49, v49
	v_rcp_f32_e32 v50, v50
	v_rcp_f32_e32 v51, v51
	v_rcp_f32_e32 v44, v44
	v_rcp_f32_e32 v45, v45
	v_rcp_f32_e32 v46, v46
	v_rcp_f32_e32 v47, v47
	v_rcp_f32_e32 v40, v40
	v_rcp_f32_e32 v41, v41
	v_rcp_f32_e32 v42, v42
	v_rcp_f32_e32 v43, v43
	v_rcp_f32_e32 v36, v36
	v_rcp_f32_e32 v37, v37
	v_rcp_f32_e32 v38, v38
	v_rcp_f32_e32 v39, v39
	v_cvt_rpi_i32_f32_e32 v48, v48
	v_cvt_rpi_i32_f32_e32 v40, v40
	v_cvt_rpi_i32_f32_sdwa v48, v49 dst_sel:BYTE_1 dst_unused:UNUSED_PRESERVE src0_sel:DWORD
	v_cvt_rpi_i32_f32_sdwa v40, v41 dst_sel:BYTE_1 dst_unused:UNUSED_PRESERVE src0_sel:DWORD
	v_cvt_rpi_i32_f32_e32 v49, v44
	v_cvt_rpi_i32_f32_e32 v41, v36
	v_cvt_rpi_i32_f32_sdwa v48, v50 dst_sel:BYTE_2 dst_unused:UNUSED_PRESERVE src0_sel:DWORD
	v_cvt_rpi_i32_f32_sdwa v40, v42 dst_sel:BYTE_2 dst_unused:UNUSED_PRESERVE src0_sel:DWORD
	v_cvt_rpi_i32_f32_sdwa v49, v45 dst_sel:BYTE_1 dst_unused:UNUSED_PRESERVE src0_sel:DWORD
	v_cvt_rpi_i32_f32_sdwa v41, v37 dst_sel:BYTE_1 dst_unused:UNUSED_PRESERVE src0_sel:DWORD
	v_cvt_rpi_i32_f32_sdwa v48, v51 dst_sel:BYTE_3 dst_unused:UNUSED_PRESERVE src0_sel:DWORD
	v_cvt_rpi_i32_f32_sdwa v40, v43 dst_sel:BYTE_3 dst_unused:UNUSED_PRESERVE src0_sel:DWORD
	v_cvt_rpi_i32_f32_sdwa v49, v46 dst_sel:BYTE_2 dst_unused:UNUSED_PRESERVE src0_sel:DWORD
	v_cvt_rpi_i32_f32_sdwa v41, v38 dst_sel:BYTE_2 dst_unused:UNUSED_PRESERVE src0_sel:DWORD
	v_cvt_rpi_i32_f32_sdwa v49, v47 dst_sel:BYTE_3 dst_unused:UNUSED_PRESERVE src0_sel:DWORD
	v_cvt_rpi_i32_f32_sdwa v41, v39 dst_sel:BYTE_3 dst_unused:UNUSED_PRESERVE src0_sel:DWORD
	ds_bpermute_b32 v48, v17, v48
	ds_bpermute_b32 v49, v17, v49
	ds_bpermute_b32 v40, v17, v40
	ds_bpermute_b32 v41, v17, v41
	s_waitcnt lgkmcnt(4)
;     static __device__ __forceinline__ unsigned q8(float z) { return (unsigned)(fast_sigmoid(z) * 255.f + 0.5f); }
;     __device__ __forceinline__ void operator()(const f32x4 (&acc)[2][2][4][2], const g8::Unit& u, int wr, int wc, int fr, int fq) const {
;         const int row0 = u.pm * 256 + wr * 64 + fr, col0 = u.pn * 256 + wc * 32 + 8 * fq;
; #pragma unroll
;         for (int bj = 0; bj < 2; ++bj) {
;             const f32x4 bv0 = *(const f32x4*)(bgate + col0 + bj * 128), bv1 = *(const f32x4*)(bgate + col0 + bj * 128 + 4);
; #pragma unroll
;             for (int ai = 0; ai < 2; ++ai)
; #pragma unroll
;                 for (int m = 0; m < 4; ++m) { const int row = row0 + ai * 128 + m * 16; unsigned char* rp = GT + (size_t)row * 4096 + col0 + bj * 128;
;                     const f32x4 v0 = acc[ai][bj][m][0] * 0.03125f + bv0, v1 = acc[ai][bj][m][1] * 0.03125f + bv1;
;                     u32x2 w; w.x = q8(v0[0]) | (q8(v0[1]) << 8) | (q8(v0[2]) << 16) | (q8(v0[3]) << 24); w.y = q8(v1[0]) | (q8(v1[1]) << 8) | (q8(v1[2]) << 16) | (q8(v1[3]) << 24);
;                     *(u32x2*)rp = w; } }
;     }
	global_store_dwordx2 v[14:15], v[64:65], off offset:128
	global_store_dwordx2 v[168:169], v[56:57], off offset:128
	v_pk_fma_f32 v[32:33], v[32:33], s[20:21], v[184:185] op_sel_hi:[1,0,1]
	v_pk_fma_f32 v[34:35], v[34:35], s[20:21], v[186:187] op_sel_hi:[1,0,1]
	v_pk_fma_f32 v[26:27], v[26:27], s[20:21], v[188:189] op_sel_hi:[1,0,1]
	v_pk_fma_f32 v[28:29], v[28:29], s[20:21], v[190:191] op_sel_hi:[1,0,1]
	v_pk_fma_f32 v[22:23], v[22:23], s[20:21], v[184:185] op_sel_hi:[1,0,1]
	v_pk_fma_f32 v[24:25], v[24:25], s[20:21], v[186:187] op_sel_hi:[1,0,1]
	v_pk_fma_f32 v[18:19], v[18:19], s[20:21], v[188:189] op_sel_hi:[1,0,1]
	v_pk_fma_f32 v[20:21], v[20:21], s[20:21], v[190:191] op_sel_hi:[1,0,1]
	v_exp_f32_e32 v32, v32
	v_exp_f32_e32 v33, v33
	v_exp_f32_e32 v34, v34
	v_exp_f32_e32 v35, v35
	v_exp_f32_e32 v26, v26
	v_exp_f32_e32 v27, v27
	v_exp_f32_e32 v28, v28
	v_exp_f32_e32 v29, v29
	v_exp_f32_e32 v22, v22
	v_exp_f32_e32 v23, v23
	v_exp_f32_e32 v24, v24
	v_exp_f32_e32 v25, v25
	v_exp_f32_e32 v18, v18
	v_exp_f32_e32 v19, v19
	v_exp_f32_e32 v20, v20
	v_exp_f32_e32 v21, v21
	v_fma_f32 v32, v32, s21, s21
	v_fma_f32 v33, v33, s21, s21
	v_fma_f32 v34, v34, s21, s21
	v_fma_f32 v35, v35, s21, s21
	v_fma_f32 v26, v26, s21, s21
	v_fma_f32 v27, v27, s21, s21
	v_fma_f32 v28, v28, s21, s21
	v_fma_f32 v29, v29, s21, s21
	v_fma_f32 v22, v22, s21, s21
	v_fma_f32 v23, v23, s21, s21
	v_fma_f32 v24, v24, s21, s21
	v_fma_f32 v25, v25, s21, s21
	v_fma_f32 v18, v18, s21, s21
	v_fma_f32 v19, v19, s21, s21
	v_fma_f32 v20, v20, s21, s21
	v_fma_f32 v21, v21, s21, s21
	v_rcp_f32_e32 v32, v32
	v_rcp_f32_e32 v33, v33
	v_rcp_f32_e32 v34, v34
	v_rcp_f32_e32 v35, v35
	v_rcp_f32_e32 v26, v26
	v_rcp_f32_e32 v27, v27
	v_rcp_f32_e32 v28, v28
	v_rcp_f32_e32 v29, v29
	v_rcp_f32_e32 v22, v22
	v_rcp_f32_e32 v23, v23
	v_rcp_f32_e32 v24, v24
	v_rcp_f32_e32 v25, v25
	v_rcp_f32_e32 v18, v18
	v_rcp_f32_e32 v19, v19
	v_rcp_f32_e32 v20, v20
	v_rcp_f32_e32 v21, v21
	v_cvt_rpi_i32_f32_e32 v32, v32
	v_cvt_rpi_i32_f32_e32 v22, v22
	v_cvt_rpi_i32_f32_sdwa v32, v33 dst_sel:BYTE_1 dst_unused:UNUSED_PRESERVE src0_sel:DWORD
	v_cvt_rpi_i32_f32_sdwa v22, v23 dst_sel:BYTE_1 dst_unused:UNUSED_PRESERVE src0_sel:DWORD
	v_cvt_rpi_i32_f32_e32 v33, v26
	v_cvt_rpi_i32_f32_e32 v23, v18
	v_cvt_rpi_i32_f32_sdwa v32, v34 dst_sel:BYTE_2 dst_unused:UNUSED_PRESERVE src0_sel:DWORD
	v_cvt_rpi_i32_f32_sdwa v22, v24 dst_sel:BYTE_2 dst_unused:UNUSED_PRESERVE src0_sel:DWORD
	v_cvt_rpi_i32_f32_sdwa v33, v27 dst_sel:BYTE_1 dst_unused:UNUSED_PRESERVE src0_sel:DWORD
	v_cvt_rpi_i32_f32_sdwa v23, v19 dst_sel:BYTE_1 dst_unused:UNUSED_PRESERVE src0_sel:DWORD
	v_cvt_rpi_i32_f32_sdwa v32, v35 dst_sel:BYTE_3 dst_unused:UNUSED_PRESERVE src0_sel:DWORD
	v_cvt_rpi_i32_f32_sdwa v22, v25 dst_sel:BYTE_3 dst_unused:UNUSED_PRESERVE src0_sel:DWORD
	v_cvt_rpi_i32_f32_sdwa v33, v28 dst_sel:BYTE_2 dst_unused:UNUSED_PRESERVE src0_sel:DWORD
	v_cvt_rpi_i32_f32_sdwa v23, v20 dst_sel:BYTE_2 dst_unused:UNUSED_PRESERVE src0_sel:DWORD
	v_cvt_rpi_i32_f32_sdwa v33, v29 dst_sel:BYTE_3 dst_unused:UNUSED_PRESERVE src0_sel:DWORD
	v_cvt_rpi_i32_f32_sdwa v23, v21 dst_sel:BYTE_3 dst_unused:UNUSED_PRESERVE src0_sel:DWORD
	ds_bpermute_b32 v32, v17, v32
	ds_bpermute_b32 v33, v17, v33
	ds_bpermute_b32 v22, v17, v22
	ds_bpermute_b32 v23, v17, v23
	s_waitcnt lgkmcnt(4)
	global_store_dwordx2 v[192:193], v[48:49], off offset:128
	global_store_dwordx2 v[194:195], v[40:41], off offset:128
	s_waitcnt lgkmcnt(0)
	global_store_dwordx2 v[196:197], v[32:33], off offset:128
	global_store_dwordx2 v[198:199], v[22:23], off offset:128
	s_mov_b64 s[52:53], -1
	s_andn2_b64 vcc, exec, s[16:17]
	s_cbranch_vccnz .LBB0_1080
	s_and_b64 vcc, exec, s[40:41]
	s_cbranch_vccnz .LBB0_1079
	s_barrier
	s_branch .LBB0_1079

;     __device__ bool next(int i, Unit& u) const { int pm, pn; if (!T.tile(i, pm, pn)) return false; u.ao = (unsigned)pm * (unsigned)(BM * LDA * 2); u.bo = (unsigned)pn * (unsigned)(BM * LDB * 2); u.nt = K / BK; u.pm = pm; u.pn = pn; u.tag = 0; return true; }
;     __device__ bool next(int i, Unit& u) const { int pm, pn; if (!T.tile(i, pm, pn)) return false; u.ao = (unsigned)pm * (unsigned)(BM * LDA * 2); u.bo = (unsigned)pn * (unsigned)(128 * LDB * 2); u.nt = K / BK; u.pm = pm; u.pn = pn; u.tag = 0; return true; }
;     __device__ bool tile(int i, int& pm, int& pn) const {
;         const long Lx = (long)i * G + c; if (Lx >= nwg) return false;
;         int wgid = (int)Lx; { const int q = nwg / NXCD, r = nwg % NXCD, xcd = wgid % NXCD, off = wgid / NXCD; wgid = (xcd < r ? xcd * (q + 1) : r * (q + 1) + (xcd - r) * q) + off; }
;         const int nig = WGM * nN, gid = wgid / nig, fm = gid * WGM, gsz = (nM - fm) < WGM ? (nM - fm) : WGM;
;         pm = fm + ((wgid % nig) % gsz); pn = (wgid % nig) / gsz; return true;
;     }
;     __device__ bool next(int i, g8::Unit& u) const { int pm, pn; if (!T.tile(i >> 3, pm, pn)) return false; const int br = i & 3, hN = (i >> 2) & 1;
;         const int coff = (br == 0) ? 0 : (br == 1) ? 256 : (br == 2) ? 512 : 1024;
;         u.ao = (unsigned)pm * (unsigned)(256 * OP * 2) + coff * 2; u.bo = (unsigned)(pn * 256 + hN * 128) * (unsigned)(OP * 2) + coff * 2; u.nt = (br == 2) ? 8 : 4; u.pm = pm; u.pn = pn; u.tag = br | (hN << 2); return true; }
.LBB0_1177:
	s_add_i32 s53, s53, 1
	s_lshr_b32 s16, s53, 3
	s_mul_hi_i32 s17, s16, s1
	s_mul_i32 s16, s16, s1
	s_add_u32 s16, s16, s92
	s_addc_u32 s17, s17, s93
	v_mov_b64_e32 v[6:7], 0x100
	v_cmp_lt_i64_e64 s[40:41], s[16:17], v[6:7]
	v_mov_b64_e32 v[6:7], 0xff
	v_cmp_gt_i64_e32 vcc, s[16:17], v[6:7]
	s_cbranch_vccnz .LBB0_1188
	s_and_b32 s34, s53, 7
	s_cmp_lt_u32 s34, 2
	s_cbranch_scc1 .Lmg_full
	s_and_b32 s34, s53, 3
	s_lshl_b32 s35, 0x100, s34
	s_cmp_eq_u32 s34, 0
	s_cselect_b32 s35, 0, s35
	s_branch .Lmg_tail
.Lmg_full:
	s_ashr_i32 s17, s16, 31
	s_lshr_b32 s17, s17, 29
	s_add_i32 s34, s16, s17
	s_and_b32 s17, s34, -8
	s_sub_i32 s35, s16, s17
	s_cmp_gt_i32 s35, -1
	s_mov_b64 s[16:17], -1
	s_cbranch_scc0 .LBB0_1180
	s_lshl_b32 s46, s35, 5
	s_mov_b64 s[16:17], 0

;     __device__ bool next(int i, Unit& u) const { int pm, pn; if (!T.tile(i, pm, pn)) return false; u.ao = (unsigned)pm * (unsigned)(BM * LDA * 2); u.bo = (unsigned)pn * (unsigned)(BM * LDB * 2); u.nt = K / BK; u.pm = pm; u.pn = pn; u.tag = 0; return true; }
;     __device__ bool next(int i, Unit& u) const { int pm, pn; if (!T.tile(i, pm, pn)) return false; u.ao = (unsigned)pm * (unsigned)(BM * LDA * 2); u.bo = (unsigned)pn * (unsigned)(128 * LDB * 2); u.nt = K / BK; u.pm = pm; u.pn = pn; u.tag = 0; return true; }
;     __device__ bool next(int i, g8::Unit& u) const { int pm, pn; if (!T.tile(i >> 3, pm, pn)) return false; const int br = i & 3, hN = (i >> 2) & 1;
;         const int coff = (br == 0) ? 0 : (br == 1) ? 256 : (br == 2) ? 512 : 1024;
;         u.ao = (unsigned)pm * (unsigned)(256 * OP * 2) + coff * 2; u.bo = (unsigned)(pn * 256 + hN * 128) * (unsigned)(OP * 2) + coff * 2; u.nt = (br == 2) ? 8 : 4; u.pm = pm; u.pn = pn; u.tag = br | (hN << 2); return true; }
.Lmg_tail:
	s_mul_i32 s16, s55, 0xa0000
	s_or_b32 s56, s35, s16
	s_lshl_b32 s16, s53, 5
	s_lshl_b32 s47, s54, 8
	s_and_b32 s16, s16, 0x80
	s_or_b32 s16, s47, s16
	s_mulk_i32 s16, 0xa00
	s_or_b32 s58, s35, s16
	s_cmp_eq_u32 s34, 2
	s_cselect_b32 s59, 8, 4
	s_and_b32 s57, s53, 7

; __device__ __forceinline__ unsigned cvt_pk_bf16(float lo, float hi) { f32x2 v = {lo, hi}; bf16x2_t b = __builtin_convertvector(v, bf16x2_t); return __builtin_bit_cast(unsigned, b); }
;     __device__ __forceinline__ void operator()(const f32x4 (&acc)[2][2][4][2], f32x4 (&tot)[2][4][2], const u32x2 (&pf)[8], const g8::Unit& u, int wr, int wc, int fr, int fq) const {
;         const int br = u.tag & 3, row0 = u.pm * 256 + wr * 64 + fr, col0 = u.pn * 256 + (u.tag >> 2) * 128 + wc * 32 + 8 * fq;
; #pragma unroll
;         for (int ai = 0; ai < 2; ++ai)
; #pragma unroll
;             for (int m = 0; m < 4; ++m) { const int row = row0 + ai * 128 + m * 16;
;                 const u32x2 g = pf[ai * 4 + m];
;                 const f32x4 g0 = {(float)(g.x & 0xffu), (float)((g.x >> 8) & 0xffu), (float)((g.x >> 16) & 0xffu), (float)(g.x >> 24)};
;                 const f32x4 g1 = {(float)(g.y & 0xffu), (float)((g.y >> 8) & 0xffu), (float)((g.y >> 16) & 0xffu), (float)(g.y >> 24)};
;                 const f32x4 t0 = g0 * acc[ai][0][m][0], t1 = g1 * acc[ai][0][m][1];
;                 if (br == 0) { tot[ai][m][0] = t0; tot[ai][m][1] = t1; } else { tot[ai][m][0] += t0; tot[ai][m][1] += t1; }
;                 if (br == 3) { const f32x4 s0 = tot[ai][m][0] * (1.f / 255.f), s1 = tot[ai][m][1] * (1.f / 255.f);
;                     u32x4 w; w.x = cvt_pk_bf16(s0[0], s0[1]); w.y = cvt_pk_bf16(s0[2], s0[3]); w.z = cvt_pk_bf16(s1[0], s1[1]); w.w = cvt_pk_bf16(s1[2], s1[3]);
;                     *(u32x4*)(MG + (size_t)row * 1024 + col0) = w; } }
;     }
.LBB0_1193:
	s_mov_b32 s42, -1
	s_lshl_b32 s43, s61, 5
	s_and_b32 s43, s43, 0xffffff80
	v_mbcnt_lo_u32_b32 v1, s42, 0
	v_mbcnt_hi_u32_b32 v1, s42, v1
	s_lshl_b32 s42, s60, 8
	s_or_b32 s43, s43, s95
	s_and_b32 s44, s61, 3
	v_lshrrev_b32_e32 v149, 1, v1
	s_add_i32 s43, s43, s42
	s_waitcnt vmcnt(8)
	v_cvt_f32_ubyte3_e32 v151, v167
	v_cvt_f32_ubyte2_e32 v150, v167
	v_and_b32_e32 v149, 56, v149
	v_cvt_f32_ubyte1_e32 v153, v166
	v_cvt_f32_ubyte0_e32 v152, v166
	v_pk_fma_f32 v[142:143], v[62:63], v[150:151], v[142:143]
	v_cvt_f32_ubyte3_e32 v173, v166
	v_cvt_f32_ubyte2_e32 v172, v166
	v_cvt_f32_ubyte1_e32 v155, v167
	v_cvt_f32_ubyte0_e32 v154, v167
	v_add_u32_e32 v168, s43, v149
	v_and_or_b32 v1, v1, 15, s9
	s_cmp_eq_u32 s44, 3
	v_pk_fma_f32 v[140:141], v[66:67], v[172:173], v[140:141]
	v_pk_fma_f32 v[138:139], v[64:65], v[152:153], v[138:139]
	v_pk_fma_f32 v[130:131], v[60:61], v[154:155], v[130:131]
	v_lshl_add_u32 v170, s4, 8, v1
	s_cselect_b64 s[46:47], -1, 0
	s_cmp_lg_u32 s44, 3
	v_ashrrev_i32_e32 v169, 31, v168
	s_cbranch_scc1 .LBB0_1195
	s_mov_b32 s4, 0x3b808081
	v_pk_mul_f32 v[62:63], v[140:141], s[4:5] op_sel_hi:[1,0]
	v_pk_mul_f32 v[60:61], v[138:139], s[4:5] op_sel_hi:[1,0]
	v_pk_mul_f32 v[64:65], v[142:143], s[4:5] op_sel_hi:[1,0]
	v_ashrrev_i32_e32 v171, 31, v170
	v_cvt_pk_bf16_f32 v60, v60, v61
	v_cvt_pk_bf16_f32 v61, v62, v63
	v_cvt_pk_bf16_f32 v63, v64, v65
	v_lshlrev_b64 v[64:65], 11, v[170:171]
	v_pk_mul_f32 v[66:67], v[130:131], s[4:5] op_sel_hi:[1,0]
	v_lshl_add_u64 v[64:65], s[14:15], 0, v[64:65]
	v_cvt_pk_bf16_f32 v62, v66, v67
	v_lshl_add_u64 v[64:65], v[168:169], 1, v[64:65]
	v_mov_b64_e32 v[142:143], 0
	v_mov_b64_e32 v[140:141], 0
	v_mov_b64_e32 v[138:139], 0
	v_mov_b64_e32 v[130:131], 0
	global_store_dwordx4 v[64:65], v[60:63], off
.LBB0_1195:
	s_nop 1
	v_cvt_f32_ubyte1_e32 v61, v164
	v_cvt_f32_ubyte0_e32 v60, v164
	v_cvt_f32_ubyte3_e32 v63, v164
	v_cvt_f32_ubyte2_e32 v62, v164
	v_cvt_f32_ubyte1_e32 v65, v165
	v_cvt_f32_ubyte0_e32 v64, v165
	v_cvt_f32_ubyte3_e32 v67, v165
	v_cvt_f32_ubyte2_e32 v66, v165
	v_pk_fma_f32 v[136:137], v[58:59], v[62:63], v[136:137]
	v_pk_fma_f32 v[134:135], v[56:57], v[60:61], v[134:135]
	v_pk_fma_f32 v[126:127], v[54:55], v[66:67], v[126:127]
	v_pk_fma_f32 v[122:123], v[52:53], v[64:65], v[122:123]
	v_cndmask_b32_e64 v1, 0, 1, s[46:47]
	v_cmp_ne_u32_e64 s[44:45], 1, v1
	s_andn2_b64 vcc, exec, s[46:47]
	s_cbranch_vccnz .LBB0_1197
	v_or_b32_e32 v56, 16, v170
	v_ashrrev_i32_e32 v57, 31, v56
	s_mov_b32 s4, 0x3b808081
	v_lshlrev_b64 v[56:57], 11, v[56:57]
	v_pk_mul_f32 v[54:55], v[136:137], s[4:5] op_sel_hi:[1,0]
	v_pk_mul_f32 v[52:53], v[134:135], s[4:5] op_sel_hi:[1,0]
	v_pk_mul_f32 v[58:59], v[126:127], s[4:5] op_sel_hi:[1,0]
	v_pk_mul_f32 v[60:61], v[122:123], s[4:5] op_sel_hi:[1,0]
	v_lshl_add_u64 v[56:57], s[14:15], 0, v[56:57]
	v_cvt_pk_bf16_f32 v52, v52, v53
	v_cvt_pk_bf16_f32 v53, v54, v55
	v_cvt_pk_bf16_f32 v54, v60, v61
	v_cvt_pk_bf16_f32 v55, v58, v59
	v_lshl_add_u64 v[56:57], v[168:169], 1, v[56:57]
	v_mov_b64_e32 v[136:137], 0
	v_mov_b64_e32 v[134:135], 0
	v_mov_b64_e32 v[126:127], 0
	v_mov_b64_e32 v[122:123], 0
	global_store_dwordx4 v[56:57], v[52:55], off
.LBB0_1197:
	s_nop 1
	v_cvt_f32_ubyte1_e32 v53, v162
	v_cvt_f32_ubyte0_e32 v52, v162
	v_cvt_f32_ubyte3_e32 v55, v162
	v_cvt_f32_ubyte2_e32 v54, v162
	v_cvt_f32_ubyte1_e32 v57, v163
	v_cvt_f32_ubyte0_e32 v56, v163
	v_cvt_f32_ubyte3_e32 v59, v163
	v_cvt_f32_ubyte2_e32 v58, v163
	v_pk_fma_f32 v[132:133], v[50:51], v[54:55], v[132:133]
	v_pk_fma_f32 v[128:129], v[48:49], v[52:53], v[128:129]
	v_pk_fma_f32 v[118:119], v[46:47], v[58:59], v[118:119]
	v_pk_fma_f32 v[114:115], v[44:45], v[56:57], v[114:115]
	s_and_b64 vcc, exec, s[44:45]
	s_cbranch_vccnz .LBB0_1199
	v_or_b32_e32 v48, 32, v170
	v_ashrrev_i32_e32 v49, 31, v48
	s_mov_b32 s4, 0x3b808081
	v_lshlrev_b64 v[48:49], 11, v[48:49]
	v_pk_mul_f32 v[46:47], v[132:133], s[4:5] op_sel_hi:[1,0]
	v_pk_mul_f32 v[44:45], v[128:129], s[4:5] op_sel_hi:[1,0]
	v_pk_mul_f32 v[50:51], v[118:119], s[4:5] op_sel_hi:[1,0]
	v_pk_mul_f32 v[52:53], v[114:115], s[4:5] op_sel_hi:[1,0]
	v_lshl_add_u64 v[48:49], s[14:15], 0, v[48:49]
	v_cvt_pk_bf16_f32 v44, v44, v45
	v_cvt_pk_bf16_f32 v45, v46, v47
	v_cvt_pk_bf16_f32 v46, v52, v53
	v_cvt_pk_bf16_f32 v47, v50, v51
	v_lshl_add_u64 v[48:49], v[168:169], 1, v[48:49]
	v_mov_b64_e32 v[132:133], 0
	v_mov_b64_e32 v[128:129], 0
	v_mov_b64_e32 v[118:119], 0
	v_mov_b64_e32 v[114:115], 0
	global_store_dwordx4 v[48:49], v[44:47], off
.LBB0_1199:
	s_nop 1
	v_cvt_f32_ubyte1_e32 v45, v160
	v_cvt_f32_ubyte0_e32 v44, v160
	v_cvt_f32_ubyte3_e32 v47, v160
	v_cvt_f32_ubyte2_e32 v46, v160
	v_cvt_f32_ubyte1_e32 v49, v161
	v_cvt_f32_ubyte0_e32 v48, v161
	v_cvt_f32_ubyte3_e32 v51, v161
	v_cvt_f32_ubyte2_e32 v50, v161
	v_pk_fma_f32 v[124:125], v[42:43], v[46:47], v[124:125]
	v_pk_fma_f32 v[120:121], v[40:41], v[44:45], v[120:121]
	v_pk_fma_f32 v[110:111], v[38:39], v[50:51], v[110:111]
	v_pk_fma_f32 v[106:107], v[36:37], v[48:49], v[106:107]
	s_and_b64 vcc, exec, s[44:45]
	s_cbranch_vccnz .LBB0_1201
	v_or_b32_e32 v40, 48, v170
	v_ashrrev_i32_e32 v41, 31, v40
	s_mov_b32 s4, 0x3b808081
	v_lshlrev_b64 v[40:41], 11, v[40:41]
	v_pk_mul_f32 v[38:39], v[124:125], s[4:5] op_sel_hi:[1,0]
	v_pk_mul_f32 v[36:37], v[120:121], s[4:5] op_sel_hi:[1,0]
	v_pk_mul_f32 v[42:43], v[110:111], s[4:5] op_sel_hi:[1,0]
	v_pk_mul_f32 v[44:45], v[106:107], s[4:5] op_sel_hi:[1,0]
	v_lshl_add_u64 v[40:41], s[14:15], 0, v[40:41]
	v_cvt_pk_bf16_f32 v36, v36, v37
	v_cvt_pk_bf16_f32 v37, v38, v39
	v_cvt_pk_bf16_f32 v38, v44, v45
	v_cvt_pk_bf16_f32 v39, v42, v43
	v_lshl_add_u64 v[40:41], v[168:169], 1, v[40:41]
	v_mov_b64_e32 v[124:125], 0
	v_mov_b64_e32 v[120:121], 0
	v_mov_b64_e32 v[110:111], 0
	v_mov_b64_e32 v[106:107], 0
	global_store_dwordx4 v[40:41], v[36:39], off
; __device__ __forceinline__ unsigned cvt_pk_bf16(float lo, float hi) { f32x2 v = {lo, hi}; bf16x2_t b = __builtin_convertvector(v, bf16x2_t); return __builtin_bit_cast(unsigned, b); }
;     __device__ __forceinline__ void operator()(const f32x4 (&acc)[2][2][4][2], f32x4 (&tot)[2][4][2], const u32x2 (&pf)[8], const g8::Unit& u, int wr, int wc, int fr, int fq) const {
;         const int br = u.tag & 3, row0 = u.pm * 256 + wr * 64 + fr, col0 = u.pn * 256 + (u.tag >> 2) * 128 + wc * 32 + 8 * fq;
; #pragma unroll
;         for (int ai = 0; ai < 2; ++ai)
; #pragma unroll
;             for (int m = 0; m < 4; ++m) { const int row = row0 + ai * 128 + m * 16;
;                 const u32x2 g = pf[ai * 4 + m];
;                 const f32x4 g0 = {(float)(g.x & 0xffu), (float)((g.x >> 8) & 0xffu), (float)((g.x >> 16) & 0xffu), (float)(g.x >> 24)};
;                 const f32x4 g1 = {(float)(g.y & 0xffu), (float)((g.y >> 8) & 0xffu), (float)((g.y >> 16) & 0xffu), (float)(g.y >> 24)};
;                 const f32x4 t0 = g0 * acc[ai][0][m][0], t1 = g1 * acc[ai][0][m][1];
;                 if (br == 0) { tot[ai][m][0] = t0; tot[ai][m][1] = t1; } else { tot[ai][m][0] += t0; tot[ai][m][1] += t1; }
;                 if (br == 3) { const f32x4 s0 = tot[ai][m][0] * (1.f / 255.f), s1 = tot[ai][m][1] * (1.f / 255.f);
;                     u32x4 w; w.x = cvt_pk_bf16(s0[0], s0[1]); w.y = cvt_pk_bf16(s0[2], s0[3]); w.z = cvt_pk_bf16(s1[0], s1[1]); w.w = cvt_pk_bf16(s1[2], s1[3]);
;                     *(u32x4*)(MG + (size_t)row * 1024 + col0) = w; } }
;     }
.LBB0_1201:
	s_nop 1
	v_cvt_f32_ubyte1_e32 v37, v158
	v_cvt_f32_ubyte0_e32 v36, v158
	v_cvt_f32_ubyte3_e32 v39, v158
	v_cvt_f32_ubyte2_e32 v38, v158
	v_cvt_f32_ubyte1_e32 v41, v159
	v_cvt_f32_ubyte0_e32 v40, v159
	v_cvt_f32_ubyte3_e32 v43, v159
	v_cvt_f32_ubyte2_e32 v42, v159
	v_pk_fma_f32 v[116:117], v[34:35], v[38:39], v[116:117]
	v_pk_fma_f32 v[112:113], v[32:33], v[36:37], v[112:113]
	v_pk_fma_f32 v[102:103], v[28:29], v[42:43], v[102:103]
	v_pk_fma_f32 v[98:99], v[26:27], v[40:41], v[98:99]
	s_and_b64 vcc, exec, s[44:45]
	s_cbranch_vccnz .LBB0_1203
	s_mov_b32 s4, 0x3b808081
	v_pk_mul_f32 v[28:29], v[116:117], s[4:5] op_sel_hi:[1,0]
	v_pk_mul_f32 v[26:27], v[112:113], s[4:5] op_sel_hi:[1,0]
	v_pk_mul_f32 v[32:33], v[102:103], s[4:5] op_sel_hi:[1,0]
	v_ashrrev_i32_e32 v171, 31, v170
	v_cvt_pk_bf16_f32 v26, v26, v27
	v_cvt_pk_bf16_f32 v27, v28, v29
	v_cvt_pk_bf16_f32 v29, v32, v33
	v_lshlrev_b64 v[32:33], 11, v[170:171]
	v_lshl_add_u64 v[32:33], s[14:15], 0, v[32:33]
	v_lshl_add_u64 v[32:33], v[168:169], 1, v[32:33]
	v_pk_mul_f32 v[34:35], v[98:99], s[4:5] op_sel_hi:[1,0]
	v_add_co_u32_e32 v32, vcc, 0x40000, v32
	v_cvt_pk_bf16_f32 v28, v34, v35
	s_nop 0
	v_addc_co_u32_e32 v33, vcc, 0, v33, vcc
	v_mov_b64_e32 v[116:117], 0
	v_mov_b64_e32 v[112:113], 0
	v_mov_b64_e32 v[102:103], 0
	v_mov_b64_e32 v[98:99], 0
	global_store_dwordx4 v[32:33], v[26:29], off
.LBB0_1203:
	s_nop 1
	v_cvt_f32_ubyte1_e32 v27, v156
	v_cvt_f32_ubyte0_e32 v26, v156
	v_cvt_f32_ubyte3_e32 v29, v156
	v_cvt_f32_ubyte2_e32 v28, v156
	v_cvt_f32_ubyte1_e32 v33, v157
	v_cvt_f32_ubyte0_e32 v32, v157
	v_cvt_f32_ubyte3_e32 v35, v157
	v_cvt_f32_ubyte2_e32 v34, v157
	v_pk_fma_f32 v[108:109], v[24:25], v[28:29], v[108:109]
	v_pk_fma_f32 v[104:105], v[22:23], v[26:27], v[104:105]
	v_pk_fma_f32 v[94:95], v[20:21], v[34:35], v[94:95]
	v_pk_fma_f32 v[90:91], v[18:19], v[32:33], v[90:91]
	s_and_b64 vcc, exec, s[44:45]
	s_cbranch_vccnz .LBB0_1205
	s_mov_b32 s4, 0x3b808081
	v_pk_mul_f32 v[20:21], v[108:109], s[4:5] op_sel_hi:[1,0]
	v_pk_mul_f32 v[18:19], v[104:105], s[4:5] op_sel_hi:[1,0]
	v_pk_mul_f32 v[22:23], v[94:95], s[4:5] op_sel_hi:[1,0]
	v_ashrrev_i32_e32 v171, 31, v170
	v_cvt_pk_bf16_f32 v18, v18, v19
	v_cvt_pk_bf16_f32 v19, v20, v21
	v_cvt_pk_bf16_f32 v21, v22, v23
	v_lshlrev_b64 v[22:23], 11, v[170:171]
	v_lshl_add_u64 v[22:23], s[14:15], 0, v[22:23]
	v_lshl_add_u64 v[22:23], v[168:169], 1, v[22:23]
	v_pk_mul_f32 v[24:25], v[90:91], s[4:5] op_sel_hi:[1,0]
	v_add_co_u32_e32 v22, vcc, 0x48000, v22
	v_cvt_pk_bf16_f32 v20, v24, v25
	s_nop 0
	v_addc_co_u32_e32 v23, vcc, 0, v23, vcc
	v_mov_b64_e32 v[108:109], 0
	v_mov_b64_e32 v[104:105], 0
	v_mov_b64_e32 v[94:95], 0
	v_mov_b64_e32 v[90:91], 0
	global_store_dwordx4 v[22:23], v[18:21], off
.LBB0_1205:
	s_nop 1
	v_cvt_f32_ubyte1_e32 v19, v146
	v_cvt_f32_ubyte0_e32 v18, v146
	v_cvt_f32_ubyte3_e32 v21, v146
	v_cvt_f32_ubyte2_e32 v20, v146
	v_cvt_f32_ubyte1_e32 v23, v147
	v_cvt_f32_ubyte0_e32 v22, v147
	v_cvt_f32_ubyte3_e32 v25, v147
	v_cvt_f32_ubyte2_e32 v24, v147
	v_pk_fma_f32 v[100:101], v[16:17], v[20:21], v[100:101]
	v_pk_fma_f32 v[96:97], v[14:15], v[18:19], v[96:97]
	v_pk_fma_f32 v[86:87], v[12:13], v[24:25], v[86:87]
	v_pk_fma_f32 v[84:85], v[10:11], v[22:23], v[84:85]
	s_and_b64 vcc, exec, s[44:45]
	s_cbranch_vccnz .LBB0_1207
	s_mov_b32 s4, 0x3b808081
	v_pk_mul_f32 v[12:13], v[100:101], s[4:5] op_sel_hi:[1,0]
	v_pk_mul_f32 v[10:11], v[96:97], s[4:5] op_sel_hi:[1,0]
	v_pk_mul_f32 v[14:15], v[86:87], s[4:5] op_sel_hi:[1,0]
	v_ashrrev_i32_e32 v171, 31, v170
	v_cvt_pk_bf16_f32 v10, v10, v11
	v_cvt_pk_bf16_f32 v11, v12, v13
	v_cvt_pk_bf16_f32 v13, v14, v15
	v_lshlrev_b64 v[14:15], 11, v[170:171]
	v_lshl_add_u64 v[14:15], s[14:15], 0, v[14:15]
	v_lshl_add_u64 v[14:15], v[168:169], 1, v[14:15]
	v_pk_mul_f32 v[16:17], v[84:85], s[4:5] op_sel_hi:[1,0]
	v_add_co_u32_e32 v14, vcc, 0x50000, v14
	v_cvt_pk_bf16_f32 v12, v16, v17
	s_nop 0
	v_addc_co_u32_e32 v15, vcc, 0, v15, vcc
	v_mov_b64_e32 v[100:101], 0
	v_mov_b64_e32 v[96:97], 0
	v_mov_b64_e32 v[86:87], 0
	v_mov_b64_e32 v[84:85], 0
	global_store_dwordx4 v[14:15], v[10:13], off
.LBB0_1207:
	s_nop 1
	v_cvt_f32_ubyte1_e32 v11, v144
	v_cvt_f32_ubyte0_e32 v10, v144
	v_cvt_f32_ubyte3_e32 v13, v144
	v_cvt_f32_ubyte2_e32 v12, v144
	v_cvt_f32_ubyte1_e32 v15, v145
	v_cvt_f32_ubyte0_e32 v14, v145
	v_cvt_f32_ubyte3_e32 v17, v145
	v_cvt_f32_ubyte2_e32 v16, v145
	v_pk_fma_f32 v[92:93], v[8:9], v[12:13], v[92:93]
	v_pk_fma_f32 v[88:89], v[6:7], v[10:11], v[88:89]
	v_pk_fma_f32 v[82:83], v[4:5], v[16:17], v[82:83]
	v_pk_fma_f32 v[80:81], v[2:3], v[14:15], v[80:81]
	s_and_b64 vcc, exec, s[44:45]
	s_cbranch_vccnz .LBB0_1209
	s_mov_b32 s4, 0x3b808081
	v_pk_mul_f32 v[4:5], v[92:93], s[4:5] op_sel_hi:[1,0]
	v_pk_mul_f32 v[2:3], v[88:89], s[4:5] op_sel_hi:[1,0]
	v_pk_mul_f32 v[6:7], v[82:83], s[4:5] op_sel_hi:[1,0]
	v_ashrrev_i32_e32 v171, 31, v170
	v_cvt_pk_bf16_f32 v2, v2, v3
	v_cvt_pk_bf16_f32 v3, v4, v5
	v_cvt_pk_bf16_f32 v5, v6, v7
	v_lshlrev_b64 v[6:7], 11, v[170:171]
	v_lshl_add_u64 v[6:7], s[14:15], 0, v[6:7]
	v_lshl_add_u64 v[6:7], v[168:169], 1, v[6:7]
	v_pk_mul_f32 v[8:9], v[80:81], s[4:5] op_sel_hi:[1,0]
	v_add_co_u32_e32 v6, vcc, 0x58000, v6
	v_cvt_pk_bf16_f32 v4, v8, v9
	s_nop 0
	v_addc_co_u32_e32 v7, vcc, 0, v7, vcc
	v_mov_b64_e32 v[92:93], 0
	v_mov_b64_e32 v[88:89], 0
	v_mov_b64_e32 v[82:83], 0
	v_mov_b64_e32 v[80:81], 0
	global_store_dwordx4 v[6:7], v[2:5], off

; __device__ __forceinline__ unsigned cvt_pk_bf16(float lo, float hi) { f32x2 v = {lo, hi}; bf16x2_t b = __builtin_convertvector(v, bf16x2_t); return __builtin_bit_cast(unsigned, b); }
;     __device__ __forceinline__ void operator()(const f32x4 (&acc)[2][2][4][2], const g8::Unit& u, int wr, int wc, int fr, int fq) const {
;         const int row0 = u.pm * 256 + wr * 64 + fr, col0 = u.pn * 256 + wc * 32 + 8 * fq;
; #pragma unroll
;         for (int ai = 0; ai < 2; ++ai)
; #pragma unroll
;             for (int m = 0; m < 4; ++m) { const size_t ro = (size_t)(row0 + ai * 128 + m * 16) * 1024;
; #pragma unroll
;                 for (int bj = 0; bj < 2; ++bj) { const size_t o = ro + col0 + bj * 128;
;                     const u32x4 xb = *(const u32x4*)(XBp + o);
;                     const f32x4 x0 = {__uint_as_float(xb.x << 16), __uint_as_float(xb.x & 0xffff0000u), __uint_as_float(xb.y << 16), __uint_as_float(xb.y & 0xffff0000u)};
;                     const f32x4 x1 = {__uint_as_float(xb.z << 16), __uint_as_float(xb.z & 0xffff0000u), __uint_as_float(xb.w << 16), __uint_as_float(xb.w & 0xffff0000u)};
;                     const f32x4 y0 = x0 * ALPHA + acc[ai][bj][m][0], y1 = x1 * ALPHA + acc[ai][bj][m][1];
;                     *(u32x4*)(Y + o) = (u32x4){cvt_pk_bf16(y0[0], y0[1]), cvt_pk_bf16(y0[2], y0[3]), cvt_pk_bf16(y1[0], y1[1]), cvt_pk_bf16(y1[2], y1[3])}; } }
;     }
.LBB0_1288:
	s_mov_b32 s42, -1
	s_andn2_b64 vcc, exec, s[40:41]
	v_mbcnt_lo_u32_b32 v1, s42, 0
	v_mbcnt_hi_u32_b32 v1, s42, v1
	s_lshl_b32 s42, s63, 8
	s_add_i32 s42, s42, s9
	v_lshrrev_b32_e32 v156, 2, v1
	v_and_b32_e32 v238, 60, v1
	v_and_b32_e32 v239, 15, v1
	v_lshrrev_b32_e32 v149, 4, v1
	v_or_b32_e32 v156, s42, v156
	s_lshl_b32 s42, s62, 8
	v_and_b32_e32 v1, 3, v1
	s_or_b32 s42, s42, s95
	v_lshl_or_b32 v238, v1, 6, v238
	v_lshlrev_b32_e32 v239, 4, v239
	v_lshl_add_u32 v146, v1, 3, s42
	v_lshl_or_b32 v239, v149, 2, v239
	v_ashrrev_i32_e32 v157, 31, v156
	v_ashrrev_i32_e32 v147, 31, v146
	v_lshlrev_b64 v[144:145], 10, v[156:157]
	v_lshl_add_u64 v[144:145], v[144:145], 0, v[146:147]
	v_lshlrev_b64 v[144:145], 1, v[144:145]
	v_lshl_add_u64 v[154:155], s[10:11], 0, v[144:145]
	v_lshl_add_u64 v[240:241], s[14:15], 0, v[144:145]
	global_load_dwordx4 v[162:165], v[154:155], off
	global_load_dwordx4 v[166:169], v[154:155], off offset:256
	s_mov_b64 s[42:43], 0x8000
	v_lshl_add_u64 v[236:237], v[154:155], 0, s[42:43]
	global_load_dwordx4 v[170:173], v[236:237], off
	global_load_dwordx4 v[174:177], v[236:237], off offset:256
	s_mov_b64 s[42:43], 0x10000
	v_lshl_add_u64 v[236:237], v[154:155], 0, s[42:43]
	global_load_dwordx4 v[178:181], v[236:237], off
	global_load_dwordx4 v[184:187], v[236:237], off offset:256
	s_mov_b64 s[42:43], 0x18000
	v_lshl_add_u64 v[236:237], v[154:155], 0, s[42:43]
	global_load_dwordx4 v[188:191], v[236:237], off
	global_load_dwordx4 v[192:195], v[236:237], off offset:256
	s_mov_b64 s[42:43], 0x40000
	v_lshl_add_u64 v[236:237], v[154:155], 0, s[42:43]
	global_load_dwordx4 v[196:199], v[236:237], off
	global_load_dwordx4 v[206:209], v[236:237], off offset:256
	s_mov_b64 s[42:43], 0x48000
	v_lshl_add_u64 v[236:237], v[154:155], 0, s[42:43]
	global_load_dwordx4 v[210:213], v[236:237], off
	global_load_dwordx4 v[214:217], v[236:237], off offset:256
	s_mov_b64 s[42:43], 0x50000
	v_lshl_add_u64 v[236:237], v[154:155], 0, s[42:43]
	global_load_dwordx4 v[218:221], v[236:237], off
	global_load_dwordx4 v[222:225], v[236:237], off offset:256
	s_mov_b64 s[42:43], 0x58000
	v_lshl_add_u64 v[236:237], v[154:155], 0, s[42:43]
	global_load_dwordx4 v[228:231], v[236:237], off
	global_load_dwordx4 v[232:235], v[236:237], off offset:256
	s_waitcnt vmcnt(15)
	ds_bpermute_b32 v162, v239, v162
	ds_bpermute_b32 v163, v239, v163
	ds_bpermute_b32 v164, v239, v164
	ds_bpermute_b32 v165, v239, v165
	s_waitcnt vmcnt(14)
	ds_bpermute_b32 v166, v239, v166
	ds_bpermute_b32 v167, v239, v167
	ds_bpermute_b32 v168, v239, v168
	ds_bpermute_b32 v169, v239, v169
	s_waitcnt lgkmcnt(4)
	v_lshlrev_b32_e32 v150, 16, v162
	v_and_b32_e32 v151, 0xffff0000, v162
	v_lshlrev_b32_e32 v152, 16, v163
	v_and_b32_e32 v153, 0xffff0000, v163
	v_lshlrev_b32_e32 v158, 16, v164
	v_and_b32_e32 v159, 0xffff0000, v164
	v_lshlrev_b32_e32 v160, 16, v165
	v_and_b32_e32 v161, 0xffff0000, v165
	v_pk_fma_f32 v[128:129], v[150:151], s[24:25], v[128:129] op_sel_hi:[1,0,1]
	v_pk_fma_f32 v[130:131], v[152:153], s[24:25], v[130:131] op_sel_hi:[1,0,1]
	v_pk_fma_f32 v[124:125], v[158:159], s[24:25], v[124:125] op_sel_hi:[1,0,1]
	v_pk_fma_f32 v[126:127], v[160:161], s[24:25], v[126:127] op_sel_hi:[1,0,1]
	v_cvt_pk_bf16_f32 v162, v128, v129
	v_cvt_pk_bf16_f32 v163, v130, v131
	v_cvt_pk_bf16_f32 v164, v124, v125
	v_cvt_pk_bf16_f32 v165, v126, v127
	ds_bpermute_b32 v162, v238, v162
	ds_bpermute_b32 v163, v238, v163
	ds_bpermute_b32 v164, v238, v164
	ds_bpermute_b32 v165, v238, v165
	s_waitcnt vmcnt(13)
	ds_bpermute_b32 v170, v239, v170
	ds_bpermute_b32 v171, v239, v171
	ds_bpermute_b32 v172, v239, v172
	ds_bpermute_b32 v173, v239, v173
	s_waitcnt lgkmcnt(8)
	v_lshlrev_b32_e32 v150, 16, v166
	v_and_b32_e32 v151, 0xffff0000, v166
	v_lshlrev_b32_e32 v152, 16, v167
	v_and_b32_e32 v153, 0xffff0000, v167
	v_lshlrev_b32_e32 v158, 16, v168
	v_and_b32_e32 v159, 0xffff0000, v168
	v_lshlrev_b32_e32 v160, 16, v169
	v_and_b32_e32 v161, 0xffff0000, v169
	v_pk_fma_f32 v[120:121], v[150:151], s[24:25], v[120:121] op_sel_hi:[1,0,1]
	v_pk_fma_f32 v[122:123], v[152:153], s[24:25], v[122:123] op_sel_hi:[1,0,1]
	v_pk_fma_f32 v[116:117], v[158:159], s[24:25], v[116:117] op_sel_hi:[1,0,1]
	v_pk_fma_f32 v[118:119], v[160:161], s[24:25], v[118:119] op_sel_hi:[1,0,1]
	v_cvt_pk_bf16_f32 v166, v120, v121
	v_cvt_pk_bf16_f32 v167, v122, v123
	v_cvt_pk_bf16_f32 v168, v116, v117
	v_cvt_pk_bf16_f32 v169, v118, v119
	ds_bpermute_b32 v166, v238, v166
	ds_bpermute_b32 v167, v238, v167
	ds_bpermute_b32 v168, v238, v168
	ds_bpermute_b32 v169, v238, v169
	s_waitcnt lgkmcnt(8)
	global_store_dwordx4 v[240:241], v[162:165], off
	s_waitcnt vmcnt(13)
	ds_bpermute_b32 v174, v239, v174
	ds_bpermute_b32 v175, v239, v175
	ds_bpermute_b32 v176, v239, v176
	ds_bpermute_b32 v177, v239, v177
	s_waitcnt lgkmcnt(8)
	v_lshlrev_b32_e32 v150, 16, v170
	v_and_b32_e32 v151, 0xffff0000, v170
	v_lshlrev_b32_e32 v152, 16, v171
	v_and_b32_e32 v153, 0xffff0000, v171
	v_lshlrev_b32_e32 v158, 16, v172
	v_and_b32_e32 v159, 0xffff0000, v172
	v_lshlrev_b32_e32 v160, 16, v173
	v_and_b32_e32 v161, 0xffff0000, v173
	v_pk_fma_f32 v[112:113], v[150:151], s[24:25], v[112:113] op_sel_hi:[1,0,1]
	v_pk_fma_f32 v[114:115], v[152:153], s[24:25], v[114:115] op_sel_hi:[1,0,1]
	v_pk_fma_f32 v[108:109], v[158:159], s[24:25], v[108:109] op_sel_hi:[1,0,1]
	v_pk_fma_f32 v[110:111], v[160:161], s[24:25], v[110:111] op_sel_hi:[1,0,1]
	v_cvt_pk_bf16_f32 v170, v112, v113
	v_cvt_pk_bf16_f32 v171, v114, v115
	v_cvt_pk_bf16_f32 v172, v108, v109
	v_cvt_pk_bf16_f32 v173, v110, v111
	s_mov_b64 s[42:43], 0x8000
	v_lshl_add_u64 v[244:245], v[240:241], 0, s[42:43]
	ds_bpermute_b32 v170, v238, v170
	ds_bpermute_b32 v171, v238, v171
	ds_bpermute_b32 v172, v238, v172
	ds_bpermute_b32 v173, v238, v173
	s_waitcnt lgkmcnt(8)
; __device__ __forceinline__ unsigned cvt_pk_bf16(float lo, float hi) { f32x2 v = {lo, hi}; bf16x2_t b = __builtin_convertvector(v, bf16x2_t); return __builtin_bit_cast(unsigned, b); }
;     __device__ __forceinline__ void operator()(const f32x4 (&acc)[2][2][4][2], const g8::Unit& u, int wr, int wc, int fr, int fq) const {
;         const int row0 = u.pm * 256 + wr * 64 + fr, col0 = u.pn * 256 + wc * 32 + 8 * fq;
; #pragma unroll
;         for (int ai = 0; ai < 2; ++ai)
; #pragma unroll
;             for (int m = 0; m < 4; ++m) { const size_t ro = (size_t)(row0 + ai * 128 + m * 16) * 1024;
; #pragma unroll
;                 for (int bj = 0; bj < 2; ++bj) { const size_t o = ro + col0 + bj * 128;
;                     const u32x4 xb = *(const u32x4*)(XBp + o);
;                     const f32x4 x0 = {__uint_as_float(xb.x << 16), __uint_as_float(xb.x & 0xffff0000u), __uint_as_float(xb.y << 16), __uint_as_float(xb.y & 0xffff0000u)};
;                     const f32x4 x1 = {__uint_as_float(xb.z << 16), __uint_as_float(xb.z & 0xffff0000u), __uint_as_float(xb.w << 16), __uint_as_float(xb.w & 0xffff0000u)};
;                     const f32x4 y0 = x0 * ALPHA + acc[ai][bj][m][0], y1 = x1 * ALPHA + acc[ai][bj][m][1];
;                     *(u32x4*)(Y + o) = (u32x4){cvt_pk_bf16(y0[0], y0[1]), cvt_pk_bf16(y0[2], y0[3]), cvt_pk_bf16(y1[0], y1[1]), cvt_pk_bf16(y1[2], y1[3])}; } }
;     }
	global_store_dwordx4 v[240:241], v[166:169], off offset:256
	s_waitcnt vmcnt(13)
	ds_bpermute_b32 v178, v239, v178
	ds_bpermute_b32 v179, v239, v179
	ds_bpermute_b32 v180, v239, v180
	ds_bpermute_b32 v181, v239, v181
	s_waitcnt lgkmcnt(8)
	v_lshlrev_b32_e32 v150, 16, v174
	v_and_b32_e32 v151, 0xffff0000, v174
	v_lshlrev_b32_e32 v152, 16, v175
	v_and_b32_e32 v153, 0xffff0000, v175
	v_lshlrev_b32_e32 v158, 16, v176
	v_and_b32_e32 v159, 0xffff0000, v176
	v_lshlrev_b32_e32 v160, 16, v177
	v_and_b32_e32 v161, 0xffff0000, v177
	v_pk_fma_f32 v[104:105], v[150:151], s[24:25], v[104:105] op_sel_hi:[1,0,1]
	v_pk_fma_f32 v[106:107], v[152:153], s[24:25], v[106:107] op_sel_hi:[1,0,1]
	v_pk_fma_f32 v[100:101], v[158:159], s[24:25], v[100:101] op_sel_hi:[1,0,1]
	v_pk_fma_f32 v[102:103], v[160:161], s[24:25], v[102:103] op_sel_hi:[1,0,1]
	v_cvt_pk_bf16_f32 v174, v104, v105
	v_cvt_pk_bf16_f32 v175, v106, v107
	v_cvt_pk_bf16_f32 v176, v100, v101
	v_cvt_pk_bf16_f32 v177, v102, v103
	ds_bpermute_b32 v174, v238, v174
	ds_bpermute_b32 v175, v238, v175
	ds_bpermute_b32 v176, v238, v176
	ds_bpermute_b32 v177, v238, v177
	s_waitcnt lgkmcnt(8)
	global_store_dwordx4 v[244:245], v[170:173], off
	s_waitcnt vmcnt(13)
	ds_bpermute_b32 v184, v239, v184
	ds_bpermute_b32 v185, v239, v185
	ds_bpermute_b32 v186, v239, v186
	ds_bpermute_b32 v187, v239, v187
	s_waitcnt lgkmcnt(8)
	v_lshlrev_b32_e32 v150, 16, v178
	v_and_b32_e32 v151, 0xffff0000, v178
	v_lshlrev_b32_e32 v152, 16, v179
	v_and_b32_e32 v153, 0xffff0000, v179
	v_lshlrev_b32_e32 v158, 16, v180
	v_and_b32_e32 v159, 0xffff0000, v180
	v_lshlrev_b32_e32 v160, 16, v181
	v_and_b32_e32 v161, 0xffff0000, v181
	v_pk_fma_f32 v[96:97], v[150:151], s[24:25], v[96:97] op_sel_hi:[1,0,1]
	v_pk_fma_f32 v[98:99], v[152:153], s[24:25], v[98:99] op_sel_hi:[1,0,1]
	v_pk_fma_f32 v[92:93], v[158:159], s[24:25], v[92:93] op_sel_hi:[1,0,1]
	v_pk_fma_f32 v[94:95], v[160:161], s[24:25], v[94:95] op_sel_hi:[1,0,1]
	v_cvt_pk_bf16_f32 v178, v96, v97
	v_cvt_pk_bf16_f32 v179, v98, v99
	v_cvt_pk_bf16_f32 v180, v92, v93
	v_cvt_pk_bf16_f32 v181, v94, v95
	s_mov_b64 s[42:43], 0x10000
	v_lshl_add_u64 v[242:243], v[240:241], 0, s[42:43]
	ds_bpermute_b32 v178, v238, v178
	ds_bpermute_b32 v179, v238, v179
	ds_bpermute_b32 v180, v238, v180
	ds_bpermute_b32 v181, v238, v181
	s_waitcnt lgkmcnt(8)
	global_store_dwordx4 v[244:245], v[174:177], off offset:256
	s_waitcnt vmcnt(13)
	ds_bpermute_b32 v188, v239, v188
	ds_bpermute_b32 v189, v239, v189
	ds_bpermute_b32 v190, v239, v190
	ds_bpermute_b32 v191, v239, v191
	s_waitcnt lgkmcnt(8)
	v_lshlrev_b32_e32 v150, 16, v184
	v_and_b32_e32 v151, 0xffff0000, v184
	v_lshlrev_b32_e32 v152, 16, v185
	v_and_b32_e32 v153, 0xffff0000, v185
	v_lshlrev_b32_e32 v158, 16, v186
	v_and_b32_e32 v159, 0xffff0000, v186
	v_lshlrev_b32_e32 v160, 16, v187
	v_and_b32_e32 v161, 0xffff0000, v187
	v_pk_fma_f32 v[88:89], v[150:151], s[24:25], v[88:89] op_sel_hi:[1,0,1]
	v_pk_fma_f32 v[90:91], v[152:153], s[24:25], v[90:91] op_sel_hi:[1,0,1]
	v_pk_fma_f32 v[84:85], v[158:159], s[24:25], v[84:85] op_sel_hi:[1,0,1]
	v_pk_fma_f32 v[86:87], v[160:161], s[24:25], v[86:87] op_sel_hi:[1,0,1]
	v_cvt_pk_bf16_f32 v184, v88, v89
	v_cvt_pk_bf16_f32 v185, v90, v91
	v_cvt_pk_bf16_f32 v186, v84, v85
	v_cvt_pk_bf16_f32 v187, v86, v87
	ds_bpermute_b32 v184, v238, v184
	ds_bpermute_b32 v185, v238, v185
	ds_bpermute_b32 v186, v238, v186
	ds_bpermute_b32 v187, v238, v187
	s_waitcnt lgkmcnt(8)
	global_store_dwordx4 v[242:243], v[178:181], off
	s_waitcnt vmcnt(13)
	ds_bpermute_b32 v192, v239, v192
	ds_bpermute_b32 v193, v239, v193
	ds_bpermute_b32 v194, v239, v194
	ds_bpermute_b32 v195, v239, v195
	s_waitcnt lgkmcnt(8)
	v_lshlrev_b32_e32 v150, 16, v188
	v_and_b32_e32 v151, 0xffff0000, v188
	v_lshlrev_b32_e32 v152, 16, v189
	v_and_b32_e32 v153, 0xffff0000, v189
	v_lshlrev_b32_e32 v158, 16, v190
	v_and_b32_e32 v159, 0xffff0000, v190
	v_lshlrev_b32_e32 v160, 16, v191
	v_and_b32_e32 v161, 0xffff0000, v191
	v_pk_fma_f32 v[80:81], v[150:151], s[24:25], v[80:81] op_sel_hi:[1,0,1]
	v_pk_fma_f32 v[82:83], v[152:153], s[24:25], v[82:83] op_sel_hi:[1,0,1]
	v_pk_fma_f32 v[76:77], v[158:159], s[24:25], v[76:77] op_sel_hi:[1,0,1]
	v_pk_fma_f32 v[78:79], v[160:161], s[24:25], v[78:79] op_sel_hi:[1,0,1]
	v_cvt_pk_bf16_f32 v188, v80, v81
	v_cvt_pk_bf16_f32 v189, v82, v83
	v_cvt_pk_bf16_f32 v190, v76, v77
	v_cvt_pk_bf16_f32 v191, v78, v79
	s_mov_b64 s[42:43], 0x18000
	v_lshl_add_u64 v[244:245], v[240:241], 0, s[42:43]
	ds_bpermute_b32 v188, v238, v188
	ds_bpermute_b32 v189, v238, v189
	ds_bpermute_b32 v190, v238, v190
	ds_bpermute_b32 v191, v238, v191
	s_waitcnt lgkmcnt(8)
	global_store_dwordx4 v[242:243], v[184:187], off offset:256
	s_waitcnt vmcnt(13)
	ds_bpermute_b32 v196, v239, v196
	ds_bpermute_b32 v197, v239, v197
	ds_bpermute_b32 v198, v239, v198
	ds_bpermute_b32 v199, v239, v199
	s_waitcnt lgkmcnt(8)
	v_lshlrev_b32_e32 v150, 16, v192
	v_and_b32_e32 v151, 0xffff0000, v192
	v_lshlrev_b32_e32 v152, 16, v193
	v_and_b32_e32 v153, 0xffff0000, v193
	v_lshlrev_b32_e32 v158, 16, v194
	v_and_b32_e32 v159, 0xffff0000, v194
	v_lshlrev_b32_e32 v160, 16, v195
	v_and_b32_e32 v161, 0xffff0000, v195
	v_pk_fma_f32 v[72:73], v[150:151], s[24:25], v[72:73] op_sel_hi:[1,0,1]
	v_pk_fma_f32 v[74:75], v[152:153], s[24:25], v[74:75] op_sel_hi:[1,0,1]
	v_pk_fma_f32 v[68:69], v[158:159], s[24:25], v[68:69] op_sel_hi:[1,0,1]
	v_pk_fma_f32 v[70:71], v[160:161], s[24:25], v[70:71] op_sel_hi:[1,0,1]
	v_cvt_pk_bf16_f32 v192, v72, v73
	v_cvt_pk_bf16_f32 v193, v74, v75
	v_cvt_pk_bf16_f32 v194, v68, v69
	v_cvt_pk_bf16_f32 v195, v70, v71
	ds_bpermute_b32 v192, v238, v192
	ds_bpermute_b32 v193, v238, v193
	ds_bpermute_b32 v194, v238, v194
	ds_bpermute_b32 v195, v238, v195
	s_waitcnt lgkmcnt(8)
; __device__ __forceinline__ unsigned cvt_pk_bf16(float lo, float hi) { f32x2 v = {lo, hi}; bf16x2_t b = __builtin_convertvector(v, bf16x2_t); return __builtin_bit_cast(unsigned, b); }
;     __device__ __forceinline__ void operator()(const f32x4 (&acc)[2][2][4][2], const g8::Unit& u, int wr, int wc, int fr, int fq) const {
;         const int row0 = u.pm * 256 + wr * 64 + fr, col0 = u.pn * 256 + wc * 32 + 8 * fq;
; #pragma unroll
;         for (int ai = 0; ai < 2; ++ai)
; #pragma unroll
;             for (int m = 0; m < 4; ++m) { const size_t ro = (size_t)(row0 + ai * 128 + m * 16) * 1024;
; #pragma unroll
;                 for (int bj = 0; bj < 2; ++bj) { const size_t o = ro + col0 + bj * 128;
;                     const u32x4 xb = *(const u32x4*)(XBp + o);
;                     const f32x4 x0 = {__uint_as_float(xb.x << 16), __uint_as_float(xb.x & 0xffff0000u), __uint_as_float(xb.y << 16), __uint_as_float(xb.y & 0xffff0000u)};
;                     const f32x4 x1 = {__uint_as_float(xb.z << 16), __uint_as_float(xb.z & 0xffff0000u), __uint_as_float(xb.w << 16), __uint_as_float(xb.w & 0xffff0000u)};
;                     const f32x4 y0 = x0 * ALPHA + acc[ai][bj][m][0], y1 = x1 * ALPHA + acc[ai][bj][m][1];
;                     *(u32x4*)(Y + o) = (u32x4){cvt_pk_bf16(y0[0], y0[1]), cvt_pk_bf16(y0[2], y0[3]), cvt_pk_bf16(y1[0], y1[1]), cvt_pk_bf16(y1[2], y1[3])}; } }
;     }
	global_store_dwordx4 v[244:245], v[188:191], off
	s_waitcnt vmcnt(13)
	ds_bpermute_b32 v206, v239, v206
	ds_bpermute_b32 v207, v239, v207
	ds_bpermute_b32 v208, v239, v208
	ds_bpermute_b32 v209, v239, v209
	s_waitcnt lgkmcnt(8)
	v_lshlrev_b32_e32 v150, 16, v196
	v_and_b32_e32 v151, 0xffff0000, v196
	v_lshlrev_b32_e32 v152, 16, v197
	v_and_b32_e32 v153, 0xffff0000, v197
	v_lshlrev_b32_e32 v158, 16, v198
	v_and_b32_e32 v159, 0xffff0000, v198
	v_lshlrev_b32_e32 v160, 16, v199
	v_and_b32_e32 v161, 0xffff0000, v199
	v_pk_fma_f32 v[64:65], v[150:151], s[24:25], v[64:65] op_sel_hi:[1,0,1]
	v_pk_fma_f32 v[66:67], v[152:153], s[24:25], v[66:67] op_sel_hi:[1,0,1]
	v_pk_fma_f32 v[60:61], v[158:159], s[24:25], v[60:61] op_sel_hi:[1,0,1]
	v_pk_fma_f32 v[62:63], v[160:161], s[24:25], v[62:63] op_sel_hi:[1,0,1]
	v_cvt_pk_bf16_f32 v196, v64, v65
	v_cvt_pk_bf16_f32 v197, v66, v67
	v_cvt_pk_bf16_f32 v198, v60, v61
	v_cvt_pk_bf16_f32 v199, v62, v63
	s_mov_b64 s[42:43], 0x40000
	v_lshl_add_u64 v[242:243], v[240:241], 0, s[42:43]
	ds_bpermute_b32 v196, v238, v196
	ds_bpermute_b32 v197, v238, v197
	ds_bpermute_b32 v198, v238, v198
	ds_bpermute_b32 v199, v238, v199
	s_waitcnt lgkmcnt(8)
	global_store_dwordx4 v[244:245], v[192:195], off offset:256
	s_waitcnt vmcnt(13)
	ds_bpermute_b32 v210, v239, v210
	ds_bpermute_b32 v211, v239, v211
	ds_bpermute_b32 v212, v239, v212
	ds_bpermute_b32 v213, v239, v213
	s_waitcnt lgkmcnt(8)
	v_lshlrev_b32_e32 v150, 16, v206
	v_and_b32_e32 v151, 0xffff0000, v206
	v_lshlrev_b32_e32 v152, 16, v207
	v_and_b32_e32 v153, 0xffff0000, v207
	v_lshlrev_b32_e32 v158, 16, v208
	v_and_b32_e32 v159, 0xffff0000, v208
	v_lshlrev_b32_e32 v160, 16, v209
	v_and_b32_e32 v161, 0xffff0000, v209
	v_pk_fma_f32 v[56:57], v[150:151], s[24:25], v[56:57] op_sel_hi:[1,0,1]
	v_pk_fma_f32 v[58:59], v[152:153], s[24:25], v[58:59] op_sel_hi:[1,0,1]
	v_pk_fma_f32 v[52:53], v[158:159], s[24:25], v[52:53] op_sel_hi:[1,0,1]
	v_pk_fma_f32 v[54:55], v[160:161], s[24:25], v[54:55] op_sel_hi:[1,0,1]
	v_cvt_pk_bf16_f32 v206, v56, v57
	v_cvt_pk_bf16_f32 v207, v58, v59
	v_cvt_pk_bf16_f32 v208, v52, v53
	v_cvt_pk_bf16_f32 v209, v54, v55
	ds_bpermute_b32 v206, v238, v206
	ds_bpermute_b32 v207, v238, v207
	ds_bpermute_b32 v208, v238, v208
	ds_bpermute_b32 v209, v238, v209
	s_waitcnt lgkmcnt(8)
	global_store_dwordx4 v[242:243], v[196:199], off
	s_waitcnt vmcnt(13)
	ds_bpermute_b32 v214, v239, v214
	ds_bpermute_b32 v215, v239, v215
	ds_bpermute_b32 v216, v239, v216
	ds_bpermute_b32 v217, v239, v217
	s_waitcnt lgkmcnt(8)
	v_lshlrev_b32_e32 v150, 16, v210
	v_and_b32_e32 v151, 0xffff0000, v210
	v_lshlrev_b32_e32 v152, 16, v211
	v_and_b32_e32 v153, 0xffff0000, v211
	v_lshlrev_b32_e32 v158, 16, v212
	v_and_b32_e32 v159, 0xffff0000, v212
	v_lshlrev_b32_e32 v160, 16, v213
	v_and_b32_e32 v161, 0xffff0000, v213
	v_pk_fma_f32 v[48:49], v[150:151], s[24:25], v[48:49] op_sel_hi:[1,0,1]
	v_pk_fma_f32 v[50:51], v[152:153], s[24:25], v[50:51] op_sel_hi:[1,0,1]
	v_pk_fma_f32 v[44:45], v[158:159], s[24:25], v[44:45] op_sel_hi:[1,0,1]
	v_pk_fma_f32 v[46:47], v[160:161], s[24:25], v[46:47] op_sel_hi:[1,0,1]
	v_cvt_pk_bf16_f32 v210, v48, v49
	v_cvt_pk_bf16_f32 v211, v50, v51
	v_cvt_pk_bf16_f32 v212, v44, v45
	v_cvt_pk_bf16_f32 v213, v46, v47
	s_mov_b64 s[42:43], 0x48000
	v_lshl_add_u64 v[244:245], v[240:241], 0, s[42:43]
	ds_bpermute_b32 v210, v238, v210
	ds_bpermute_b32 v211, v238, v211
	ds_bpermute_b32 v212, v238, v212
	ds_bpermute_b32 v213, v238, v213
	s_waitcnt lgkmcnt(8)
	global_store_dwordx4 v[242:243], v[206:209], off offset:256
	s_waitcnt vmcnt(13)
	ds_bpermute_b32 v218, v239, v218
	ds_bpermute_b32 v219, v239, v219
	ds_bpermute_b32 v220, v239, v220
	ds_bpermute_b32 v221, v239, v221
	s_waitcnt lgkmcnt(8)
	v_lshlrev_b32_e32 v150, 16, v214
	v_and_b32_e32 v151, 0xffff0000, v214
	v_lshlrev_b32_e32 v152, 16, v215
	v_and_b32_e32 v153, 0xffff0000, v215
	v_lshlrev_b32_e32 v158, 16, v216
	v_and_b32_e32 v159, 0xffff0000, v216
	v_lshlrev_b32_e32 v160, 16, v217
	v_and_b32_e32 v161, 0xffff0000, v217
	v_pk_fma_f32 v[40:41], v[150:151], s[24:25], v[40:41] op_sel_hi:[1,0,1]
	v_pk_fma_f32 v[42:43], v[152:153], s[24:25], v[42:43] op_sel_hi:[1,0,1]
	v_pk_fma_f32 v[36:37], v[158:159], s[24:25], v[36:37] op_sel_hi:[1,0,1]
	v_pk_fma_f32 v[38:39], v[160:161], s[24:25], v[38:39] op_sel_hi:[1,0,1]
	v_cvt_pk_bf16_f32 v214, v40, v41
	v_cvt_pk_bf16_f32 v215, v42, v43
	v_cvt_pk_bf16_f32 v216, v36, v37
	v_cvt_pk_bf16_f32 v217, v38, v39
	ds_bpermute_b32 v214, v238, v214
	ds_bpermute_b32 v215, v238, v215
	ds_bpermute_b32 v216, v238, v216
	ds_bpermute_b32 v217, v238, v217
	s_waitcnt lgkmcnt(8)
	global_store_dwordx4 v[244:245], v[210:213], off
	s_waitcnt vmcnt(13)
; __device__ __forceinline__ unsigned cvt_pk_bf16(float lo, float hi) { f32x2 v = {lo, hi}; bf16x2_t b = __builtin_convertvector(v, bf16x2_t); return __builtin_bit_cast(unsigned, b); }
;     __device__ __forceinline__ void operator()(const f32x4 (&acc)[2][2][4][2], const g8::Unit& u, int wr, int wc, int fr, int fq) const {
;         const int row0 = u.pm * 256 + wr * 64 + fr, col0 = u.pn * 256 + wc * 32 + 8 * fq;
; #pragma unroll
;         for (int ai = 0; ai < 2; ++ai)
; #pragma unroll
;             for (int m = 0; m < 4; ++m) { const size_t ro = (size_t)(row0 + ai * 128 + m * 16) * 1024;
; #pragma unroll
;                 for (int bj = 0; bj < 2; ++bj) { const size_t o = ro + col0 + bj * 128;
;                     const u32x4 xb = *(const u32x4*)(XBp + o);
;                     const f32x4 x0 = {__uint_as_float(xb.x << 16), __uint_as_float(xb.x & 0xffff0000u), __uint_as_float(xb.y << 16), __uint_as_float(xb.y & 0xffff0000u)};
;                     const f32x4 x1 = {__uint_as_float(xb.z << 16), __uint_as_float(xb.z & 0xffff0000u), __uint_as_float(xb.w << 16), __uint_as_float(xb.w & 0xffff0000u)};
;                     const f32x4 y0 = x0 * ALPHA + acc[ai][bj][m][0], y1 = x1 * ALPHA + acc[ai][bj][m][1];
;                     *(u32x4*)(Y + o) = (u32x4){cvt_pk_bf16(y0[0], y0[1]), cvt_pk_bf16(y0[2], y0[3]), cvt_pk_bf16(y1[0], y1[1]), cvt_pk_bf16(y1[2], y1[3])}; } }
;     }
	ds_bpermute_b32 v222, v239, v222
	ds_bpermute_b32 v223, v239, v223
	ds_bpermute_b32 v224, v239, v224
	ds_bpermute_b32 v225, v239, v225
	s_waitcnt lgkmcnt(8)
	v_lshlrev_b32_e32 v150, 16, v218
	v_and_b32_e32 v151, 0xffff0000, v218
	v_lshlrev_b32_e32 v152, 16, v219
	v_and_b32_e32 v153, 0xffff0000, v219
	v_lshlrev_b32_e32 v158, 16, v220
	v_and_b32_e32 v159, 0xffff0000, v220
	v_lshlrev_b32_e32 v160, 16, v221
	v_and_b32_e32 v161, 0xffff0000, v221
	v_pk_fma_f32 v[32:33], v[150:151], s[24:25], v[32:33] op_sel_hi:[1,0,1]
	v_pk_fma_f32 v[34:35], v[152:153], s[24:25], v[34:35] op_sel_hi:[1,0,1]
	v_pk_fma_f32 v[26:27], v[158:159], s[24:25], v[26:27] op_sel_hi:[1,0,1]
	v_pk_fma_f32 v[28:29], v[160:161], s[24:25], v[28:29] op_sel_hi:[1,0,1]
	v_cvt_pk_bf16_f32 v218, v32, v33
	v_cvt_pk_bf16_f32 v219, v34, v35
	v_cvt_pk_bf16_f32 v220, v26, v27
	v_cvt_pk_bf16_f32 v221, v28, v29
	s_mov_b64 s[42:43], 0x50000
	v_lshl_add_u64 v[242:243], v[240:241], 0, s[42:43]
	ds_bpermute_b32 v218, v238, v218
	ds_bpermute_b32 v219, v238, v219
	ds_bpermute_b32 v220, v238, v220
	ds_bpermute_b32 v221, v238, v221
	s_waitcnt lgkmcnt(8)
	global_store_dwordx4 v[244:245], v[214:217], off offset:256
	s_waitcnt vmcnt(13)
	ds_bpermute_b32 v228, v239, v228
	ds_bpermute_b32 v229, v239, v229
	ds_bpermute_b32 v230, v239, v230
	ds_bpermute_b32 v231, v239, v231
	s_waitcnt lgkmcnt(8)
	v_lshlrev_b32_e32 v150, 16, v222
	v_and_b32_e32 v151, 0xffff0000, v222
	v_lshlrev_b32_e32 v152, 16, v223
	v_and_b32_e32 v153, 0xffff0000, v223
	v_lshlrev_b32_e32 v158, 16, v224
	v_and_b32_e32 v159, 0xffff0000, v224
	v_lshlrev_b32_e32 v160, 16, v225
	v_and_b32_e32 v161, 0xffff0000, v225
	v_pk_fma_f32 v[22:23], v[150:151], s[24:25], v[22:23] op_sel_hi:[1,0,1]
	v_pk_fma_f32 v[24:25], v[152:153], s[24:25], v[24:25] op_sel_hi:[1,0,1]
	v_pk_fma_f32 v[18:19], v[158:159], s[24:25], v[18:19] op_sel_hi:[1,0,1]
	v_pk_fma_f32 v[20:21], v[160:161], s[24:25], v[20:21] op_sel_hi:[1,0,1]
	v_cvt_pk_bf16_f32 v222, v22, v23
	v_cvt_pk_bf16_f32 v223, v24, v25
	v_cvt_pk_bf16_f32 v224, v18, v19
	v_cvt_pk_bf16_f32 v225, v20, v21
	ds_bpermute_b32 v222, v238, v222
	ds_bpermute_b32 v223, v238, v223
	ds_bpermute_b32 v224, v238, v224
	ds_bpermute_b32 v225, v238, v225
	s_waitcnt lgkmcnt(8)
	global_store_dwordx4 v[242:243], v[218:221], off
	s_waitcnt vmcnt(13)
	ds_bpermute_b32 v232, v239, v232
	ds_bpermute_b32 v233, v239, v233
	ds_bpermute_b32 v234, v239, v234
	ds_bpermute_b32 v235, v239, v235
	s_waitcnt lgkmcnt(8)
	v_lshlrev_b32_e32 v150, 16, v228
	v_and_b32_e32 v151, 0xffff0000, v228
	v_lshlrev_b32_e32 v152, 16, v229
	v_and_b32_e32 v153, 0xffff0000, v229
	v_lshlrev_b32_e32 v158, 16, v230
	v_and_b32_e32 v159, 0xffff0000, v230
	v_lshlrev_b32_e32 v160, 16, v231
	v_and_b32_e32 v161, 0xffff0000, v231
	v_pk_fma_f32 v[14:15], v[150:151], s[24:25], v[14:15] op_sel_hi:[1,0,1]
	v_pk_fma_f32 v[16:17], v[152:153], s[24:25], v[16:17] op_sel_hi:[1,0,1]
	v_pk_fma_f32 v[10:11], v[158:159], s[24:25], v[10:11] op_sel_hi:[1,0,1]
	v_pk_fma_f32 v[12:13], v[160:161], s[24:25], v[12:13] op_sel_hi:[1,0,1]
	v_cvt_pk_bf16_f32 v228, v14, v15
	v_cvt_pk_bf16_f32 v229, v16, v17
	v_cvt_pk_bf16_f32 v230, v10, v11
	v_cvt_pk_bf16_f32 v231, v12, v13
	s_mov_b64 s[42:43], 0x58000
	v_lshl_add_u64 v[244:245], v[240:241], 0, s[42:43]
	ds_bpermute_b32 v228, v238, v228
	ds_bpermute_b32 v229, v238, v229
	ds_bpermute_b32 v230, v238, v230
	ds_bpermute_b32 v231, v238, v231
	s_waitcnt lgkmcnt(8)
	global_store_dwordx4 v[242:243], v[222:225], off offset:256
	s_waitcnt lgkmcnt(4)
	v_lshlrev_b32_e32 v150, 16, v232
	v_and_b32_e32 v151, 0xffff0000, v232
	v_lshlrev_b32_e32 v152, 16, v233
	v_and_b32_e32 v153, 0xffff0000, v233
	v_lshlrev_b32_e32 v158, 16, v234
	v_and_b32_e32 v159, 0xffff0000, v234
	v_lshlrev_b32_e32 v160, 16, v235
	v_and_b32_e32 v161, 0xffff0000, v235
	v_pk_fma_f32 v[6:7], v[150:151], s[24:25], v[6:7] op_sel_hi:[1,0,1]
	v_pk_fma_f32 v[8:9], v[152:153], s[24:25], v[8:9] op_sel_hi:[1,0,1]
	v_pk_fma_f32 v[2:3], v[158:159], s[24:25], v[2:3] op_sel_hi:[1,0,1]
	v_pk_fma_f32 v[4:5], v[160:161], s[24:25], v[4:5] op_sel_hi:[1,0,1]
	v_cvt_pk_bf16_f32 v232, v6, v7
	v_cvt_pk_bf16_f32 v233, v8, v9
	v_cvt_pk_bf16_f32 v234, v2, v3
	v_cvt_pk_bf16_f32 v235, v4, v5
	ds_bpermute_b32 v232, v238, v232
	ds_bpermute_b32 v233, v238, v233
	ds_bpermute_b32 v234, v238, v234
	ds_bpermute_b32 v235, v238, v235
	s_waitcnt lgkmcnt(4)
	global_store_dwordx4 v[244:245], v[228:231], off
	s_waitcnt lgkmcnt(0)
	global_store_dwordx4 v[244:245], v[232:235], off offset:256
	s_mov_b64 s[42:43], -1
	s_cbranch_vccnz .LBB0_1276
	s_and_b64 vcc, exec, s[38:39]
	s_cbranch_vccnz .LBB0_1275
	s_barrier
	s_branch .LBB0_1275
